# speedup vs baseline: 1.0043x; 1.0043x over previous
_Z9k_rowstatPKDv2_fPS_:
	s_load_dwordx4 s[4:7], s[0:1], 0x0
	v_lshl_or_b32 v24, s2, 8, v0
	v_ashrrev_i32_e32 v25, 31, v24
	v_lshlrev_b32_e32 v26, 3, v24
	s_waitcnt lgkmcnt(0)
	global_load_dwordx2 v[0:1], v26, s[4:5] nt
	s_add_u32 s8, s4, 0x80000
	s_addc_u32 s9, s5, 0
	global_load_dwordx2 v[2:3], v26, s[8:9] nt
	s_add_u32 s8, s8, 0x80000
	s_addc_u32 s9, s9, 0
	global_load_dwordx2 v[4:5], v26, s[8:9] nt
	s_add_u32 s8, s8, 0x80000
	s_addc_u32 s9, s9, 0
	global_load_dwordx2 v[6:7], v26, s[8:9] nt
	s_add_u32 s8, s8, 0x80000
	s_addc_u32 s9, s9, 0
	global_load_dwordx2 v[8:9], v26, s[8:9] nt
	s_add_u32 s8, s8, 0x80000
	s_addc_u32 s9, s9, 0
	global_load_dwordx2 v[10:11], v26, s[8:9] nt
	s_add_u32 s8, s8, 0x80000
	s_addc_u32 s9, s9, 0
	global_load_dwordx2 v[12:13], v26, s[8:9] nt
	s_add_u32 s8, s8, 0x80000
	s_addc_u32 s9, s9, 0
	global_load_dwordx2 v[14:15], v26, s[8:9] nt
	s_add_u32 s8, s8, 0x80000
	s_addc_u32 s9, s9, 0
	global_load_dwordx2 v[16:17], v26, s[8:9] nt
	s_add_u32 s8, s8, 0x80000
	s_addc_u32 s9, s9, 0
	global_load_dwordx2 v[18:19], v26, s[8:9] nt
	s_add_u32 s8, s8, 0x80000
	s_addc_u32 s9, s9, 0
	global_load_dwordx2 v[20:21], v26, s[8:9] nt
	s_add_u32 s8, s8, 0x80000
	s_addc_u32 s9, s9, 0
	global_load_dwordx2 v[22:23], v26, s[8:9] nt
	s_mov_b32 s0, 0x3aaaaaab
	s_mov_b32 s1, 0xf800000
	s_waitcnt vmcnt(10)
	v_pk_add_f32 v[0:1], v[0:1], v[2:3]
	s_waitcnt vmcnt(8)
	v_pk_add_f32 v[2:3], v[4:5], v[6:7]
	v_pk_add_f32 v[0:1], v[0:1], 0 op_sel_hi:[1,0]
	s_waitcnt vmcnt(6)
	v_pk_add_f32 v[4:5], v[8:9], v[10:11]
	v_pk_add_f32 v[0:1], v[0:1], v[2:3]
	s_waitcnt vmcnt(4)
	v_pk_add_f32 v[6:7], v[12:13], v[14:15]
	v_pk_add_f32 v[0:1], v[0:1], v[4:5]
	s_waitcnt vmcnt(2)
	v_pk_add_f32 v[8:9], v[16:17], v[18:19]
	v_pk_add_f32 v[0:1], v[0:1], v[6:7]
	s_waitcnt vmcnt(0)
	v_pk_add_f32 v[10:11], v[20:21], v[22:23]
	v_pk_add_f32 v[0:1], v[0:1], v[8:9]
	v_mov_b32_e32 v3, 0x260
	v_pk_add_f32 v[0:1], v[0:1], v[10:11]
	s_nop 0
	v_pk_mul_f32 v[0:1], v[0:1], s[0:1] op_sel_hi:[1,0]
	s_nop 0
	v_fma_f32 v1, -v0, v0, v1
	v_max_f32_e32 v1, 0, v1
	v_add_f32_e32 v1, 0x3727c5ac, v1
	v_mul_f32_e32 v2, 0x4f800000, v1
	v_cmp_gt_f32_e32 vcc, s1, v1
	s_nop 1
	v_cndmask_b32_e32 v1, v1, v2, vcc
	v_sqrt_f32_e32 v2, v1
	s_nop 0
	v_add_u32_e32 v4, -1, v2
	v_add_u32_e32 v5, 1, v2
	v_fma_f32 v6, -v4, v2, v1
	v_fma_f32 v7, -v5, v2, v1
	v_cmp_ge_f32_e64 s[0:1], 0, v6
	s_nop 1
	v_cndmask_b32_e64 v2, v2, v4, s[0:1]
	v_cmp_lt_f32_e64 s[0:1], 0, v7
	s_nop 1
	v_cndmask_b32_e64 v2, v2, v5, s[0:1]
	v_mul_f32_e32 v4, 0x37800000, v2
	v_cndmask_b32_e32 v2, v2, v4, vcc
	v_cmp_class_f32_e32 vcc, v1, v3
	s_nop 1
	v_cndmask_b32_e32 v1, v2, v1, vcc
	v_div_scale_f32 v2, s[0:1], v1, v1, 1.0
	v_rcp_f32_e32 v3, v2
	v_div_scale_f32 v4, vcc, 1.0, v1, 1.0
	v_fma_f32 v5, -v2, v3, 1.0
	v_fmac_f32_e32 v3, v5, v3
	v_mul_f32_e32 v5, v4, v3
	v_fma_f32 v6, -v2, v5, v4
	v_fmac_f32_e32 v5, v6, v3
	v_fma_f32 v2, -v2, v5, v4
	v_div_fmas_f32 v2, v2, v3, v5
	v_div_fixup_f32 v1, v2, v1, 1.0
	v_lshl_add_u64 v[2:3], v[24:25], 3, s[6:7]
	global_store_dwordx2 v[2:3], v[0:1], off
	s_endpgm

	.amdhsa_kernel _Z9k_rowstatPKDv2_fPS_
		.amdhsa_group_segment_fixed_size 0
		.amdhsa_private_segment_fixed_size 0
		.amdhsa_kernarg_size 16
		.amdhsa_user_sgpr_count 2
		.amdhsa_user_sgpr_dispatch_ptr 0
		.amdhsa_user_sgpr_queue_ptr 0
		.amdhsa_user_sgpr_kernarg_segment_ptr 1
		.amdhsa_user_sgpr_dispatch_id 0
		.amdhsa_user_sgpr_kernarg_preload_length 0
		.amdhsa_user_sgpr_kernarg_preload_offset 0
		.amdhsa_user_sgpr_private_segment_size 0
		.amdhsa_uses_dynamic_stack 0
		.amdhsa_enable_private_segment 0
		.amdhsa_system_sgpr_workgroup_id_x 1
		.amdhsa_system_sgpr_workgroup_id_y 0
		.amdhsa_system_sgpr_workgroup_id_z 0
		.amdhsa_system_sgpr_workgroup_info 0
		.amdhsa_system_vgpr_workitem_id 0
		.amdhsa_next_free_vgpr 28
		.amdhsa_next_free_sgpr 10
		.amdhsa_accum_offset 28
		.amdhsa_reserve_vcc 1
		.amdhsa_float_round_mode_32 0
		.amdhsa_float_round_mode_16_64 0
		.amdhsa_float_denorm_mode_32 3
		.amdhsa_float_denorm_mode_16_64 3
		.amdhsa_dx10_clamp 1
		.amdhsa_ieee_mode 1
		.amdhsa_fp16_overflow 0
		.amdhsa_tg_split 0
		.amdhsa_exception_fp_ieee_invalid_op 0
		.amdhsa_exception_fp_denorm_src 0
		.amdhsa_exception_fp_ieee_div_zero 0
		.amdhsa_exception_fp_ieee_overflow 0
		.amdhsa_exception_fp_ieee_underflow 0
		.amdhsa_exception_fp_ieee_inexact 0
		.amdhsa_exception_int_div_zero 0
	.end_amdhsa_kernel

.LBB8_27:
	ds_read_b128 v[72:75], v231
	ds_read_b128 v[80:83], v231 offset:1024
	ds_read_b128 v[88:91], v231 offset:2048
	ds_read_b128 v[92:95], v231 offset:3072
	s_add_u32 s40, s38, 0xfffd0080
	s_addc_u32 s41, s39, -1
	s_cmp_eq_u32 s87, 8
	s_cselect_b32 s43, s9, s41
	s_cselect_b32 s42, s8, s40
	s_cselect_b32 s41, s1, s86
	s_cselect_b32 s40, s0, s85
	v_lshl_add_u64 v[190:191], s[38:39], 0, v[184:185]
	s_add_i32 m0, s51, 0xc000
	ds_read_b128 v[136:139], v232
	ds_read_b128 v[148:151], v232 offset:1024
	ds_read_b128 v[152:155], v232 offset:2048
	ds_read_b128 v[156:159], v232 offset:3072
	ds_read_b128 v[160:163], v232 offset:4096
	ds_read_b128 v[164:167], v232 offset:5120
	ds_read_b128 v[168:171], v232 offset:6144
	ds_read_b128 v[172:175], v232 offset:7168
	global_load_lds_dwordx4 v[190:191], off
	v_lshl_add_u64 v[190:191], s[38:39], 0, v[186:187]
	s_add_i32 m0, s51, 0xe000
	s_nop 0
	global_load_lds_dwordx4 v[190:191], off
	s_waitcnt lgkmcnt(8)
	s_barrier
	s_waitcnt lgkmcnt(0)
	s_setprio 1
	s_waitcnt lgkmcnt(0)
	v_mfma_f32_16x16x32_f16 v[144:147], v[72:75], v[136:139], v[144:147]
	v_mfma_f32_16x16x32_f16 v[140:143], v[88:91], v[136:139], v[140:143]
	v_mfma_f32_16x16x32_f16 v[124:127], v[72:75], v[152:155], v[124:127]
	v_mfma_f32_16x16x32_f16 v[120:123], v[88:91], v[152:155], v[120:123]
	v_mfma_f32_16x16x32_f16 v[108:111], v[72:75], v[160:163], v[108:111]
	v_mfma_f32_16x16x32_f16 v[104:107], v[88:91], v[160:163], v[104:107]
	v_mfma_f32_16x16x32_f16 v[84:87], v[72:75], v[168:171], v[84:87]
	v_mfma_f32_16x16x32_f16 v[76:79], v[88:91], v[168:171], v[76:79]
	v_mfma_f32_16x16x32_f16 v[144:147], v[80:83], v[148:151], v[144:147]
	v_mfma_f32_16x16x32_f16 v[140:143], v[92:95], v[148:151], v[140:143]
	v_mfma_f32_16x16x32_f16 v[124:127], v[80:83], v[156:159], v[124:127]
	v_mfma_f32_16x16x32_f16 v[120:123], v[92:95], v[156:159], v[120:123]
	v_mfma_f32_16x16x32_f16 v[108:111], v[80:83], v[164:167], v[108:111]
	v_mfma_f32_16x16x32_f16 v[104:107], v[92:95], v[164:167], v[104:107]
	v_mfma_f32_16x16x32_f16 v[84:87], v[80:83], v[172:175], v[84:87]
	v_mfma_f32_16x16x32_f16 v[76:79], v[92:95], v[172:175], v[76:79]
	s_setprio 0
	s_barrier
	s_add_i32 s88, s70, s50
	v_lshl_add_u64 v[206:207], s[40:41], 0, v[178:179]
	s_mov_b32 m0, s88
	ds_read_b128 v[190:193], v233
	ds_read_b128 v[194:197], v233 offset:1024
	ds_read_b128 v[198:201], v233 offset:2048
	ds_read_b128 v[202:205], v233 offset:3072
	global_load_lds_dwordx4 v[206:207], off
	v_lshl_add_u64 v[208:209], s[40:41], 0, v[182:183]
	s_add_i32 m0, s88, 0x2000
	s_nop 0
	global_load_lds_dwordx4 v[208:209], off
	s_barrier
	s_waitcnt lgkmcnt(0)
	s_setprio 1
	s_waitcnt lgkmcnt(0)
	v_mfma_f32_16x16x32_f16 v[132:135], v[190:193], v[136:139], v[132:135]
	v_mfma_f32_16x16x32_f16 v[128:131], v[198:201], v[136:139], v[128:131]
	v_mfma_f32_16x16x32_f16 v[116:119], v[190:193], v[152:155], v[116:119]
	v_mfma_f32_16x16x32_f16 v[112:115], v[198:201], v[152:155], v[112:115]
	v_mfma_f32_16x16x32_f16 v[100:103], v[190:193], v[160:163], v[100:103]
	v_mfma_f32_16x16x32_f16 v[96:99], v[198:201], v[160:163], v[96:99]
	v_mfma_f32_16x16x32_f16 v[68:71], v[190:193], v[168:171], v[68:71]
	v_mfma_f32_16x16x32_f16 v[64:67], v[198:201], v[168:171], v[64:67]
	v_mfma_f32_16x16x32_f16 v[132:135], v[194:197], v[148:151], v[132:135]
	v_mfma_f32_16x16x32_f16 v[128:131], v[202:205], v[148:151], v[128:131]
	v_mfma_f32_16x16x32_f16 v[116:119], v[194:197], v[156:159], v[116:119]
	v_mfma_f32_16x16x32_f16 v[112:115], v[202:205], v[156:159], v[112:115]
	v_mfma_f32_16x16x32_f16 v[100:103], v[194:197], v[164:167], v[100:103]
	v_mfma_f32_16x16x32_f16 v[96:99], v[202:205], v[164:167], v[96:99]
	v_mfma_f32_16x16x32_f16 v[68:71], v[194:197], v[172:175], v[68:71]
	v_mfma_f32_16x16x32_f16 v[64:67], v[202:205], v[172:175], v[64:67]
	s_setprio 0
	s_mov_b32 m0, s51
	v_lshl_add_u64 v[210:211], s[42:43], 0, v[176:177]
	s_barrier
	ds_read_b128 v[136:139], v232 offset:16384
	ds_read_b128 v[148:151], v232 offset:17408
	ds_read_b128 v[152:155], v232 offset:18432
	ds_read_b128 v[156:159], v232 offset:19456
	ds_read_b128 v[160:163], v232 offset:20480
	ds_read_b128 v[164:167], v232 offset:21504
	ds_read_b128 v[168:171], v232 offset:22528
	ds_read_b128 v[172:175], v232 offset:23552
	global_load_lds_dwordx4 v[210:211], off
	v_lshl_add_u64 v[212:213], s[42:43], 0, v[180:181]
	s_mov_b32 m0, s52
	s_nop 0
	global_load_lds_dwordx4 v[212:213], off
	s_barrier
	s_waitcnt lgkmcnt(0)
	s_setprio 1
	s_waitcnt lgkmcnt(0)
	v_mfma_f32_16x16x32_f16 v[60:63], v[72:75], v[136:139], v[60:63]
	v_mfma_f32_16x16x32_f16 v[56:59], v[88:91], v[136:139], v[56:59]
	v_mfma_f32_16x16x32_f16 v[44:47], v[72:75], v[152:155], v[44:47]
	v_mfma_f32_16x16x32_f16 v[40:43], v[88:91], v[152:155], v[40:43]
	v_mfma_f32_16x16x32_f16 v[28:31], v[72:75], v[160:163], v[28:31]
	v_mfma_f32_16x16x32_f16 v[24:27], v[88:91], v[160:163], v[24:27]
	v_mfma_f32_16x16x32_f16 v[12:15], v[72:75], v[168:171], v[12:15]
	v_mfma_f32_16x16x32_f16 v[8:11], v[88:91], v[168:171], v[8:11]
	v_mfma_f32_16x16x32_f16 v[60:63], v[80:83], v[148:151], v[60:63]
	v_mfma_f32_16x16x32_f16 v[56:59], v[92:95], v[148:151], v[56:59]
	v_mfma_f32_16x16x32_f16 v[44:47], v[80:83], v[156:159], v[44:47]
	v_mfma_f32_16x16x32_f16 v[40:43], v[92:95], v[156:159], v[40:43]
	v_mfma_f32_16x16x32_f16 v[28:31], v[80:83], v[164:167], v[28:31]
	v_mfma_f32_16x16x32_f16 v[24:27], v[92:95], v[164:167], v[24:27]
	v_mfma_f32_16x16x32_f16 v[12:15], v[80:83], v[172:175], v[12:15]
	v_mfma_f32_16x16x32_f16 v[8:11], v[92:95], v[172:175], v[8:11]
	s_setprio 0
	s_barrier
	s_add_u32 s88, s40, 0xc000
	s_addc_u32 s89, s41, 0
	s_add_i32 s90, s71, s50
	v_lshl_add_u64 v[72:73], s[88:89], 0, v[178:179]
	s_mov_b32 m0, s90
	s_nop 0
	global_load_lds_dwordx4 v[72:73], off
	v_lshl_add_u64 v[72:73], s[88:89], 0, v[182:183]
	s_add_i32 m0, s90, 0x2000
	s_nop 0
	global_load_lds_dwordx4 v[72:73], off
	s_waitcnt vmcnt(6)
	s_barrier
	s_setprio 1
	v_mfma_f32_16x16x32_f16 v[52:55], v[190:193], v[136:139], v[52:55]
	v_mfma_f32_16x16x32_f16 v[48:51], v[198:201], v[136:139], v[48:51]
	v_mfma_f32_16x16x32_f16 v[36:39], v[190:193], v[152:155], v[36:39]
	v_mfma_f32_16x16x32_f16 v[32:35], v[198:201], v[152:155], v[32:35]
	v_mfma_f32_16x16x32_f16 v[20:23], v[190:193], v[160:163], v[20:23]
	v_mfma_f32_16x16x32_f16 v[16:19], v[198:201], v[160:163], v[16:19]
	v_mfma_f32_16x16x32_f16 v[4:7], v[190:193], v[168:171], v[4:7]
	v_mfma_f32_16x16x32_f16 v[0:3], v[198:201], v[168:171], v[0:3]
	v_mfma_f32_16x16x32_f16 v[52:55], v[194:197], v[148:151], v[52:55]
	v_mfma_f32_16x16x32_f16 v[48:51], v[202:205], v[148:151], v[48:51]
	v_mfma_f32_16x16x32_f16 v[36:39], v[194:197], v[156:159], v[36:39]
	v_mfma_f32_16x16x32_f16 v[32:35], v[202:205], v[156:159], v[32:35]
	v_mfma_f32_16x16x32_f16 v[20:23], v[194:197], v[164:167], v[20:23]
	v_mfma_f32_16x16x32_f16 v[16:19], v[202:205], v[164:167], v[16:19]
	v_mfma_f32_16x16x32_f16 v[4:7], v[194:197], v[172:175], v[4:7]
	v_mfma_f32_16x16x32_f16 v[0:3], v[202:205], v[172:175], v[0:3]
	s_setprio 0
	s_add_i32 s88, 0, 0x18000
	v_add_u32_e32 v92, s88, v228
	s_barrier
	ds_read_b128 v[72:75], v92
	ds_read_b128 v[80:83], v92 offset:1024
	ds_read_b128 v[88:91], v92 offset:2048
	ds_read_b128 v[92:95], v92 offset:3072
	s_add_u32 s42, s42, 0x30000
	s_addc_u32 s43, s43, 0
	s_mov_b32 m0, s53
	v_lshl_add_u64 v[190:191], s[42:43], 0, v[176:177]
	ds_read_b128 v[136:139], v232 offset:32768
	ds_read_b128 v[148:151], v232 offset:33792
	ds_read_b128 v[152:155], v232 offset:34816
	ds_read_b128 v[156:159], v232 offset:35840
	ds_read_b128 v[160:163], v232 offset:36864
	ds_read_b128 v[164:167], v232 offset:37888
	ds_read_b128 v[168:171], v232 offset:38912
	ds_read_b128 v[172:175], v232 offset:39936
	global_load_lds_dwordx4 v[190:191], off
	v_lshl_add_u64 v[190:191], s[42:43], 0, v[180:181]
	s_mov_b32 m0, s54
	s_nop 0
	global_load_lds_dwordx4 v[190:191], off
	s_waitcnt lgkmcnt(8)
	s_barrier
	s_waitcnt lgkmcnt(0)
	s_setprio 1
	s_waitcnt lgkmcnt(0)
	v_mfma_f32_16x16x32_f16 v[144:147], v[72:75], v[136:139], v[144:147]
	v_mfma_f32_16x16x32_f16 v[140:143], v[88:91], v[136:139], v[140:143]
	v_mfma_f32_16x16x32_f16 v[124:127], v[72:75], v[152:155], v[124:127]
	v_mfma_f32_16x16x32_f16 v[120:123], v[88:91], v[152:155], v[120:123]
	v_mfma_f32_16x16x32_f16 v[108:111], v[72:75], v[160:163], v[108:111]
	v_mfma_f32_16x16x32_f16 v[104:107], v[88:91], v[160:163], v[104:107]
	v_mfma_f32_16x16x32_f16 v[84:87], v[72:75], v[168:171], v[84:87]
	v_mfma_f32_16x16x32_f16 v[76:79], v[88:91], v[168:171], v[76:79]
	v_mfma_f32_16x16x32_f16 v[144:147], v[80:83], v[148:151], v[144:147]
	v_mfma_f32_16x16x32_f16 v[140:143], v[92:95], v[148:151], v[140:143]
	v_mfma_f32_16x16x32_f16 v[124:127], v[80:83], v[156:159], v[124:127]
	v_mfma_f32_16x16x32_f16 v[120:123], v[92:95], v[156:159], v[120:123]
	v_mfma_f32_16x16x32_f16 v[108:111], v[80:83], v[164:167], v[108:111]
	v_mfma_f32_16x16x32_f16 v[104:107], v[92:95], v[164:167], v[104:107]
	v_mfma_f32_16x16x32_f16 v[84:87], v[80:83], v[172:175], v[84:87]
	v_mfma_f32_16x16x32_f16 v[76:79], v[92:95], v[172:175], v[76:79]
	s_setprio 0
	s_barrier
	s_add_i32 s42, 0, 0x1c000
	s_add_i32 s43, s88, s50
	v_add_u32_e32 v202, s42, v228
	v_lshl_add_u64 v[206:207], v[206:207], 0, s[36:37]
	s_mov_b32 m0, s43
	ds_read_b128 v[190:193], v202
	ds_read_b128 v[194:197], v202 offset:1024
	ds_read_b128 v[198:201], v202 offset:2048
	ds_read_b128 v[202:205], v202 offset:3072
	global_load_lds_dwordx4 v[206:207], off
	v_lshl_add_u64 v[206:207], v[208:209], 0, s[36:37]
	s_add_i32 m0, s43, 0x2000
	s_nop 0
	global_load_lds_dwordx4 v[206:207], off
	s_barrier
	s_waitcnt lgkmcnt(0)
	s_setprio 1
	s_waitcnt lgkmcnt(0)
	v_mfma_f32_16x16x32_f16 v[132:135], v[190:193], v[136:139], v[132:135]
	v_mfma_f32_16x16x32_f16 v[128:131], v[198:201], v[136:139], v[128:131]
	v_mfma_f32_16x16x32_f16 v[116:119], v[190:193], v[152:155], v[116:119]
	v_mfma_f32_16x16x32_f16 v[112:115], v[198:201], v[152:155], v[112:115]
	v_mfma_f32_16x16x32_f16 v[100:103], v[190:193], v[160:163], v[100:103]
	v_mfma_f32_16x16x32_f16 v[96:99], v[198:201], v[160:163], v[96:99]
	v_mfma_f32_16x16x32_f16 v[68:71], v[190:193], v[168:171], v[68:71]
	v_mfma_f32_16x16x32_f16 v[64:67], v[198:201], v[168:171], v[64:67]
	v_mfma_f32_16x16x32_f16 v[132:135], v[194:197], v[148:151], v[132:135]
	v_mfma_f32_16x16x32_f16 v[128:131], v[202:205], v[148:151], v[128:131]
	v_mfma_f32_16x16x32_f16 v[116:119], v[194:197], v[156:159], v[116:119]
	v_mfma_f32_16x16x32_f16 v[112:115], v[202:205], v[156:159], v[112:115]
	v_mfma_f32_16x16x32_f16 v[100:103], v[194:197], v[164:167], v[100:103]
	v_mfma_f32_16x16x32_f16 v[96:99], v[202:205], v[164:167], v[96:99]
	v_mfma_f32_16x16x32_f16 v[68:71], v[194:197], v[172:175], v[68:71]
	v_mfma_f32_16x16x32_f16 v[64:67], v[202:205], v[172:175], v[64:67]
	s_setprio 0
	s_mov_b32 m0, s59
	v_lshl_add_u64 v[206:207], v[210:211], 0, s[36:37]
	s_barrier
	ds_read_b128 v[136:139], v232 offset:49152
	ds_read_b128 v[148:151], v232 offset:50176
	ds_read_b128 v[152:155], v232 offset:51200
	ds_read_b128 v[156:159], v232 offset:52224
	ds_read_b128 v[160:163], v232 offset:53248
	ds_read_b128 v[164:167], v232 offset:54272
	ds_read_b128 v[168:171], v232 offset:55296
	ds_read_b128 v[172:175], v232 offset:56320
	global_load_lds_dwordx4 v[206:207], off
	v_lshl_add_u64 v[206:207], v[212:213], 0, s[36:37]
	s_mov_b32 m0, s60
	s_nop 0
	global_load_lds_dwordx4 v[206:207], off
	s_barrier
	s_waitcnt lgkmcnt(0)
	s_setprio 1
	s_waitcnt lgkmcnt(0)
	v_mfma_f32_16x16x32_f16 v[60:63], v[72:75], v[136:139], v[60:63]
	v_mfma_f32_16x16x32_f16 v[56:59], v[88:91], v[136:139], v[56:59]
	v_mfma_f32_16x16x32_f16 v[44:47], v[72:75], v[152:155], v[44:47]
	v_mfma_f32_16x16x32_f16 v[40:43], v[88:91], v[152:155], v[40:43]
	v_mfma_f32_16x16x32_f16 v[28:31], v[72:75], v[160:163], v[28:31]
	v_mfma_f32_16x16x32_f16 v[24:27], v[88:91], v[160:163], v[24:27]
	v_mfma_f32_16x16x32_f16 v[12:15], v[72:75], v[168:171], v[12:15]
	v_mfma_f32_16x16x32_f16 v[8:11], v[88:91], v[168:171], v[8:11]
	v_mfma_f32_16x16x32_f16 v[60:63], v[80:83], v[148:151], v[60:63]
	v_mfma_f32_16x16x32_f16 v[56:59], v[92:95], v[148:151], v[56:59]
	v_mfma_f32_16x16x32_f16 v[44:47], v[80:83], v[156:159], v[44:47]
	v_mfma_f32_16x16x32_f16 v[40:43], v[92:95], v[156:159], v[40:43]
	v_mfma_f32_16x16x32_f16 v[28:31], v[80:83], v[164:167], v[28:31]
	v_mfma_f32_16x16x32_f16 v[24:27], v[92:95], v[164:167], v[24:27]
	v_mfma_f32_16x16x32_f16 v[12:15], v[80:83], v[172:175], v[12:15]
	v_mfma_f32_16x16x32_f16 v[8:11], v[92:95], v[172:175], v[8:11]
	s_setprio 0
	s_barrier
	s_add_u32 s40, s40, 0xc080
	s_addc_u32 s41, s41, 0
	s_add_i32 s42, s42, s50
	v_lshl_add_u64 v[72:73], s[40:41], 0, v[178:179]
	s_mov_b32 m0, s42
	s_nop 0
	global_load_lds_dwordx4 v[72:73], off
	v_lshl_add_u64 v[72:73], s[40:41], 0, v[182:183]
	s_add_i32 m0, s42, 0x2000
	s_nop 0
	global_load_lds_dwordx4 v[72:73], off
	s_waitcnt vmcnt(6)
	s_barrier
	s_setprio 1
	v_mfma_f32_16x16x32_f16 v[52:55], v[190:193], v[136:139], v[52:55]
	v_mfma_f32_16x16x32_f16 v[48:51], v[198:201], v[136:139], v[48:51]
	v_mfma_f32_16x16x32_f16 v[36:39], v[190:193], v[152:155], v[36:39]
	v_mfma_f32_16x16x32_f16 v[32:35], v[198:201], v[152:155], v[32:35]
	v_mfma_f32_16x16x32_f16 v[20:23], v[190:193], v[160:163], v[20:23]
	v_mfma_f32_16x16x32_f16 v[16:19], v[198:201], v[160:163], v[16:19]
	v_mfma_f32_16x16x32_f16 v[4:7], v[190:193], v[168:171], v[4:7]
	v_mfma_f32_16x16x32_f16 v[0:3], v[198:201], v[168:171], v[0:3]
	v_mfma_f32_16x16x32_f16 v[52:55], v[194:197], v[148:151], v[52:55]
	v_mfma_f32_16x16x32_f16 v[48:51], v[202:205], v[148:151], v[48:51]
	v_mfma_f32_16x16x32_f16 v[36:39], v[194:197], v[156:159], v[36:39]
	v_mfma_f32_16x16x32_f16 v[32:35], v[202:205], v[156:159], v[32:35]
	v_mfma_f32_16x16x32_f16 v[20:23], v[194:197], v[164:167], v[20:23]
	v_mfma_f32_16x16x32_f16 v[16:19], v[202:205], v[164:167], v[16:19]
	v_mfma_f32_16x16x32_f16 v[4:7], v[194:197], v[172:175], v[4:7]
	v_mfma_f32_16x16x32_f16 v[0:3], v[202:205], v[172:175], v[0:3]
	s_setprio 0
	s_add_i32 s87, s87, 2
	s_add_u32 s38, s38, 0x100
	s_addc_u32 s39, s39, 0
	s_add_u32 s85, s85, 0x100
	s_addc_u32 s86, s86, 0
	s_cmp_gt_u32 s87, 9
	s_barrier
	s_cbranch_scc0 .LBB8_27
	s_lshl_b32 s92, s84, 8
	s_add_i32 s92, s92, s58
	s_lshl_b32 s93, s83, 8
	s_or_b32 s93, s93, s61
	v_lshlrev_b32_e32 v237, 2, v226
	s_lshl_b32 s96, s93, 2
	s_add_u32 s94, s16, s96
	s_addc_u32 s95, s17, 0
	global_load_dwordx4 v[72:75], v237, s[94:95] offset:0
	global_load_dwordx4 v[80:83], v237, s[94:95] offset:16
	global_load_dwordx4 v[88:91], v237, s[94:95] offset:128
	global_load_dwordx4 v[92:95], v237, s[94:95] offset:144
	s_add_u32 s94, s18, s96
	s_addc_u32 s95, s19, 0
	global_load_dwordx4 v[136:139], v237, s[94:95] offset:0
	global_load_dwordx4 v[148:151], v237, s[94:95] offset:16
	global_load_dwordx4 v[152:155], v237, s[94:95] offset:128
	global_load_dwordx4 v[156:159], v237, s[94:95] offset:144
	s_add_u32 s94, s14, s96
	s_addc_u32 s95, s15, 0
	global_load_dwordx4 v[160:163], v237, s[94:95] offset:0
	global_load_dwordx4 v[164:167], v237, s[94:95] offset:16
	global_load_dwordx4 v[168:171], v237, s[94:95] offset:128
	global_load_dwordx4 v[172:175], v237, s[94:95] offset:144
	v_lshlrev_b32_e32 v190, 3, v227
	s_lshl_b32 s96, s92, 3
	s_add_u32 s94, s12, s96
	s_addc_u32 s95, s13, 0
	global_load_dwordx2 v[238:239], v190, s[94:95] offset:0
	global_load_dwordx2 v[192:193], v190, s[94:95] offset:128
	global_load_dwordx2 v[194:195], v190, s[94:95] offset:256
	global_load_dwordx2 v[196:197], v190, s[94:95] offset:384
	global_load_dwordx2 v[198:199], v190, s[94:95] offset:1024
	global_load_dwordx2 v[200:201], v190, s[94:95] offset:1152
	global_load_dwordx2 v[202:203], v190, s[94:95] offset:1280
	global_load_dwordx2 v[204:205], v190, s[94:95] offset:1408
	v_mul_u32_u24_e32 v191, 0x600, v227
	v_lshl_add_u32 v191, v226, 1, v191
	s_mul_i32 s96, s92, 0x600
	s_lshl_b32 s97, s93, 1
	s_add_u32 s96, s96, s97
	s_add_u32 s98, s10, s96
	s_addc_u32 s99, s11, 0
	s_add_u32 s94, s98, 0x0
	s_addc_u32 s95, s99, 0
	global_load_dwordx4 v[208:211], v191, s[94:95] offset:0 nt
	global_load_dwordx4 v[212:215], v191, s[94:95] offset:64 nt
	s_add_u32 s94, s98, 0x6000
	s_addc_u32 s95, s99, 0
	global_load_dwordx4 v[216:219], v191, s[94:95] offset:0 nt
	global_load_dwordx4 v[220:223], v191, s[94:95] offset:64 nt
	v_add_u32_e32 v224, s92, v229
	v_mul_u32_u24_e32 v224, 0x600, v224
	s_lshl_b32 s97, s93, 1
	v_add3_u32 v224, v224, v230, s97
	s_lshl_b32 s96, s83, 2
	s_lshr_b32 s97, s61, 6
	s_add_u32 s96, s96, s97
	s_lshl_b32 s96, s96, 19
	s_lshl_b32 s97, s92, 3
	s_add_u32 s96, s96, s97
	s_add_u32 s100, s28, s96
	s_addc_u32 s101, s29, 0
	s_waitcnt vmcnt(19)
	v_pk_add_f32 v[72:73], v[72:73], v[136:137]
	v_pk_add_f32 v[74:75], v[74:75], v[138:139]
	s_waitcnt vmcnt(18)
	v_pk_add_f32 v[80:81], v[80:81], v[148:149]
	v_pk_add_f32 v[82:83], v[82:83], v[150:151]
	s_waitcnt vmcnt(17)
	v_pk_add_f32 v[88:89], v[88:89], v[152:153]
	v_pk_add_f32 v[90:91], v[90:91], v[154:155]
	s_waitcnt vmcnt(16)
	v_pk_add_f32 v[92:93], v[92:93], v[156:157]
	v_pk_add_f32 v[94:95], v[94:95], v[158:159]
	v_pk_add_f32 v[144:145], v[144:145], v[72:73]
	v_pk_add_f32 v[146:147], v[146:147], v[74:75]
	v_pk_add_f32 v[124:125], v[124:125], v[72:73]
	v_pk_add_f32 v[126:127], v[126:127], v[74:75]
	v_pk_add_f32 v[108:109], v[108:109], v[72:73]
	v_pk_add_f32 v[110:111], v[110:111], v[74:75]
	v_pk_add_f32 v[84:85], v[84:85], v[72:73]
	v_pk_add_f32 v[86:87], v[86:87], v[74:75]
	v_pk_add_f32 v[60:61], v[60:61], v[72:73]
	v_pk_add_f32 v[62:63], v[62:63], v[74:75]
	v_pk_add_f32 v[44:45], v[44:45], v[72:73]
	v_pk_add_f32 v[46:47], v[46:47], v[74:75]
	v_pk_add_f32 v[28:29], v[28:29], v[72:73]
	v_pk_add_f32 v[30:31], v[30:31], v[74:75]
	v_pk_add_f32 v[12:13], v[12:13], v[72:73]
	v_pk_add_f32 v[14:15], v[14:15], v[74:75]
	v_pk_add_f32 v[140:141], v[140:141], v[80:81]
	v_pk_add_f32 v[142:143], v[142:143], v[82:83]
	v_pk_add_f32 v[120:121], v[120:121], v[80:81]
	v_pk_add_f32 v[122:123], v[122:123], v[82:83]
	v_pk_add_f32 v[104:105], v[104:105], v[80:81]
	v_pk_add_f32 v[106:107], v[106:107], v[82:83]
	v_pk_add_f32 v[76:77], v[76:77], v[80:81]
	v_pk_add_f32 v[78:79], v[78:79], v[82:83]
	v_pk_add_f32 v[56:57], v[56:57], v[80:81]
	v_pk_add_f32 v[58:59], v[58:59], v[82:83]
	v_pk_add_f32 v[40:41], v[40:41], v[80:81]
	v_pk_add_f32 v[42:43], v[42:43], v[82:83]
	v_pk_add_f32 v[24:25], v[24:25], v[80:81]
	v_pk_add_f32 v[26:27], v[26:27], v[82:83]
	v_pk_add_f32 v[8:9], v[8:9], v[80:81]
	v_pk_add_f32 v[10:11], v[10:11], v[82:83]
	v_pk_add_f32 v[132:133], v[132:133], v[88:89]
	v_pk_add_f32 v[134:135], v[134:135], v[90:91]
	v_pk_add_f32 v[116:117], v[116:117], v[88:89]
	v_pk_add_f32 v[118:119], v[118:119], v[90:91]
	v_pk_add_f32 v[100:101], v[100:101], v[88:89]
	v_pk_add_f32 v[102:103], v[102:103], v[90:91]
	v_pk_add_f32 v[68:69], v[68:69], v[88:89]
	v_pk_add_f32 v[70:71], v[70:71], v[90:91]
	v_pk_add_f32 v[52:53], v[52:53], v[88:89]
	v_pk_add_f32 v[54:55], v[54:55], v[90:91]
	v_pk_add_f32 v[36:37], v[36:37], v[88:89]
	v_pk_add_f32 v[38:39], v[38:39], v[90:91]
	v_pk_add_f32 v[20:21], v[20:21], v[88:89]
	v_pk_add_f32 v[22:23], v[22:23], v[90:91]
	v_pk_add_f32 v[4:5], v[4:5], v[88:89]
	v_pk_add_f32 v[6:7], v[6:7], v[90:91]
	v_pk_add_f32 v[128:129], v[128:129], v[92:93]
	v_pk_add_f32 v[130:131], v[130:131], v[94:95]
	v_pk_add_f32 v[112:113], v[112:113], v[92:93]
	v_pk_add_f32 v[114:115], v[114:115], v[94:95]
	v_pk_add_f32 v[96:97], v[96:97], v[92:93]
	v_pk_add_f32 v[98:99], v[98:99], v[94:95]
	v_pk_add_f32 v[64:65], v[64:65], v[92:93]
	v_pk_add_f32 v[66:67], v[66:67], v[94:95]
	v_pk_add_f32 v[48:49], v[48:49], v[92:93]
	v_pk_add_f32 v[50:51], v[50:51], v[94:95]
	v_pk_add_f32 v[32:33], v[32:33], v[92:93]
	v_pk_add_f32 v[34:35], v[34:35], v[94:95]
	v_pk_add_f32 v[16:17], v[16:17], v[92:93]
	v_pk_add_f32 v[18:19], v[18:19], v[94:95]
	v_pk_add_f32 v[0:1], v[0:1], v[92:93]
	v_pk_add_f32 v[2:3], v[2:3], v[94:95]
	s_add_u32 s94, s98, 0xc000
	s_addc_u32 s95, s99, 0
	global_load_dwordx4 v[240:243], v191, s[94:95] offset:0 nt
	global_load_dwordx4 v[244:247], v191, s[94:95] offset:64 nt
	s_add_u32 s94, s98, 0x12000
	s_addc_u32 s95, s99, 0
	global_load_dwordx4 v[248:251], v191, s[94:95] offset:0 nt
	global_load_dwordx4 v[252:255], v191, s[94:95] offset:64 nt
	s_add_u32 s94, s98, 0x30000
	s_addc_u32 s95, s99, 0
	global_load_dwordx4 v[136:139], v191, s[94:95] offset:0 nt
	global_load_dwordx4 v[148:151], v191, s[94:95] offset:64 nt
	s_add_u32 s94, s98, 0x36000
	s_addc_u32 s95, s99, 0
	global_load_dwordx4 v[152:155], v191, s[94:95] offset:0 nt
	global_load_dwordx4 v[156:159], v191, s[94:95] offset:64 nt
	s_waitcnt vmcnt(19)
	s_waitcnt vmcnt(11)
	v_cvt_f32_f16_e32 v72, v208
	v_cvt_f32_f16_sdwa v73, v208 dst_sel:DWORD dst_unused:UNUSED_PAD src0_sel:WORD_1
	v_cvt_f32_f16_e32 v74, v209
	v_cvt_f32_f16_sdwa v75, v209 dst_sel:DWORD dst_unused:UNUSED_PAD src0_sel:WORD_1
	v_cvt_f32_f16_e32 v80, v210
	v_cvt_f32_f16_sdwa v81, v210 dst_sel:DWORD dst_unused:UNUSED_PAD src0_sel:WORD_1
	v_cvt_f32_f16_e32 v82, v211
	v_cvt_f32_f16_sdwa v83, v211 dst_sel:DWORD dst_unused:UNUSED_PAD src0_sel:WORD_1
	v_sub_f32_e32 v72, v72, v238
	v_sub_f32_e32 v73, v73, v238
	v_sub_f32_e32 v74, v74, v238
	v_sub_f32_e32 v75, v75, v238
	v_sub_f32_e32 v80, v80, v238
	v_sub_f32_e32 v81, v81, v238
	v_sub_f32_e32 v82, v82, v238
	v_sub_f32_e32 v83, v83, v238
	v_pk_mul_f32 v[72:73], v[238:239], v[72:73] op_sel:[1,0]
	v_pk_mul_f32 v[74:75], v[238:239], v[74:75] op_sel:[1,0]
	v_pk_mul_f32 v[80:81], v[238:239], v[80:81] op_sel:[1,0]
	v_pk_mul_f32 v[82:83], v[238:239], v[82:83] op_sel:[1,0]
	v_pk_fma_f32 v[144:145], v[72:73], v[160:161], v[144:145]
	v_pk_fma_f32 v[146:147], v[74:75], v[162:163], v[146:147]
	v_pk_fma_f32 v[140:141], v[80:81], v[164:165], v[140:141]
	v_pk_fma_f32 v[142:143], v[82:83], v[166:167], v[142:143]
	v_cvt_pk_f16_f32 v144, v144, v145
	v_cvt_pk_f16_f32 v145, v146, v147
	v_cvt_pk_f16_f32 v146, v140, v141
	v_cvt_pk_f16_f32 v147, v142, v143
	ds_write_b128 v235, v[144:147]
	v_fma_mix_f32 v206, v144, 1.0, 0 op_sel_hi:[1,0,0]
	v_fma_mix_f32 v207, v144, v144, 0 op_sel_hi:[1,1,0]
	v_fma_mix_f32 v206, v144, 1.0, v206 op_sel:[1,0,0] op_sel_hi:[1,0,0]
	v_fma_mix_f32 v207, v144, v144, v207 op_sel:[1,1,0] op_sel_hi:[1,1,0]
	v_fma_mix_f32 v206, v145, 1.0, v206 op_sel_hi:[1,0,0]
	v_fma_mix_f32 v207, v145, v145, v207 op_sel_hi:[1,1,0]
	v_fma_mix_f32 v206, v145, 1.0, v206 op_sel:[1,0,0] op_sel_hi:[1,0,0]
	v_fma_mix_f32 v207, v145, v145, v207 op_sel:[1,1,0] op_sel_hi:[1,1,0]
	v_fma_mix_f32 v206, v146, 1.0, v206 op_sel_hi:[1,0,0]
	v_fma_mix_f32 v207, v146, v146, v207 op_sel_hi:[1,1,0]
	v_fma_mix_f32 v206, v146, 1.0, v206 op_sel:[1,0,0] op_sel_hi:[1,0,0]
	v_fma_mix_f32 v207, v146, v146, v207 op_sel:[1,1,0] op_sel_hi:[1,1,0]
	v_fma_mix_f32 v206, v147, 1.0, v206 op_sel_hi:[1,0,0]
	v_fma_mix_f32 v207, v147, v147, v207 op_sel_hi:[1,1,0]
	v_fma_mix_f32 v206, v147, 1.0, v206 op_sel:[1,0,0] op_sel_hi:[1,0,0]
	v_fma_mix_f32 v207, v147, v147, v207 op_sel:[1,1,0] op_sel_hi:[1,1,0]
	s_waitcnt vmcnt(10)
	v_cvt_f32_f16_e32 v72, v212
	v_cvt_f32_f16_sdwa v73, v212 dst_sel:DWORD dst_unused:UNUSED_PAD src0_sel:WORD_1
	v_cvt_f32_f16_e32 v74, v213
	v_cvt_f32_f16_sdwa v75, v213 dst_sel:DWORD dst_unused:UNUSED_PAD src0_sel:WORD_1
	v_cvt_f32_f16_e32 v80, v214
	v_cvt_f32_f16_sdwa v81, v214 dst_sel:DWORD dst_unused:UNUSED_PAD src0_sel:WORD_1
	v_cvt_f32_f16_e32 v82, v215
	v_cvt_f32_f16_sdwa v83, v215 dst_sel:DWORD dst_unused:UNUSED_PAD src0_sel:WORD_1
	v_sub_f32_e32 v72, v72, v238
	v_sub_f32_e32 v73, v73, v238
	v_sub_f32_e32 v74, v74, v238
	v_sub_f32_e32 v75, v75, v238
	v_sub_f32_e32 v80, v80, v238
	v_sub_f32_e32 v81, v81, v238
	v_sub_f32_e32 v82, v82, v238
	v_sub_f32_e32 v83, v83, v238
	v_pk_mul_f32 v[72:73], v[238:239], v[72:73] op_sel:[1,0]
	v_pk_mul_f32 v[74:75], v[238:239], v[74:75] op_sel:[1,0]
	v_pk_mul_f32 v[80:81], v[238:239], v[80:81] op_sel:[1,0]
	v_pk_mul_f32 v[82:83], v[238:239], v[82:83] op_sel:[1,0]
	v_pk_fma_f32 v[132:133], v[72:73], v[168:169], v[132:133]
	v_pk_fma_f32 v[134:135], v[74:75], v[170:171], v[134:135]
	v_pk_fma_f32 v[128:129], v[80:81], v[172:173], v[128:129]
	v_pk_fma_f32 v[130:131], v[82:83], v[174:175], v[130:131]
	v_cvt_pk_f16_f32 v132, v132, v133
	v_cvt_pk_f16_f32 v133, v134, v135
	v_cvt_pk_f16_f32 v134, v128, v129
	v_cvt_pk_f16_f32 v135, v130, v131
	ds_write_b128 v235, v[132:135] offset:64
	v_fma_mix_f32 v206, v132, 1.0, v206 op_sel_hi:[1,0,0]
	v_fma_mix_f32 v207, v132, v132, v207 op_sel_hi:[1,1,0]
	v_fma_mix_f32 v206, v132, 1.0, v206 op_sel:[1,0,0] op_sel_hi:[1,0,0]
	v_fma_mix_f32 v207, v132, v132, v207 op_sel:[1,1,0] op_sel_hi:[1,1,0]
	v_fma_mix_f32 v206, v133, 1.0, v206 op_sel_hi:[1,0,0]
	v_fma_mix_f32 v207, v133, v133, v207 op_sel_hi:[1,1,0]
	v_fma_mix_f32 v206, v133, 1.0, v206 op_sel:[1,0,0] op_sel_hi:[1,0,0]
	v_fma_mix_f32 v207, v133, v133, v207 op_sel:[1,1,0] op_sel_hi:[1,1,0]
	v_fma_mix_f32 v206, v134, 1.0, v206 op_sel_hi:[1,0,0]
	v_fma_mix_f32 v207, v134, v134, v207 op_sel_hi:[1,1,0]
	v_fma_mix_f32 v206, v134, 1.0, v206 op_sel:[1,0,0] op_sel_hi:[1,0,0]
	v_fma_mix_f32 v207, v134, v134, v207 op_sel:[1,1,0] op_sel_hi:[1,1,0]
	v_fma_mix_f32 v206, v135, 1.0, v206 op_sel_hi:[1,0,0]
	v_fma_mix_f32 v207, v135, v135, v207 op_sel_hi:[1,1,0]
	v_fma_mix_f32 v206, v135, 1.0, v206 op_sel:[1,0,0] op_sel_hi:[1,0,0]
	v_fma_mix_f32 v207, v135, v135, v207 op_sel:[1,1,0] op_sel_hi:[1,1,0]
	ds_read_b128 v[88:91], v236
	ds_read_b128 v[92:95], v236 offset:1152
	s_waitcnt vmcnt(9)
	v_cvt_f32_f16_e32 v72, v216
	v_cvt_f32_f16_sdwa v73, v216 dst_sel:DWORD dst_unused:UNUSED_PAD src0_sel:WORD_1
	v_cvt_f32_f16_e32 v74, v217
	v_cvt_f32_f16_sdwa v75, v217 dst_sel:DWORD dst_unused:UNUSED_PAD src0_sel:WORD_1
	v_cvt_f32_f16_e32 v80, v218
	v_cvt_f32_f16_sdwa v81, v218 dst_sel:DWORD dst_unused:UNUSED_PAD src0_sel:WORD_1
	v_cvt_f32_f16_e32 v82, v219
	v_cvt_f32_f16_sdwa v83, v219 dst_sel:DWORD dst_unused:UNUSED_PAD src0_sel:WORD_1
	v_sub_f32_e32 v72, v72, v192
	v_sub_f32_e32 v73, v73, v192
	v_sub_f32_e32 v74, v74, v192
	v_sub_f32_e32 v75, v75, v192
	v_sub_f32_e32 v80, v80, v192
	v_sub_f32_e32 v81, v81, v192
	v_sub_f32_e32 v82, v82, v192
	v_sub_f32_e32 v83, v83, v192
	v_pk_mul_f32 v[72:73], v[192:193], v[72:73] op_sel:[1,0]
	v_pk_mul_f32 v[74:75], v[192:193], v[74:75] op_sel:[1,0]
	v_pk_mul_f32 v[80:81], v[192:193], v[80:81] op_sel:[1,0]
	v_pk_mul_f32 v[82:83], v[192:193], v[82:83] op_sel:[1,0]
	v_pk_fma_f32 v[124:125], v[72:73], v[160:161], v[124:125]
	v_pk_fma_f32 v[126:127], v[74:75], v[162:163], v[126:127]
	v_pk_fma_f32 v[120:121], v[80:81], v[164:165], v[120:121]
	v_pk_fma_f32 v[122:123], v[82:83], v[166:167], v[122:123]
	v_cvt_pk_f16_f32 v124, v124, v125
	v_cvt_pk_f16_f32 v125, v126, v127
	v_cvt_pk_f16_f32 v126, v120, v121
	v_cvt_pk_f16_f32 v127, v122, v123
	s_waitcnt lgkmcnt(0)
	buffer_store_dwordx4 v[88:91], v224, s[24:27], 0 offen nt
	v_add_u32_e32 v82, 0x3000, v224
	buffer_store_dwordx4 v[92:95], v82, s[24:27], 0 offen nt
	ds_write_b128 v235, v[124:127]
	v_fma_mix_f32 v140, v124, 1.0, 0 op_sel_hi:[1,0,0]
	v_fma_mix_f32 v141, v124, v124, 0 op_sel_hi:[1,1,0]
	v_fma_mix_f32 v140, v124, 1.0, v140 op_sel:[1,0,0] op_sel_hi:[1,0,0]
	v_fma_mix_f32 v141, v124, v124, v141 op_sel:[1,1,0] op_sel_hi:[1,1,0]
	v_fma_mix_f32 v140, v125, 1.0, v140 op_sel_hi:[1,0,0]
	v_fma_mix_f32 v141, v125, v125, v141 op_sel_hi:[1,1,0]
	v_fma_mix_f32 v140, v125, 1.0, v140 op_sel:[1,0,0] op_sel_hi:[1,0,0]
	v_fma_mix_f32 v141, v125, v125, v141 op_sel:[1,1,0] op_sel_hi:[1,1,0]
	v_fma_mix_f32 v140, v126, 1.0, v140 op_sel_hi:[1,0,0]
	v_fma_mix_f32 v141, v126, v126, v141 op_sel_hi:[1,1,0]
	v_fma_mix_f32 v140, v126, 1.0, v140 op_sel:[1,0,0] op_sel_hi:[1,0,0]
	v_fma_mix_f32 v141, v126, v126, v141 op_sel:[1,1,0] op_sel_hi:[1,1,0]
	v_fma_mix_f32 v140, v127, 1.0, v140 op_sel_hi:[1,0,0]
	v_fma_mix_f32 v141, v127, v127, v141 op_sel_hi:[1,1,0]
	v_fma_mix_f32 v140, v127, 1.0, v140 op_sel:[1,0,0] op_sel_hi:[1,0,0]
	v_fma_mix_f32 v141, v127, v127, v141 op_sel:[1,1,0] op_sel_hi:[1,1,0]
	s_waitcnt vmcnt(10)
	v_cvt_f32_f16_e32 v72, v220
	v_cvt_f32_f16_sdwa v73, v220 dst_sel:DWORD dst_unused:UNUSED_PAD src0_sel:WORD_1
	v_cvt_f32_f16_e32 v74, v221
	v_cvt_f32_f16_sdwa v75, v221 dst_sel:DWORD dst_unused:UNUSED_PAD src0_sel:WORD_1
	v_cvt_f32_f16_e32 v80, v222
	v_cvt_f32_f16_sdwa v81, v222 dst_sel:DWORD dst_unused:UNUSED_PAD src0_sel:WORD_1
	v_cvt_f32_f16_e32 v82, v223
	v_cvt_f32_f16_sdwa v83, v223 dst_sel:DWORD dst_unused:UNUSED_PAD src0_sel:WORD_1
	v_sub_f32_e32 v72, v72, v192
	v_sub_f32_e32 v73, v73, v192
	v_sub_f32_e32 v74, v74, v192
	v_sub_f32_e32 v75, v75, v192
	v_sub_f32_e32 v80, v80, v192
	v_sub_f32_e32 v81, v81, v192
	v_sub_f32_e32 v82, v82, v192
	v_sub_f32_e32 v83, v83, v192
	v_pk_mul_f32 v[72:73], v[192:193], v[72:73] op_sel:[1,0]
	v_pk_mul_f32 v[74:75], v[192:193], v[74:75] op_sel:[1,0]
	v_pk_mul_f32 v[80:81], v[192:193], v[80:81] op_sel:[1,0]
	v_pk_mul_f32 v[82:83], v[192:193], v[82:83] op_sel:[1,0]
	v_pk_fma_f32 v[116:117], v[72:73], v[168:169], v[116:117]
	v_pk_fma_f32 v[118:119], v[74:75], v[170:171], v[118:119]
	v_pk_fma_f32 v[112:113], v[80:81], v[172:173], v[112:113]
	v_pk_fma_f32 v[114:115], v[82:83], v[174:175], v[114:115]
	v_cvt_pk_f16_f32 v116, v116, v117
	v_cvt_pk_f16_f32 v117, v118, v119
	v_cvt_pk_f16_f32 v118, v112, v113
	v_cvt_pk_f16_f32 v119, v114, v115
	ds_write_b128 v235, v[116:119] offset:64
	v_fma_mix_f32 v140, v116, 1.0, v140 op_sel_hi:[1,0,0]
	v_fma_mix_f32 v141, v116, v116, v141 op_sel_hi:[1,1,0]
	v_fma_mix_f32 v140, v116, 1.0, v140 op_sel:[1,0,0] op_sel_hi:[1,0,0]
	v_fma_mix_f32 v141, v116, v116, v141 op_sel:[1,1,0] op_sel_hi:[1,1,0]
	v_fma_mix_f32 v140, v117, 1.0, v140 op_sel_hi:[1,0,0]
	v_fma_mix_f32 v141, v117, v117, v141 op_sel_hi:[1,1,0]
	v_fma_mix_f32 v140, v117, 1.0, v140 op_sel:[1,0,0] op_sel_hi:[1,0,0]
	v_fma_mix_f32 v141, v117, v117, v141 op_sel:[1,1,0] op_sel_hi:[1,1,0]
	v_fma_mix_f32 v140, v118, 1.0, v140 op_sel_hi:[1,0,0]
	v_fma_mix_f32 v141, v118, v118, v141 op_sel_hi:[1,1,0]
	v_fma_mix_f32 v140, v118, 1.0, v140 op_sel:[1,0,0] op_sel_hi:[1,0,0]
	v_fma_mix_f32 v141, v118, v118, v141 op_sel:[1,1,0] op_sel_hi:[1,1,0]
	v_fma_mix_f32 v140, v119, 1.0, v140 op_sel_hi:[1,0,0]
	v_fma_mix_f32 v141, v119, v119, v141 op_sel_hi:[1,1,0]
	v_fma_mix_f32 v140, v119, 1.0, v140 op_sel:[1,0,0] op_sel_hi:[1,0,0]
	v_fma_mix_f32 v141, v119, v119, v141 op_sel:[1,1,0] op_sel_hi:[1,1,0]
	ds_read_b128 v[208:211], v236
	ds_read_b128 v[128:131], v236 offset:1152
	s_add_u32 s94, s98, 0x3c000
	s_addc_u32 s95, s99, 0
	global_load_dwordx4 v[212:215], v191, s[94:95] offset:0 nt
	global_load_dwordx4 v[144:147], v191, s[94:95] offset:64 nt
	s_add_u32 s94, s98, 0x42000
	s_addc_u32 s95, s99, 0
	global_load_dwordx4 v[132:135], v191, s[94:95] offset:0 nt
	global_load_dwordx4 v[88:91], v191, s[94:95] offset:64 nt
	s_waitcnt vmcnt(13)
	v_cvt_f32_f16_e32 v72, v240
	v_cvt_f32_f16_sdwa v73, v240 dst_sel:DWORD dst_unused:UNUSED_PAD src0_sel:WORD_1
	v_cvt_f32_f16_e32 v74, v241
	v_cvt_f32_f16_sdwa v75, v241 dst_sel:DWORD dst_unused:UNUSED_PAD src0_sel:WORD_1
	v_cvt_f32_f16_e32 v80, v242
	v_cvt_f32_f16_sdwa v81, v242 dst_sel:DWORD dst_unused:UNUSED_PAD src0_sel:WORD_1
	v_cvt_f32_f16_e32 v82, v243
	v_cvt_f32_f16_sdwa v83, v243 dst_sel:DWORD dst_unused:UNUSED_PAD src0_sel:WORD_1
	v_sub_f32_e32 v72, v72, v194
	v_sub_f32_e32 v73, v73, v194
	v_sub_f32_e32 v74, v74, v194
	v_sub_f32_e32 v75, v75, v194
	v_sub_f32_e32 v80, v80, v194
	v_sub_f32_e32 v81, v81, v194
	v_sub_f32_e32 v82, v82, v194
	v_sub_f32_e32 v83, v83, v194
	v_pk_mul_f32 v[72:73], v[194:195], v[72:73] op_sel:[1,0]
	v_pk_mul_f32 v[74:75], v[194:195], v[74:75] op_sel:[1,0]
	v_pk_mul_f32 v[80:81], v[194:195], v[80:81] op_sel:[1,0]
	v_pk_mul_f32 v[82:83], v[194:195], v[82:83] op_sel:[1,0]
	v_pk_fma_f32 v[108:109], v[72:73], v[160:161], v[108:109]
	v_pk_fma_f32 v[110:111], v[74:75], v[162:163], v[110:111]
	v_pk_fma_f32 v[104:105], v[80:81], v[164:165], v[104:105]
	v_pk_fma_f32 v[106:107], v[82:83], v[166:167], v[106:107]
	v_cvt_pk_f16_f32 v108, v108, v109
	v_cvt_pk_f16_f32 v109, v110, v111
	v_cvt_pk_f16_f32 v110, v104, v105
	v_cvt_pk_f16_f32 v111, v106, v107
	s_waitcnt lgkmcnt(0)
	v_add_u32_e32 v83, 0x6000, v224
	buffer_store_dwordx4 v[208:211], v83, s[24:27], 0 offen nt
	v_add_u32_e32 v82, 0x9000, v224
	buffer_store_dwordx4 v[128:131], v82, s[24:27], 0 offen nt
	ds_write_b128 v235, v[108:111]
	v_fma_mix_f32 v142, v108, 1.0, 0 op_sel_hi:[1,0,0]
	v_fma_mix_f32 v143, v108, v108, 0 op_sel_hi:[1,1,0]
	v_fma_mix_f32 v142, v108, 1.0, v142 op_sel:[1,0,0] op_sel_hi:[1,0,0]
	v_fma_mix_f32 v143, v108, v108, v143 op_sel:[1,1,0] op_sel_hi:[1,1,0]
	v_fma_mix_f32 v142, v109, 1.0, v142 op_sel_hi:[1,0,0]
	v_fma_mix_f32 v143, v109, v109, v143 op_sel_hi:[1,1,0]
	v_fma_mix_f32 v142, v109, 1.0, v142 op_sel:[1,0,0] op_sel_hi:[1,0,0]
	v_fma_mix_f32 v143, v109, v109, v143 op_sel:[1,1,0] op_sel_hi:[1,1,0]
	v_fma_mix_f32 v142, v110, 1.0, v142 op_sel_hi:[1,0,0]
	v_fma_mix_f32 v143, v110, v110, v143 op_sel_hi:[1,1,0]
	v_fma_mix_f32 v142, v110, 1.0, v142 op_sel:[1,0,0] op_sel_hi:[1,0,0]
	v_fma_mix_f32 v143, v110, v110, v143 op_sel:[1,1,0] op_sel_hi:[1,1,0]
	v_fma_mix_f32 v142, v111, 1.0, v142 op_sel_hi:[1,0,0]
	v_fma_mix_f32 v143, v111, v111, v143 op_sel_hi:[1,1,0]
	v_fma_mix_f32 v142, v111, 1.0, v142 op_sel:[1,0,0] op_sel_hi:[1,0,0]
	v_fma_mix_f32 v143, v111, v111, v143 op_sel:[1,1,0] op_sel_hi:[1,1,0]
	s_waitcnt vmcnt(14)
	v_cvt_f32_f16_e32 v72, v244
	v_cvt_f32_f16_sdwa v73, v244 dst_sel:DWORD dst_unused:UNUSED_PAD src0_sel:WORD_1
	v_cvt_f32_f16_e32 v74, v245
	v_cvt_f32_f16_sdwa v75, v245 dst_sel:DWORD dst_unused:UNUSED_PAD src0_sel:WORD_1
	v_cvt_f32_f16_e32 v80, v246
	v_cvt_f32_f16_sdwa v81, v246 dst_sel:DWORD dst_unused:UNUSED_PAD src0_sel:WORD_1
	v_cvt_f32_f16_e32 v82, v247
	v_cvt_f32_f16_sdwa v83, v247 dst_sel:DWORD dst_unused:UNUSED_PAD src0_sel:WORD_1
	v_sub_f32_e32 v72, v72, v194
	v_sub_f32_e32 v73, v73, v194
	v_sub_f32_e32 v74, v74, v194
	v_sub_f32_e32 v75, v75, v194
	v_sub_f32_e32 v80, v80, v194
	v_sub_f32_e32 v81, v81, v194
	v_sub_f32_e32 v82, v82, v194
	v_sub_f32_e32 v83, v83, v194
	v_pk_mul_f32 v[72:73], v[194:195], v[72:73] op_sel:[1,0]
	v_pk_mul_f32 v[74:75], v[194:195], v[74:75] op_sel:[1,0]
	v_pk_mul_f32 v[80:81], v[194:195], v[80:81] op_sel:[1,0]
	v_pk_mul_f32 v[82:83], v[194:195], v[82:83] op_sel:[1,0]
	v_pk_fma_f32 v[100:101], v[72:73], v[168:169], v[100:101]
	v_pk_fma_f32 v[102:103], v[74:75], v[170:171], v[102:103]
	v_pk_fma_f32 v[96:97], v[80:81], v[172:173], v[96:97]
	v_pk_fma_f32 v[98:99], v[82:83], v[174:175], v[98:99]
	v_cvt_pk_f16_f32 v100, v100, v101
	v_cvt_pk_f16_f32 v101, v102, v103
	v_cvt_pk_f16_f32 v102, v96, v97
	v_cvt_pk_f16_f32 v103, v98, v99
	ds_write_b128 v235, v[100:103] offset:64
	v_fma_mix_f32 v142, v100, 1.0, v142 op_sel_hi:[1,0,0]
	v_fma_mix_f32 v143, v100, v100, v143 op_sel_hi:[1,1,0]
	v_fma_mix_f32 v142, v100, 1.0, v142 op_sel:[1,0,0] op_sel_hi:[1,0,0]
	v_fma_mix_f32 v143, v100, v100, v143 op_sel:[1,1,0] op_sel_hi:[1,1,0]
	v_fma_mix_f32 v142, v101, 1.0, v142 op_sel_hi:[1,0,0]
	v_fma_mix_f32 v143, v101, v101, v143 op_sel_hi:[1,1,0]
	v_fma_mix_f32 v142, v101, 1.0, v142 op_sel:[1,0,0] op_sel_hi:[1,0,0]
	v_fma_mix_f32 v143, v101, v101, v143 op_sel:[1,1,0] op_sel_hi:[1,1,0]
	v_fma_mix_f32 v142, v102, 1.0, v142 op_sel_hi:[1,0,0]
	v_fma_mix_f32 v143, v102, v102, v143 op_sel_hi:[1,1,0]
	v_fma_mix_f32 v142, v102, 1.0, v142 op_sel:[1,0,0] op_sel_hi:[1,0,0]
	v_fma_mix_f32 v143, v102, v102, v143 op_sel:[1,1,0] op_sel_hi:[1,1,0]
	v_fma_mix_f32 v142, v103, 1.0, v142 op_sel_hi:[1,0,0]
	v_fma_mix_f32 v143, v103, v103, v143 op_sel_hi:[1,1,0]
	v_fma_mix_f32 v142, v103, 1.0, v142 op_sel:[1,0,0] op_sel_hi:[1,0,0]
	v_fma_mix_f32 v143, v103, v103, v143 op_sel:[1,1,0] op_sel_hi:[1,1,0]
	ds_read_b128 v[92:95], v236
	ds_read_b128 v[120:123], v236 offset:1152
	s_waitcnt vmcnt(13)
	v_cvt_f32_f16_e32 v72, v248
	v_cvt_f32_f16_sdwa v73, v248 dst_sel:DWORD dst_unused:UNUSED_PAD src0_sel:WORD_1
	v_cvt_f32_f16_e32 v74, v249
	v_cvt_f32_f16_sdwa v75, v249 dst_sel:DWORD dst_unused:UNUSED_PAD src0_sel:WORD_1
	v_cvt_f32_f16_e32 v80, v250
	v_cvt_f32_f16_sdwa v81, v250 dst_sel:DWORD dst_unused:UNUSED_PAD src0_sel:WORD_1
	v_cvt_f32_f16_e32 v82, v251
	v_cvt_f32_f16_sdwa v83, v251 dst_sel:DWORD dst_unused:UNUSED_PAD src0_sel:WORD_1
	v_sub_f32_e32 v72, v72, v196
	v_sub_f32_e32 v73, v73, v196
	v_sub_f32_e32 v74, v74, v196
	v_sub_f32_e32 v75, v75, v196
	v_sub_f32_e32 v80, v80, v196
	v_sub_f32_e32 v81, v81, v196
	v_sub_f32_e32 v82, v82, v196
	v_sub_f32_e32 v83, v83, v196
	v_pk_mul_f32 v[72:73], v[196:197], v[72:73] op_sel:[1,0]
	v_pk_mul_f32 v[74:75], v[196:197], v[74:75] op_sel:[1,0]
	v_pk_mul_f32 v[80:81], v[196:197], v[80:81] op_sel:[1,0]
	v_pk_mul_f32 v[82:83], v[196:197], v[82:83] op_sel:[1,0]
	v_pk_fma_f32 v[84:85], v[72:73], v[160:161], v[84:85]
	v_pk_fma_f32 v[86:87], v[74:75], v[162:163], v[86:87]
	v_pk_fma_f32 v[76:77], v[80:81], v[164:165], v[76:77]
	v_pk_fma_f32 v[78:79], v[82:83], v[166:167], v[78:79]
	v_cvt_pk_f16_f32 v84, v84, v85
	v_cvt_pk_f16_f32 v85, v86, v87
	v_cvt_pk_f16_f32 v86, v76, v77
	v_cvt_pk_f16_f32 v87, v78, v79
	s_waitcnt lgkmcnt(0)
	v_add_u32_e32 v83, 0xc000, v224
	buffer_store_dwordx4 v[92:95], v83, s[24:27], 0 offen nt
	v_add_u32_e32 v82, 0xf000, v224
	buffer_store_dwordx4 v[120:123], v82, s[24:27], 0 offen nt
	ds_write_b128 v235, v[84:87]
	v_fma_mix_f32 v216, v84, 1.0, 0 op_sel_hi:[1,0,0]
	v_fma_mix_f32 v217, v84, v84, 0 op_sel_hi:[1,1,0]
	v_fma_mix_f32 v216, v84, 1.0, v216 op_sel:[1,0,0] op_sel_hi:[1,0,0]
	v_fma_mix_f32 v217, v84, v84, v217 op_sel:[1,1,0] op_sel_hi:[1,1,0]
	v_fma_mix_f32 v216, v85, 1.0, v216 op_sel_hi:[1,0,0]
	v_fma_mix_f32 v217, v85, v85, v217 op_sel_hi:[1,1,0]
	v_fma_mix_f32 v216, v85, 1.0, v216 op_sel:[1,0,0] op_sel_hi:[1,0,0]
	v_fma_mix_f32 v217, v85, v85, v217 op_sel:[1,1,0] op_sel_hi:[1,1,0]
	v_fma_mix_f32 v216, v86, 1.0, v216 op_sel_hi:[1,0,0]
	v_fma_mix_f32 v217, v86, v86, v217 op_sel_hi:[1,1,0]
	v_fma_mix_f32 v216, v86, 1.0, v216 op_sel:[1,0,0] op_sel_hi:[1,0,0]
	v_fma_mix_f32 v217, v86, v86, v217 op_sel:[1,1,0] op_sel_hi:[1,1,0]
	v_fma_mix_f32 v216, v87, 1.0, v216 op_sel_hi:[1,0,0]
	v_fma_mix_f32 v217, v87, v87, v217 op_sel_hi:[1,1,0]
	v_fma_mix_f32 v216, v87, 1.0, v216 op_sel:[1,0,0] op_sel_hi:[1,0,0]
	v_fma_mix_f32 v217, v87, v87, v217 op_sel:[1,1,0] op_sel_hi:[1,1,0]
	s_waitcnt vmcnt(14)
	v_cvt_f32_f16_e32 v72, v252
	v_cvt_f32_f16_sdwa v73, v252 dst_sel:DWORD dst_unused:UNUSED_PAD src0_sel:WORD_1
	v_cvt_f32_f16_e32 v74, v253
	v_cvt_f32_f16_sdwa v75, v253 dst_sel:DWORD dst_unused:UNUSED_PAD src0_sel:WORD_1
	v_cvt_f32_f16_e32 v80, v254
	v_cvt_f32_f16_sdwa v81, v254 dst_sel:DWORD dst_unused:UNUSED_PAD src0_sel:WORD_1
	v_cvt_f32_f16_e32 v82, v255
	v_cvt_f32_f16_sdwa v83, v255 dst_sel:DWORD dst_unused:UNUSED_PAD src0_sel:WORD_1
	v_sub_f32_e32 v72, v72, v196
	v_sub_f32_e32 v73, v73, v196
	v_sub_f32_e32 v74, v74, v196
	v_sub_f32_e32 v75, v75, v196
	v_sub_f32_e32 v80, v80, v196
	v_sub_f32_e32 v81, v81, v196
	v_sub_f32_e32 v82, v82, v196
	v_sub_f32_e32 v83, v83, v196
	v_pk_mul_f32 v[72:73], v[196:197], v[72:73] op_sel:[1,0]
	v_pk_mul_f32 v[74:75], v[196:197], v[74:75] op_sel:[1,0]
	v_pk_mul_f32 v[80:81], v[196:197], v[80:81] op_sel:[1,0]
	v_pk_mul_f32 v[82:83], v[196:197], v[82:83] op_sel:[1,0]
	v_pk_fma_f32 v[68:69], v[72:73], v[168:169], v[68:69]
	v_pk_fma_f32 v[70:71], v[74:75], v[170:171], v[70:71]
	v_pk_fma_f32 v[64:65], v[80:81], v[172:173], v[64:65]
	v_pk_fma_f32 v[66:67], v[82:83], v[174:175], v[66:67]
	v_cvt_pk_f16_f32 v68, v68, v69
	v_cvt_pk_f16_f32 v69, v70, v71
	v_cvt_pk_f16_f32 v70, v64, v65
	v_cvt_pk_f16_f32 v71, v66, v67
	ds_write_b128 v235, v[68:71] offset:64
	v_fma_mix_f32 v216, v68, 1.0, v216 op_sel_hi:[1,0,0]
	v_fma_mix_f32 v217, v68, v68, v217 op_sel_hi:[1,1,0]
	v_fma_mix_f32 v216, v68, 1.0, v216 op_sel:[1,0,0] op_sel_hi:[1,0,0]
	v_fma_mix_f32 v217, v68, v68, v217 op_sel:[1,1,0] op_sel_hi:[1,1,0]
	v_fma_mix_f32 v216, v69, 1.0, v216 op_sel_hi:[1,0,0]
	v_fma_mix_f32 v217, v69, v69, v217 op_sel_hi:[1,1,0]
	v_fma_mix_f32 v216, v69, 1.0, v216 op_sel:[1,0,0] op_sel_hi:[1,0,0]
	v_fma_mix_f32 v217, v69, v69, v217 op_sel:[1,1,0] op_sel_hi:[1,1,0]
	v_fma_mix_f32 v216, v70, 1.0, v216 op_sel_hi:[1,0,0]
	v_fma_mix_f32 v217, v70, v70, v217 op_sel_hi:[1,1,0]
	v_fma_mix_f32 v216, v70, 1.0, v216 op_sel:[1,0,0] op_sel_hi:[1,0,0]
	v_fma_mix_f32 v217, v70, v70, v217 op_sel:[1,1,0] op_sel_hi:[1,1,0]
	v_fma_mix_f32 v216, v71, 1.0, v216 op_sel_hi:[1,0,0]
	v_fma_mix_f32 v217, v71, v71, v217 op_sel_hi:[1,1,0]
	v_fma_mix_f32 v216, v71, 1.0, v216 op_sel:[1,0,0] op_sel_hi:[1,0,0]
	v_fma_mix_f32 v217, v71, v71, v217 op_sel:[1,1,0] op_sel_hi:[1,1,0]
	ds_read_b128 v[112:115], v236
	ds_read_b128 v[220:223], v236 offset:1152
	s_waitcnt vmcnt(13)
	v_cvt_f32_f16_e32 v72, v136
	v_cvt_f32_f16_sdwa v73, v136 dst_sel:DWORD dst_unused:UNUSED_PAD src0_sel:WORD_1
	v_cvt_f32_f16_e32 v74, v137
	v_cvt_f32_f16_sdwa v75, v137 dst_sel:DWORD dst_unused:UNUSED_PAD src0_sel:WORD_1
	v_cvt_f32_f16_e32 v80, v138
	v_cvt_f32_f16_sdwa v81, v138 dst_sel:DWORD dst_unused:UNUSED_PAD src0_sel:WORD_1
	v_cvt_f32_f16_e32 v82, v139
	v_cvt_f32_f16_sdwa v83, v139 dst_sel:DWORD dst_unused:UNUSED_PAD src0_sel:WORD_1
	v_sub_f32_e32 v72, v72, v198
	v_sub_f32_e32 v73, v73, v198
	v_sub_f32_e32 v74, v74, v198
	v_sub_f32_e32 v75, v75, v198
	v_sub_f32_e32 v80, v80, v198
	v_sub_f32_e32 v81, v81, v198
	v_sub_f32_e32 v82, v82, v198
	v_sub_f32_e32 v83, v83, v198
	v_pk_mul_f32 v[72:73], v[198:199], v[72:73] op_sel:[1,0]
	v_pk_mul_f32 v[74:75], v[198:199], v[74:75] op_sel:[1,0]
	v_pk_mul_f32 v[80:81], v[198:199], v[80:81] op_sel:[1,0]
	v_pk_mul_f32 v[82:83], v[198:199], v[82:83] op_sel:[1,0]
	v_pk_fma_f32 v[60:61], v[72:73], v[160:161], v[60:61]
	v_pk_fma_f32 v[62:63], v[74:75], v[162:163], v[62:63]
	v_pk_fma_f32 v[56:57], v[80:81], v[164:165], v[56:57]
	v_pk_fma_f32 v[58:59], v[82:83], v[166:167], v[58:59]
	v_cvt_pk_f16_f32 v60, v60, v61
	v_cvt_pk_f16_f32 v61, v62, v63
	v_cvt_pk_f16_f32 v62, v56, v57
	v_cvt_pk_f16_f32 v63, v58, v59
	s_waitcnt lgkmcnt(0)
	v_add_u32_e32 v83, 0x12000, v224
	buffer_store_dwordx4 v[112:115], v83, s[24:27], 0 offen nt
	v_add_u32_e32 v82, 0x15000, v224
	buffer_store_dwordx4 v[220:223], v82, s[24:27], 0 offen nt
	ds_write_b128 v235, v[60:63]
	v_fma_mix_f32 v218, v60, 1.0, 0 op_sel_hi:[1,0,0]
	v_fma_mix_f32 v219, v60, v60, 0 op_sel_hi:[1,1,0]
	v_fma_mix_f32 v218, v60, 1.0, v218 op_sel:[1,0,0] op_sel_hi:[1,0,0]
	v_fma_mix_f32 v219, v60, v60, v219 op_sel:[1,1,0] op_sel_hi:[1,1,0]
	v_fma_mix_f32 v218, v61, 1.0, v218 op_sel_hi:[1,0,0]
	v_fma_mix_f32 v219, v61, v61, v219 op_sel_hi:[1,1,0]
	v_fma_mix_f32 v218, v61, 1.0, v218 op_sel:[1,0,0] op_sel_hi:[1,0,0]
	v_fma_mix_f32 v219, v61, v61, v219 op_sel:[1,1,0] op_sel_hi:[1,1,0]
	v_fma_mix_f32 v218, v62, 1.0, v218 op_sel_hi:[1,0,0]
	v_fma_mix_f32 v219, v62, v62, v219 op_sel_hi:[1,1,0]
	v_fma_mix_f32 v218, v62, 1.0, v218 op_sel:[1,0,0] op_sel_hi:[1,0,0]
	v_fma_mix_f32 v219, v62, v62, v219 op_sel:[1,1,0] op_sel_hi:[1,1,0]
	v_fma_mix_f32 v218, v63, 1.0, v218 op_sel_hi:[1,0,0]
	v_fma_mix_f32 v219, v63, v63, v219 op_sel_hi:[1,1,0]
	v_fma_mix_f32 v218, v63, 1.0, v218 op_sel:[1,0,0] op_sel_hi:[1,0,0]
	v_fma_mix_f32 v219, v63, v63, v219 op_sel:[1,1,0] op_sel_hi:[1,1,0]
	s_waitcnt vmcnt(14)
	v_cvt_f32_f16_e32 v72, v148
	v_cvt_f32_f16_sdwa v73, v148 dst_sel:DWORD dst_unused:UNUSED_PAD src0_sel:WORD_1
	v_cvt_f32_f16_e32 v74, v149
	v_cvt_f32_f16_sdwa v75, v149 dst_sel:DWORD dst_unused:UNUSED_PAD src0_sel:WORD_1
	v_cvt_f32_f16_e32 v80, v150
	v_cvt_f32_f16_sdwa v81, v150 dst_sel:DWORD dst_unused:UNUSED_PAD src0_sel:WORD_1
	v_cvt_f32_f16_e32 v82, v151
	v_cvt_f32_f16_sdwa v83, v151 dst_sel:DWORD dst_unused:UNUSED_PAD src0_sel:WORD_1
	v_sub_f32_e32 v72, v72, v198
	v_sub_f32_e32 v73, v73, v198
	v_sub_f32_e32 v74, v74, v198
	v_sub_f32_e32 v75, v75, v198
	v_sub_f32_e32 v80, v80, v198
	v_sub_f32_e32 v81, v81, v198
	v_sub_f32_e32 v82, v82, v198
	v_sub_f32_e32 v83, v83, v198
	v_pk_mul_f32 v[72:73], v[198:199], v[72:73] op_sel:[1,0]
	v_pk_mul_f32 v[74:75], v[198:199], v[74:75] op_sel:[1,0]
	v_pk_mul_f32 v[80:81], v[198:199], v[80:81] op_sel:[1,0]
	v_pk_mul_f32 v[82:83], v[198:199], v[82:83] op_sel:[1,0]
	v_pk_fma_f32 v[52:53], v[72:73], v[168:169], v[52:53]
	v_pk_fma_f32 v[54:55], v[74:75], v[170:171], v[54:55]
	v_pk_fma_f32 v[48:49], v[80:81], v[172:173], v[48:49]
	v_pk_fma_f32 v[50:51], v[82:83], v[174:175], v[50:51]
	v_cvt_pk_f16_f32 v52, v52, v53
	v_cvt_pk_f16_f32 v53, v54, v55
	v_cvt_pk_f16_f32 v54, v48, v49
	v_cvt_pk_f16_f32 v55, v50, v51
	ds_write_b128 v235, v[52:55] offset:64
	v_fma_mix_f32 v218, v52, 1.0, v218 op_sel_hi:[1,0,0]
	v_fma_mix_f32 v219, v52, v52, v219 op_sel_hi:[1,1,0]
	v_fma_mix_f32 v218, v52, 1.0, v218 op_sel:[1,0,0] op_sel_hi:[1,0,0]
	v_fma_mix_f32 v219, v52, v52, v219 op_sel:[1,1,0] op_sel_hi:[1,1,0]
	v_fma_mix_f32 v218, v53, 1.0, v218 op_sel_hi:[1,0,0]
	v_fma_mix_f32 v219, v53, v53, v219 op_sel_hi:[1,1,0]
	v_fma_mix_f32 v218, v53, 1.0, v218 op_sel:[1,0,0] op_sel_hi:[1,0,0]
	v_fma_mix_f32 v219, v53, v53, v219 op_sel:[1,1,0] op_sel_hi:[1,1,0]
	v_fma_mix_f32 v218, v54, 1.0, v218 op_sel_hi:[1,0,0]
	v_fma_mix_f32 v219, v54, v54, v219 op_sel_hi:[1,1,0]
	v_fma_mix_f32 v218, v54, 1.0, v218 op_sel:[1,0,0] op_sel_hi:[1,0,0]
	v_fma_mix_f32 v219, v54, v54, v219 op_sel:[1,1,0] op_sel_hi:[1,1,0]
	v_fma_mix_f32 v218, v55, 1.0, v218 op_sel_hi:[1,0,0]
	v_fma_mix_f32 v219, v55, v55, v219 op_sel_hi:[1,1,0]
	v_fma_mix_f32 v218, v55, 1.0, v218 op_sel:[1,0,0] op_sel_hi:[1,0,0]
	v_fma_mix_f32 v219, v55, v55, v219 op_sel:[1,1,0] op_sel_hi:[1,1,0]
	ds_read_b128 v[124:127], v236
	ds_read_b128 v[116:119], v236 offset:1152
	s_waitcnt vmcnt(13)
	v_cvt_f32_f16_e32 v72, v152
	v_cvt_f32_f16_sdwa v73, v152 dst_sel:DWORD dst_unused:UNUSED_PAD src0_sel:WORD_1
	v_cvt_f32_f16_e32 v74, v153
	v_cvt_f32_f16_sdwa v75, v153 dst_sel:DWORD dst_unused:UNUSED_PAD src0_sel:WORD_1
	v_cvt_f32_f16_e32 v80, v154
	v_cvt_f32_f16_sdwa v81, v154 dst_sel:DWORD dst_unused:UNUSED_PAD src0_sel:WORD_1
	v_cvt_f32_f16_e32 v82, v155
	v_cvt_f32_f16_sdwa v83, v155 dst_sel:DWORD dst_unused:UNUSED_PAD src0_sel:WORD_1
	v_sub_f32_e32 v72, v72, v200
	v_sub_f32_e32 v73, v73, v200
	v_sub_f32_e32 v74, v74, v200
	v_sub_f32_e32 v75, v75, v200
	v_sub_f32_e32 v80, v80, v200
	v_sub_f32_e32 v81, v81, v200
	v_sub_f32_e32 v82, v82, v200
	v_sub_f32_e32 v83, v83, v200
	v_pk_mul_f32 v[72:73], v[200:201], v[72:73] op_sel:[1,0]
	v_pk_mul_f32 v[74:75], v[200:201], v[74:75] op_sel:[1,0]
	v_pk_mul_f32 v[80:81], v[200:201], v[80:81] op_sel:[1,0]
	v_pk_mul_f32 v[82:83], v[200:201], v[82:83] op_sel:[1,0]
	v_pk_fma_f32 v[44:45], v[72:73], v[160:161], v[44:45]
	v_pk_fma_f32 v[46:47], v[74:75], v[162:163], v[46:47]
	v_pk_fma_f32 v[40:41], v[80:81], v[164:165], v[40:41]
	v_pk_fma_f32 v[42:43], v[82:83], v[166:167], v[42:43]
	v_cvt_pk_f16_f32 v44, v44, v45
	v_cvt_pk_f16_f32 v45, v46, v47
	v_cvt_pk_f16_f32 v46, v40, v41
	v_cvt_pk_f16_f32 v47, v42, v43
	s_waitcnt lgkmcnt(0)
	v_add_u32_e32 v83, 0x30000, v224
	buffer_store_dwordx4 v[124:127], v83, s[24:27], 0 offen nt
	v_add_u32_e32 v82, 0x33000, v224
	buffer_store_dwordx4 v[116:119], v82, s[24:27], 0 offen nt
	ds_write_b128 v235, v[44:47]
	v_fma_mix_f32 v208, v44, 1.0, 0 op_sel_hi:[1,0,0]
	v_fma_mix_f32 v209, v44, v44, 0 op_sel_hi:[1,1,0]
	v_fma_mix_f32 v208, v44, 1.0, v208 op_sel:[1,0,0] op_sel_hi:[1,0,0]
	v_fma_mix_f32 v209, v44, v44, v209 op_sel:[1,1,0] op_sel_hi:[1,1,0]
	v_fma_mix_f32 v208, v45, 1.0, v208 op_sel_hi:[1,0,0]
	v_fma_mix_f32 v209, v45, v45, v209 op_sel_hi:[1,1,0]
	v_fma_mix_f32 v208, v45, 1.0, v208 op_sel:[1,0,0] op_sel_hi:[1,0,0]
	v_fma_mix_f32 v209, v45, v45, v209 op_sel:[1,1,0] op_sel_hi:[1,1,0]
	v_fma_mix_f32 v208, v46, 1.0, v208 op_sel_hi:[1,0,0]
	v_fma_mix_f32 v209, v46, v46, v209 op_sel_hi:[1,1,0]
	v_fma_mix_f32 v208, v46, 1.0, v208 op_sel:[1,0,0] op_sel_hi:[1,0,0]
	v_fma_mix_f32 v209, v46, v46, v209 op_sel:[1,1,0] op_sel_hi:[1,1,0]
	v_fma_mix_f32 v208, v47, 1.0, v208 op_sel_hi:[1,0,0]
	v_fma_mix_f32 v209, v47, v47, v209 op_sel_hi:[1,1,0]
	v_fma_mix_f32 v208, v47, 1.0, v208 op_sel:[1,0,0] op_sel_hi:[1,0,0]
	v_fma_mix_f32 v209, v47, v47, v209 op_sel:[1,1,0] op_sel_hi:[1,1,0]
	s_waitcnt vmcnt(14)
	v_cvt_f32_f16_e32 v72, v156
	v_cvt_f32_f16_sdwa v73, v156 dst_sel:DWORD dst_unused:UNUSED_PAD src0_sel:WORD_1
	v_cvt_f32_f16_e32 v74, v157
	v_cvt_f32_f16_sdwa v75, v157 dst_sel:DWORD dst_unused:UNUSED_PAD src0_sel:WORD_1
	v_cvt_f32_f16_e32 v80, v158
	v_cvt_f32_f16_sdwa v81, v158 dst_sel:DWORD dst_unused:UNUSED_PAD src0_sel:WORD_1
	v_cvt_f32_f16_e32 v82, v159
	v_cvt_f32_f16_sdwa v83, v159 dst_sel:DWORD dst_unused:UNUSED_PAD src0_sel:WORD_1
	v_sub_f32_e32 v72, v72, v200
	v_sub_f32_e32 v73, v73, v200
	v_sub_f32_e32 v74, v74, v200
	v_sub_f32_e32 v75, v75, v200
	v_sub_f32_e32 v80, v80, v200
	v_sub_f32_e32 v81, v81, v200
	v_sub_f32_e32 v82, v82, v200
	v_sub_f32_e32 v83, v83, v200
	v_pk_mul_f32 v[72:73], v[200:201], v[72:73] op_sel:[1,0]
	v_pk_mul_f32 v[74:75], v[200:201], v[74:75] op_sel:[1,0]
	v_pk_mul_f32 v[80:81], v[200:201], v[80:81] op_sel:[1,0]
	v_pk_mul_f32 v[82:83], v[200:201], v[82:83] op_sel:[1,0]
	v_pk_fma_f32 v[36:37], v[72:73], v[168:169], v[36:37]
	v_pk_fma_f32 v[38:39], v[74:75], v[170:171], v[38:39]
	v_pk_fma_f32 v[32:33], v[80:81], v[172:173], v[32:33]
	v_pk_fma_f32 v[34:35], v[82:83], v[174:175], v[34:35]
	v_cvt_pk_f16_f32 v36, v36, v37
	v_cvt_pk_f16_f32 v37, v38, v39
	v_cvt_pk_f16_f32 v38, v32, v33
	v_cvt_pk_f16_f32 v39, v34, v35
	ds_write_b128 v235, v[36:39] offset:64
	v_fma_mix_f32 v208, v36, 1.0, v208 op_sel_hi:[1,0,0]
	v_fma_mix_f32 v209, v36, v36, v209 op_sel_hi:[1,1,0]
	v_fma_mix_f32 v208, v36, 1.0, v208 op_sel:[1,0,0] op_sel_hi:[1,0,0]
	v_fma_mix_f32 v209, v36, v36, v209 op_sel:[1,1,0] op_sel_hi:[1,1,0]
	v_fma_mix_f32 v208, v37, 1.0, v208 op_sel_hi:[1,0,0]
	v_fma_mix_f32 v209, v37, v37, v209 op_sel_hi:[1,1,0]
	v_fma_mix_f32 v208, v37, 1.0, v208 op_sel:[1,0,0] op_sel_hi:[1,0,0]
	v_fma_mix_f32 v209, v37, v37, v209 op_sel:[1,1,0] op_sel_hi:[1,1,0]
	v_fma_mix_f32 v208, v38, 1.0, v208 op_sel_hi:[1,0,0]
	v_fma_mix_f32 v209, v38, v38, v209 op_sel_hi:[1,1,0]
	v_fma_mix_f32 v208, v38, 1.0, v208 op_sel:[1,0,0] op_sel_hi:[1,0,0]
	v_fma_mix_f32 v209, v38, v38, v209 op_sel:[1,1,0] op_sel_hi:[1,1,0]
	v_fma_mix_f32 v208, v39, 1.0, v208 op_sel_hi:[1,0,0]
	v_fma_mix_f32 v209, v39, v39, v209 op_sel_hi:[1,1,0]
	v_fma_mix_f32 v208, v39, 1.0, v208 op_sel:[1,0,0] op_sel_hi:[1,0,0]
	v_fma_mix_f32 v209, v39, v39, v209 op_sel:[1,1,0] op_sel_hi:[1,1,0]
	ds_read_b128 v[128:131], v236
	ds_read_b128 v[104:107], v236 offset:1152
	s_waitcnt vmcnt(11)
	v_cvt_f32_f16_e32 v72, v212
	v_cvt_f32_f16_sdwa v73, v212 dst_sel:DWORD dst_unused:UNUSED_PAD src0_sel:WORD_1
	v_cvt_f32_f16_e32 v74, v213
	v_cvt_f32_f16_sdwa v75, v213 dst_sel:DWORD dst_unused:UNUSED_PAD src0_sel:WORD_1
	v_cvt_f32_f16_e32 v80, v214
	v_cvt_f32_f16_sdwa v81, v214 dst_sel:DWORD dst_unused:UNUSED_PAD src0_sel:WORD_1
	v_cvt_f32_f16_e32 v82, v215
	v_cvt_f32_f16_sdwa v83, v215 dst_sel:DWORD dst_unused:UNUSED_PAD src0_sel:WORD_1
	v_sub_f32_e32 v72, v72, v202
	v_sub_f32_e32 v73, v73, v202
	v_sub_f32_e32 v74, v74, v202
	v_sub_f32_e32 v75, v75, v202
	v_sub_f32_e32 v80, v80, v202
	v_sub_f32_e32 v81, v81, v202
	v_sub_f32_e32 v82, v82, v202
	v_sub_f32_e32 v83, v83, v202
	v_pk_mul_f32 v[72:73], v[202:203], v[72:73] op_sel:[1,0]
	v_pk_mul_f32 v[74:75], v[202:203], v[74:75] op_sel:[1,0]
	v_pk_mul_f32 v[80:81], v[202:203], v[80:81] op_sel:[1,0]
	v_pk_mul_f32 v[82:83], v[202:203], v[82:83] op_sel:[1,0]
	v_pk_fma_f32 v[28:29], v[72:73], v[160:161], v[28:29]
	v_pk_fma_f32 v[30:31], v[74:75], v[162:163], v[30:31]
	v_pk_fma_f32 v[24:25], v[80:81], v[164:165], v[24:25]
	v_pk_fma_f32 v[26:27], v[82:83], v[166:167], v[26:27]
	v_cvt_pk_f16_f32 v28, v28, v29
	v_cvt_pk_f16_f32 v29, v30, v31
	v_cvt_pk_f16_f32 v30, v24, v25
	v_cvt_pk_f16_f32 v31, v26, v27
	s_waitcnt lgkmcnt(0)
	v_add_u32_e32 v83, 0x36000, v224
	buffer_store_dwordx4 v[128:131], v83, s[24:27], 0 offen nt
	v_add_u32_e32 v82, 0x39000, v224
	buffer_store_dwordx4 v[104:107], v82, s[24:27], 0 offen nt
	ds_write_b128 v235, v[28:31]
	v_fma_mix_f32 v210, v28, 1.0, 0 op_sel_hi:[1,0,0]
	v_fma_mix_f32 v211, v28, v28, 0 op_sel_hi:[1,1,0]
	v_fma_mix_f32 v210, v28, 1.0, v210 op_sel:[1,0,0] op_sel_hi:[1,0,0]
	v_fma_mix_f32 v211, v28, v28, v211 op_sel:[1,1,0] op_sel_hi:[1,1,0]
	v_fma_mix_f32 v210, v29, 1.0, v210 op_sel_hi:[1,0,0]
	v_fma_mix_f32 v211, v29, v29, v211 op_sel_hi:[1,1,0]
	v_fma_mix_f32 v210, v29, 1.0, v210 op_sel:[1,0,0] op_sel_hi:[1,0,0]
	v_fma_mix_f32 v211, v29, v29, v211 op_sel:[1,1,0] op_sel_hi:[1,1,0]
	v_fma_mix_f32 v210, v30, 1.0, v210 op_sel_hi:[1,0,0]
	v_fma_mix_f32 v211, v30, v30, v211 op_sel_hi:[1,1,0]
	v_fma_mix_f32 v210, v30, 1.0, v210 op_sel:[1,0,0] op_sel_hi:[1,0,0]
	v_fma_mix_f32 v211, v30, v30, v211 op_sel:[1,1,0] op_sel_hi:[1,1,0]
	v_fma_mix_f32 v210, v31, 1.0, v210 op_sel_hi:[1,0,0]
	v_fma_mix_f32 v211, v31, v31, v211 op_sel_hi:[1,1,0]
	v_fma_mix_f32 v210, v31, 1.0, v210 op_sel:[1,0,0] op_sel_hi:[1,0,0]
	v_fma_mix_f32 v211, v31, v31, v211 op_sel:[1,1,0] op_sel_hi:[1,1,0]
	s_waitcnt vmcnt(12)
	v_cvt_f32_f16_e32 v72, v144
	v_cvt_f32_f16_sdwa v73, v144 dst_sel:DWORD dst_unused:UNUSED_PAD src0_sel:WORD_1
	v_cvt_f32_f16_e32 v74, v145
	v_cvt_f32_f16_sdwa v75, v145 dst_sel:DWORD dst_unused:UNUSED_PAD src0_sel:WORD_1
	v_cvt_f32_f16_e32 v80, v146
	v_cvt_f32_f16_sdwa v81, v146 dst_sel:DWORD dst_unused:UNUSED_PAD src0_sel:WORD_1
	v_cvt_f32_f16_e32 v82, v147
	v_cvt_f32_f16_sdwa v83, v147 dst_sel:DWORD dst_unused:UNUSED_PAD src0_sel:WORD_1
	v_sub_f32_e32 v72, v72, v202
	v_sub_f32_e32 v73, v73, v202
	v_sub_f32_e32 v74, v74, v202
	v_sub_f32_e32 v75, v75, v202
	v_sub_f32_e32 v80, v80, v202
	v_sub_f32_e32 v81, v81, v202
	v_sub_f32_e32 v82, v82, v202
	v_sub_f32_e32 v83, v83, v202
	v_pk_mul_f32 v[72:73], v[202:203], v[72:73] op_sel:[1,0]
	v_pk_mul_f32 v[74:75], v[202:203], v[74:75] op_sel:[1,0]
	v_pk_mul_f32 v[80:81], v[202:203], v[80:81] op_sel:[1,0]
	v_pk_mul_f32 v[82:83], v[202:203], v[82:83] op_sel:[1,0]
	v_pk_fma_f32 v[20:21], v[72:73], v[168:169], v[20:21]
	v_pk_fma_f32 v[22:23], v[74:75], v[170:171], v[22:23]
	v_pk_fma_f32 v[16:17], v[80:81], v[172:173], v[16:17]
	v_pk_fma_f32 v[18:19], v[82:83], v[174:175], v[18:19]
	v_cvt_pk_f16_f32 v20, v20, v21
	v_cvt_pk_f16_f32 v21, v22, v23
	v_cvt_pk_f16_f32 v22, v16, v17
	v_cvt_pk_f16_f32 v23, v18, v19
	ds_write_b128 v235, v[20:23] offset:64
	v_fma_mix_f32 v210, v20, 1.0, v210 op_sel_hi:[1,0,0]
	v_fma_mix_f32 v211, v20, v20, v211 op_sel_hi:[1,1,0]
	v_fma_mix_f32 v210, v20, 1.0, v210 op_sel:[1,0,0] op_sel_hi:[1,0,0]
	v_fma_mix_f32 v211, v20, v20, v211 op_sel:[1,1,0] op_sel_hi:[1,1,0]
	v_fma_mix_f32 v210, v21, 1.0, v210 op_sel_hi:[1,0,0]
	v_fma_mix_f32 v211, v21, v21, v211 op_sel_hi:[1,1,0]
	v_fma_mix_f32 v210, v21, 1.0, v210 op_sel:[1,0,0] op_sel_hi:[1,0,0]
	v_fma_mix_f32 v211, v21, v21, v211 op_sel:[1,1,0] op_sel_hi:[1,1,0]
	v_fma_mix_f32 v210, v22, 1.0, v210 op_sel_hi:[1,0,0]
	v_fma_mix_f32 v211, v22, v22, v211 op_sel_hi:[1,1,0]
	v_fma_mix_f32 v210, v22, 1.0, v210 op_sel:[1,0,0] op_sel_hi:[1,0,0]
	v_fma_mix_f32 v211, v22, v22, v211 op_sel:[1,1,0] op_sel_hi:[1,1,0]
	v_fma_mix_f32 v210, v23, 1.0, v210 op_sel_hi:[1,0,0]
	v_fma_mix_f32 v211, v23, v23, v211 op_sel_hi:[1,1,0]
	v_fma_mix_f32 v210, v23, 1.0, v210 op_sel:[1,0,0] op_sel_hi:[1,0,0]
	v_fma_mix_f32 v211, v23, v23, v211 op_sel:[1,1,0] op_sel_hi:[1,1,0]
	ds_read_b128 v[240:243], v236
	ds_read_b128 v[96:99], v236 offset:1152
	s_waitcnt vmcnt(11)
	v_cvt_f32_f16_e32 v72, v132
	v_cvt_f32_f16_sdwa v73, v132 dst_sel:DWORD dst_unused:UNUSED_PAD src0_sel:WORD_1
	v_cvt_f32_f16_e32 v74, v133
	v_cvt_f32_f16_sdwa v75, v133 dst_sel:DWORD dst_unused:UNUSED_PAD src0_sel:WORD_1
	v_cvt_f32_f16_e32 v80, v134
	v_cvt_f32_f16_sdwa v81, v134 dst_sel:DWORD dst_unused:UNUSED_PAD src0_sel:WORD_1
	v_cvt_f32_f16_e32 v82, v135
	v_cvt_f32_f16_sdwa v83, v135 dst_sel:DWORD dst_unused:UNUSED_PAD src0_sel:WORD_1
	v_sub_f32_e32 v72, v72, v204
	v_sub_f32_e32 v73, v73, v204
	v_sub_f32_e32 v74, v74, v204
	v_sub_f32_e32 v75, v75, v204
	v_sub_f32_e32 v80, v80, v204
	v_sub_f32_e32 v81, v81, v204
	v_sub_f32_e32 v82, v82, v204
	v_sub_f32_e32 v83, v83, v204
	v_pk_mul_f32 v[72:73], v[204:205], v[72:73] op_sel:[1,0]
	v_pk_mul_f32 v[74:75], v[204:205], v[74:75] op_sel:[1,0]
	v_pk_mul_f32 v[80:81], v[204:205], v[80:81] op_sel:[1,0]
	v_pk_mul_f32 v[82:83], v[204:205], v[82:83] op_sel:[1,0]
	v_pk_fma_f32 v[12:13], v[72:73], v[160:161], v[12:13]
	v_pk_fma_f32 v[14:15], v[74:75], v[162:163], v[14:15]
	v_pk_fma_f32 v[8:9], v[80:81], v[164:165], v[8:9]
	v_pk_fma_f32 v[10:11], v[82:83], v[166:167], v[10:11]
	v_cvt_pk_f16_f32 v12, v12, v13
	v_cvt_pk_f16_f32 v13, v14, v15
	v_cvt_pk_f16_f32 v14, v8, v9
	v_cvt_pk_f16_f32 v15, v10, v11
	s_waitcnt lgkmcnt(0)
	v_add_u32_e32 v83, 0x3c000, v224
	buffer_store_dwordx4 v[240:243], v83, s[24:27], 0 offen nt
	v_add_u32_e32 v82, 0x3f000, v224
	buffer_store_dwordx4 v[96:99], v82, s[24:27], 0 offen nt
	ds_write_b128 v235, v[12:15]
	v_fma_mix_f32 v244, v12, 1.0, 0 op_sel_hi:[1,0,0]
	v_fma_mix_f32 v245, v12, v12, 0 op_sel_hi:[1,1,0]
	v_fma_mix_f32 v244, v12, 1.0, v244 op_sel:[1,0,0] op_sel_hi:[1,0,0]
	v_fma_mix_f32 v245, v12, v12, v245 op_sel:[1,1,0] op_sel_hi:[1,1,0]
	v_fma_mix_f32 v244, v13, 1.0, v244 op_sel_hi:[1,0,0]
	v_fma_mix_f32 v245, v13, v13, v245 op_sel_hi:[1,1,0]
	v_fma_mix_f32 v244, v13, 1.0, v244 op_sel:[1,0,0] op_sel_hi:[1,0,0]
	v_fma_mix_f32 v245, v13, v13, v245 op_sel:[1,1,0] op_sel_hi:[1,1,0]
	v_fma_mix_f32 v244, v14, 1.0, v244 op_sel_hi:[1,0,0]
	v_fma_mix_f32 v245, v14, v14, v245 op_sel_hi:[1,1,0]
	v_fma_mix_f32 v244, v14, 1.0, v244 op_sel:[1,0,0] op_sel_hi:[1,0,0]
	v_fma_mix_f32 v245, v14, v14, v245 op_sel:[1,1,0] op_sel_hi:[1,1,0]
	v_fma_mix_f32 v244, v15, 1.0, v244 op_sel_hi:[1,0,0]
	v_fma_mix_f32 v245, v15, v15, v245 op_sel_hi:[1,1,0]
	v_fma_mix_f32 v244, v15, 1.0, v244 op_sel:[1,0,0] op_sel_hi:[1,0,0]
	v_fma_mix_f32 v245, v15, v15, v245 op_sel:[1,1,0] op_sel_hi:[1,1,0]
	s_waitcnt vmcnt(12)
	v_cvt_f32_f16_e32 v72, v88
	v_cvt_f32_f16_sdwa v73, v88 dst_sel:DWORD dst_unused:UNUSED_PAD src0_sel:WORD_1
	v_cvt_f32_f16_e32 v74, v89
	v_cvt_f32_f16_sdwa v75, v89 dst_sel:DWORD dst_unused:UNUSED_PAD src0_sel:WORD_1
	v_cvt_f32_f16_e32 v80, v90
	v_cvt_f32_f16_sdwa v81, v90 dst_sel:DWORD dst_unused:UNUSED_PAD src0_sel:WORD_1
	v_cvt_f32_f16_e32 v82, v91
	v_cvt_f32_f16_sdwa v83, v91 dst_sel:DWORD dst_unused:UNUSED_PAD src0_sel:WORD_1
	v_sub_f32_e32 v72, v72, v204
	v_sub_f32_e32 v73, v73, v204
	v_sub_f32_e32 v74, v74, v204
	v_sub_f32_e32 v75, v75, v204
	v_sub_f32_e32 v80, v80, v204
	v_sub_f32_e32 v81, v81, v204
	v_sub_f32_e32 v82, v82, v204
	v_sub_f32_e32 v83, v83, v204
	v_pk_mul_f32 v[72:73], v[204:205], v[72:73] op_sel:[1,0]
	v_pk_mul_f32 v[74:75], v[204:205], v[74:75] op_sel:[1,0]
	v_pk_mul_f32 v[80:81], v[204:205], v[80:81] op_sel:[1,0]
	v_pk_mul_f32 v[82:83], v[204:205], v[82:83] op_sel:[1,0]
	v_pk_fma_f32 v[4:5], v[72:73], v[168:169], v[4:5]
	v_pk_fma_f32 v[6:7], v[74:75], v[170:171], v[6:7]
	v_pk_fma_f32 v[0:1], v[80:81], v[172:173], v[0:1]
	v_pk_fma_f32 v[2:3], v[82:83], v[174:175], v[2:3]
	v_cvt_pk_f16_f32 v4, v4, v5
	v_cvt_pk_f16_f32 v5, v6, v7
	v_cvt_pk_f16_f32 v6, v0, v1
	v_cvt_pk_f16_f32 v7, v2, v3
	ds_write_b128 v235, v[4:7] offset:64
	v_fma_mix_f32 v244, v4, 1.0, v244 op_sel_hi:[1,0,0]
	v_fma_mix_f32 v245, v4, v4, v245 op_sel_hi:[1,1,0]
	v_fma_mix_f32 v244, v4, 1.0, v244 op_sel:[1,0,0] op_sel_hi:[1,0,0]
	v_fma_mix_f32 v245, v4, v4, v245 op_sel:[1,1,0] op_sel_hi:[1,1,0]
	v_fma_mix_f32 v244, v5, 1.0, v244 op_sel_hi:[1,0,0]
	v_fma_mix_f32 v245, v5, v5, v245 op_sel_hi:[1,1,0]
	v_fma_mix_f32 v244, v5, 1.0, v244 op_sel:[1,0,0] op_sel_hi:[1,0,0]
	v_fma_mix_f32 v245, v5, v5, v245 op_sel:[1,1,0] op_sel_hi:[1,1,0]
	v_fma_mix_f32 v244, v6, 1.0, v244 op_sel_hi:[1,0,0]
	v_fma_mix_f32 v245, v6, v6, v245 op_sel_hi:[1,1,0]
	v_fma_mix_f32 v244, v6, 1.0, v244 op_sel:[1,0,0] op_sel_hi:[1,0,0]
	v_fma_mix_f32 v245, v6, v6, v245 op_sel:[1,1,0] op_sel_hi:[1,1,0]
	v_fma_mix_f32 v244, v7, 1.0, v244 op_sel_hi:[1,0,0]
	v_fma_mix_f32 v245, v7, v7, v245 op_sel_hi:[1,1,0]
	v_fma_mix_f32 v244, v7, 1.0, v244 op_sel:[1,0,0] op_sel_hi:[1,0,0]
	v_fma_mix_f32 v245, v7, v7, v245 op_sel:[1,1,0] op_sel_hi:[1,1,0]
	ds_read_b128 v[108:111], v236
	ds_read_b128 v[100:103], v236 offset:1152
	s_waitcnt lgkmcnt(0)
	v_add_u32_e32 v83, 0x42000, v224
	buffer_store_dwordx4 v[108:111], v83, s[24:27], 0 offen nt
	v_add_u32_e32 v82, 0x45000, v224
	buffer_store_dwordx4 v[100:103], v82, s[24:27], 0 offen nt
	v_xor_b32_e32 v225, 16, v234
	v_lshlrev_b32_e32 v225, 2, v225
	v_xor_b32_e32 v246, 32, v234
	v_lshlrev_b32_e32 v246, 2, v246
	ds_bpermute_b32 v92, v225, v206
	ds_bpermute_b32 v93, v225, v207
	ds_bpermute_b32 v94, v225, v140
	ds_bpermute_b32 v95, v225, v141
	ds_bpermute_b32 v120, v225, v142
	ds_bpermute_b32 v121, v225, v143
	ds_bpermute_b32 v122, v225, v216
	ds_bpermute_b32 v123, v225, v217
	s_waitcnt lgkmcnt(0)
	v_pk_add_f32 v[206:207], v[206:207], v[92:93]
	v_pk_add_f32 v[140:141], v[140:141], v[94:95]
	v_pk_add_f32 v[142:143], v[142:143], v[120:121]
	v_pk_add_f32 v[216:217], v[216:217], v[122:123]
	ds_bpermute_b32 v92, v225, v218
	ds_bpermute_b32 v93, v225, v219
	ds_bpermute_b32 v94, v225, v208
	ds_bpermute_b32 v95, v225, v209
	ds_bpermute_b32 v120, v225, v210
	ds_bpermute_b32 v121, v225, v211
	ds_bpermute_b32 v122, v225, v244
	ds_bpermute_b32 v123, v225, v245
	s_waitcnt lgkmcnt(0)
	v_pk_add_f32 v[218:219], v[218:219], v[92:93]
	v_pk_add_f32 v[208:209], v[208:209], v[94:95]
	v_pk_add_f32 v[210:211], v[210:211], v[120:121]
	v_pk_add_f32 v[244:245], v[244:245], v[122:123]
	ds_bpermute_b32 v92, v246, v206
	ds_bpermute_b32 v93, v246, v207
	ds_bpermute_b32 v94, v246, v140
	ds_bpermute_b32 v95, v246, v141
	ds_bpermute_b32 v120, v246, v142
	ds_bpermute_b32 v121, v246, v143
	ds_bpermute_b32 v122, v246, v216
	ds_bpermute_b32 v123, v246, v217
	s_waitcnt lgkmcnt(0)
	v_pk_add_f32 v[206:207], v[206:207], v[92:93]
	v_pk_add_f32 v[140:141], v[140:141], v[94:95]
	v_pk_add_f32 v[142:143], v[142:143], v[120:121]
	v_pk_add_f32 v[216:217], v[216:217], v[122:123]
	ds_bpermute_b32 v92, v246, v218
	ds_bpermute_b32 v93, v246, v219
	ds_bpermute_b32 v94, v246, v208
	ds_bpermute_b32 v95, v246, v209
	ds_bpermute_b32 v120, v246, v210
	ds_bpermute_b32 v121, v246, v211
	ds_bpermute_b32 v122, v246, v244
	ds_bpermute_b32 v123, v246, v245
	s_waitcnt lgkmcnt(0)
	v_pk_add_f32 v[218:219], v[218:219], v[92:93]
	v_pk_add_f32 v[208:209], v[208:209], v[94:95]
	v_pk_add_f32 v[210:211], v[210:211], v[120:121]
	v_pk_add_f32 v[244:245], v[244:245], v[122:123]
	s_mov_b64 exec, 0xffff
	global_store_dwordx2 v190, v[206:207], s[100:101] offset:0
	global_store_dwordx2 v190, v[140:141], s[100:101] offset:128
	global_store_dwordx2 v190, v[142:143], s[100:101] offset:256
	global_store_dwordx2 v190, v[216:217], s[100:101] offset:384
	global_store_dwordx2 v190, v[218:219], s[100:101] offset:1024
	global_store_dwordx2 v190, v[208:209], s[100:101] offset:1152
	global_store_dwordx2 v190, v[210:211], s[100:101] offset:1280
	global_store_dwordx2 v190, v[244:245], s[100:101] offset:1408
	s_mov_b64 exec, -1
	s_mov_b32 s83, s81
	s_mov_b32 s84, s82
	s_mov_b64 s[40:41], s[0:1]
	s_mov_b64 s[38:39], s[8:9]
	s_mov_b64 vcc, s[6:7]
	s_cbranch_vccz .LBB8_12
	s_waitcnt vmcnt(0)
	s_cmpk_gt_u32 s44, 0xff
	s_cbranch_scc1 .LBB8_31
	s_barrier

.LBB10_27:
	ds_read_b128 v[72:75], v231
	ds_read_b128 v[80:83], v231 offset:1024
	ds_read_b128 v[88:91], v231 offset:2048
	ds_read_b128 v[92:95], v231 offset:3072
	s_add_u32 s40, s38, 0xfff40080
	s_addc_u32 s41, s39, -1
	s_cmp_eq_u32 s87, 44
	s_cselect_b32 s43, s9, s41
	s_cselect_b32 s42, s8, s40
	s_cselect_b32 s41, s1, s86
	s_cselect_b32 s40, s0, s85
	v_lshl_add_u64 v[190:191], s[38:39], 0, v[184:185]
	s_add_i32 m0, s51, 0xc000
	ds_read_b128 v[136:139], v232
	ds_read_b128 v[148:151], v232 offset:1024
	ds_read_b128 v[152:155], v232 offset:2048
	ds_read_b128 v[156:159], v232 offset:3072
	ds_read_b128 v[160:163], v232 offset:4096
	ds_read_b128 v[164:167], v232 offset:5120
	ds_read_b128 v[168:171], v232 offset:6144
	ds_read_b128 v[172:175], v232 offset:7168
	global_load_lds_dwordx4 v[190:191], off
	v_lshl_add_u64 v[190:191], s[38:39], 0, v[186:187]
	s_add_i32 m0, s51, 0xe000
	s_nop 0
	global_load_lds_dwordx4 v[190:191], off
	s_waitcnt lgkmcnt(8)
	s_barrier
	s_waitcnt lgkmcnt(0)
	s_setprio 1
	s_waitcnt lgkmcnt(0)
	v_mfma_f32_16x16x32_f16 v[144:147], v[72:75], v[136:139], v[144:147]
	v_mfma_f32_16x16x32_f16 v[140:143], v[88:91], v[136:139], v[140:143]
	v_mfma_f32_16x16x32_f16 v[124:127], v[72:75], v[152:155], v[124:127]
	v_mfma_f32_16x16x32_f16 v[120:123], v[88:91], v[152:155], v[120:123]
	v_mfma_f32_16x16x32_f16 v[108:111], v[72:75], v[160:163], v[108:111]
	v_mfma_f32_16x16x32_f16 v[104:107], v[88:91], v[160:163], v[104:107]
	v_mfma_f32_16x16x32_f16 v[84:87], v[72:75], v[168:171], v[84:87]
	v_mfma_f32_16x16x32_f16 v[76:79], v[88:91], v[168:171], v[76:79]
	v_mfma_f32_16x16x32_f16 v[144:147], v[80:83], v[148:151], v[144:147]
	v_mfma_f32_16x16x32_f16 v[140:143], v[92:95], v[148:151], v[140:143]
	v_mfma_f32_16x16x32_f16 v[124:127], v[80:83], v[156:159], v[124:127]
	v_mfma_f32_16x16x32_f16 v[120:123], v[92:95], v[156:159], v[120:123]
	v_mfma_f32_16x16x32_f16 v[108:111], v[80:83], v[164:167], v[108:111]
	v_mfma_f32_16x16x32_f16 v[104:107], v[92:95], v[164:167], v[104:107]
	v_mfma_f32_16x16x32_f16 v[84:87], v[80:83], v[172:175], v[84:87]
	v_mfma_f32_16x16x32_f16 v[76:79], v[92:95], v[172:175], v[76:79]
	s_setprio 0
	s_barrier
	s_add_i32 s88, s69, s50
	v_lshl_add_u64 v[206:207], s[40:41], 0, v[178:179]
	s_mov_b32 m0, s88
	ds_read_b128 v[190:193], v233
	ds_read_b128 v[194:197], v233 offset:1024
	ds_read_b128 v[198:201], v233 offset:2048
	ds_read_b128 v[202:205], v233 offset:3072
	global_load_lds_dwordx4 v[206:207], off
	v_lshl_add_u64 v[208:209], s[40:41], 0, v[182:183]
	s_add_i32 m0, s88, 0x2000
	s_nop 0
	global_load_lds_dwordx4 v[208:209], off
	s_barrier
	s_waitcnt lgkmcnt(0)
	s_setprio 1
	s_waitcnt lgkmcnt(0)
	v_mfma_f32_16x16x32_f16 v[132:135], v[190:193], v[136:139], v[132:135]
	v_mfma_f32_16x16x32_f16 v[128:131], v[198:201], v[136:139], v[128:131]
	v_mfma_f32_16x16x32_f16 v[116:119], v[190:193], v[152:155], v[116:119]
	v_mfma_f32_16x16x32_f16 v[112:115], v[198:201], v[152:155], v[112:115]
	v_mfma_f32_16x16x32_f16 v[100:103], v[190:193], v[160:163], v[100:103]
	v_mfma_f32_16x16x32_f16 v[96:99], v[198:201], v[160:163], v[96:99]
	v_mfma_f32_16x16x32_f16 v[68:71], v[190:193], v[168:171], v[68:71]
	v_mfma_f32_16x16x32_f16 v[64:67], v[198:201], v[168:171], v[64:67]
	v_mfma_f32_16x16x32_f16 v[132:135], v[194:197], v[148:151], v[132:135]
	v_mfma_f32_16x16x32_f16 v[128:131], v[202:205], v[148:151], v[128:131]
	v_mfma_f32_16x16x32_f16 v[116:119], v[194:197], v[156:159], v[116:119]
	v_mfma_f32_16x16x32_f16 v[112:115], v[202:205], v[156:159], v[112:115]
	v_mfma_f32_16x16x32_f16 v[100:103], v[194:197], v[164:167], v[100:103]
	v_mfma_f32_16x16x32_f16 v[96:99], v[202:205], v[164:167], v[96:99]
	v_mfma_f32_16x16x32_f16 v[68:71], v[194:197], v[172:175], v[68:71]
	v_mfma_f32_16x16x32_f16 v[64:67], v[202:205], v[172:175], v[64:67]
	s_setprio 0
	s_mov_b32 m0, s51
	v_lshl_add_u64 v[210:211], s[42:43], 0, v[176:177]
	s_barrier
	ds_read_b128 v[136:139], v232 offset:16384
	ds_read_b128 v[148:151], v232 offset:17408
	ds_read_b128 v[152:155], v232 offset:18432
	ds_read_b128 v[156:159], v232 offset:19456
	ds_read_b128 v[160:163], v232 offset:20480
	ds_read_b128 v[164:167], v232 offset:21504
	ds_read_b128 v[168:171], v232 offset:22528
	ds_read_b128 v[172:175], v232 offset:23552
	global_load_lds_dwordx4 v[210:211], off
	v_lshl_add_u64 v[212:213], s[42:43], 0, v[180:181]
	s_mov_b32 m0, s52
	s_nop 0
	global_load_lds_dwordx4 v[212:213], off
	s_barrier
	s_waitcnt lgkmcnt(0)
	s_setprio 1
	s_waitcnt lgkmcnt(0)
	v_mfma_f32_16x16x32_f16 v[60:63], v[72:75], v[136:139], v[60:63]
	v_mfma_f32_16x16x32_f16 v[56:59], v[88:91], v[136:139], v[56:59]
	v_mfma_f32_16x16x32_f16 v[44:47], v[72:75], v[152:155], v[44:47]
	v_mfma_f32_16x16x32_f16 v[40:43], v[88:91], v[152:155], v[40:43]
	v_mfma_f32_16x16x32_f16 v[28:31], v[72:75], v[160:163], v[28:31]
	v_mfma_f32_16x16x32_f16 v[24:27], v[88:91], v[160:163], v[24:27]
	v_mfma_f32_16x16x32_f16 v[12:15], v[72:75], v[168:171], v[12:15]
	v_mfma_f32_16x16x32_f16 v[8:11], v[88:91], v[168:171], v[8:11]
	v_mfma_f32_16x16x32_f16 v[60:63], v[80:83], v[148:151], v[60:63]
	v_mfma_f32_16x16x32_f16 v[56:59], v[92:95], v[148:151], v[56:59]
	v_mfma_f32_16x16x32_f16 v[44:47], v[80:83], v[156:159], v[44:47]
	v_mfma_f32_16x16x32_f16 v[40:43], v[92:95], v[156:159], v[40:43]
	v_mfma_f32_16x16x32_f16 v[28:31], v[80:83], v[164:167], v[28:31]
	v_mfma_f32_16x16x32_f16 v[24:27], v[92:95], v[164:167], v[24:27]
	v_mfma_f32_16x16x32_f16 v[12:15], v[80:83], v[172:175], v[12:15]
	v_mfma_f32_16x16x32_f16 v[8:11], v[92:95], v[172:175], v[8:11]
	s_setprio 0
	s_barrier
	s_add_u32 s88, s40, 0x30000
	s_addc_u32 s89, s41, 0
	s_add_i32 s90, s70, s50
	v_lshl_add_u64 v[72:73], s[88:89], 0, v[178:179]
	s_mov_b32 m0, s90
	s_nop 0
	global_load_lds_dwordx4 v[72:73], off
	v_lshl_add_u64 v[72:73], s[88:89], 0, v[182:183]
	s_add_i32 m0, s90, 0x2000
	s_nop 0
	global_load_lds_dwordx4 v[72:73], off
	s_waitcnt vmcnt(6)
	s_barrier
	s_setprio 1
	v_mfma_f32_16x16x32_f16 v[52:55], v[190:193], v[136:139], v[52:55]
	v_mfma_f32_16x16x32_f16 v[48:51], v[198:201], v[136:139], v[48:51]
	v_mfma_f32_16x16x32_f16 v[36:39], v[190:193], v[152:155], v[36:39]
	v_mfma_f32_16x16x32_f16 v[32:35], v[198:201], v[152:155], v[32:35]
	v_mfma_f32_16x16x32_f16 v[20:23], v[190:193], v[160:163], v[20:23]
	v_mfma_f32_16x16x32_f16 v[16:19], v[198:201], v[160:163], v[16:19]
	v_mfma_f32_16x16x32_f16 v[4:7], v[190:193], v[168:171], v[4:7]
	v_mfma_f32_16x16x32_f16 v[0:3], v[198:201], v[168:171], v[0:3]
	v_mfma_f32_16x16x32_f16 v[52:55], v[194:197], v[148:151], v[52:55]
	v_mfma_f32_16x16x32_f16 v[48:51], v[202:205], v[148:151], v[48:51]
	v_mfma_f32_16x16x32_f16 v[36:39], v[194:197], v[156:159], v[36:39]
	v_mfma_f32_16x16x32_f16 v[32:35], v[202:205], v[156:159], v[32:35]
	v_mfma_f32_16x16x32_f16 v[20:23], v[194:197], v[164:167], v[20:23]
	v_mfma_f32_16x16x32_f16 v[16:19], v[202:205], v[164:167], v[16:19]
	v_mfma_f32_16x16x32_f16 v[4:7], v[194:197], v[172:175], v[4:7]
	v_mfma_f32_16x16x32_f16 v[0:3], v[202:205], v[172:175], v[0:3]
	s_setprio 0
	s_add_i32 s88, 0, 0x18000
	v_add_u32_e32 v92, s88, v228
	s_barrier
	ds_read_b128 v[72:75], v92
	ds_read_b128 v[80:83], v92 offset:1024
	ds_read_b128 v[88:91], v92 offset:2048
	ds_read_b128 v[92:95], v92 offset:3072
	s_add_u32 s42, s42, 0xc0000
	s_addc_u32 s43, s43, 0
	s_mov_b32 m0, s53
	v_lshl_add_u64 v[190:191], s[42:43], 0, v[176:177]
	ds_read_b128 v[136:139], v232 offset:32768
	ds_read_b128 v[148:151], v232 offset:33792
	ds_read_b128 v[152:155], v232 offset:34816
	ds_read_b128 v[156:159], v232 offset:35840
	ds_read_b128 v[160:163], v232 offset:36864
	ds_read_b128 v[164:167], v232 offset:37888
	ds_read_b128 v[168:171], v232 offset:38912
	ds_read_b128 v[172:175], v232 offset:39936
	global_load_lds_dwordx4 v[190:191], off
	v_lshl_add_u64 v[190:191], s[42:43], 0, v[180:181]
	s_mov_b32 m0, s54
	s_nop 0
	global_load_lds_dwordx4 v[190:191], off
	s_waitcnt lgkmcnt(8)
	s_barrier
	s_waitcnt lgkmcnt(0)
	s_setprio 1
	s_waitcnt lgkmcnt(0)
	v_mfma_f32_16x16x32_f16 v[144:147], v[72:75], v[136:139], v[144:147]
	v_mfma_f32_16x16x32_f16 v[140:143], v[88:91], v[136:139], v[140:143]
	v_mfma_f32_16x16x32_f16 v[124:127], v[72:75], v[152:155], v[124:127]
	v_mfma_f32_16x16x32_f16 v[120:123], v[88:91], v[152:155], v[120:123]
	v_mfma_f32_16x16x32_f16 v[108:111], v[72:75], v[160:163], v[108:111]
	v_mfma_f32_16x16x32_f16 v[104:107], v[88:91], v[160:163], v[104:107]
	v_mfma_f32_16x16x32_f16 v[84:87], v[72:75], v[168:171], v[84:87]
	v_mfma_f32_16x16x32_f16 v[76:79], v[88:91], v[168:171], v[76:79]
	v_mfma_f32_16x16x32_f16 v[144:147], v[80:83], v[148:151], v[144:147]
	v_mfma_f32_16x16x32_f16 v[140:143], v[92:95], v[148:151], v[140:143]
	v_mfma_f32_16x16x32_f16 v[124:127], v[80:83], v[156:159], v[124:127]
	v_mfma_f32_16x16x32_f16 v[120:123], v[92:95], v[156:159], v[120:123]
	v_mfma_f32_16x16x32_f16 v[108:111], v[80:83], v[164:167], v[108:111]
	v_mfma_f32_16x16x32_f16 v[104:107], v[92:95], v[164:167], v[104:107]
	v_mfma_f32_16x16x32_f16 v[84:87], v[80:83], v[172:175], v[84:87]
	v_mfma_f32_16x16x32_f16 v[76:79], v[92:95], v[172:175], v[76:79]
	s_setprio 0
	s_barrier
	s_add_i32 s42, 0, 0x1c000
	s_add_i32 s43, s88, s50
	v_add_u32_e32 v202, s42, v228
	v_lshl_add_u64 v[206:207], v[206:207], 0, s[36:37]
	s_mov_b32 m0, s43
	ds_read_b128 v[190:193], v202
	ds_read_b128 v[194:197], v202 offset:1024
	ds_read_b128 v[198:201], v202 offset:2048
	ds_read_b128 v[202:205], v202 offset:3072
	global_load_lds_dwordx4 v[206:207], off
	v_lshl_add_u64 v[206:207], v[208:209], 0, s[36:37]
	s_add_i32 m0, s43, 0x2000
	s_nop 0
	global_load_lds_dwordx4 v[206:207], off
	s_barrier
	s_waitcnt lgkmcnt(0)
	s_setprio 1
	s_waitcnt lgkmcnt(0)
	v_mfma_f32_16x16x32_f16 v[132:135], v[190:193], v[136:139], v[132:135]
	v_mfma_f32_16x16x32_f16 v[128:131], v[198:201], v[136:139], v[128:131]
	v_mfma_f32_16x16x32_f16 v[116:119], v[190:193], v[152:155], v[116:119]
	v_mfma_f32_16x16x32_f16 v[112:115], v[198:201], v[152:155], v[112:115]
	v_mfma_f32_16x16x32_f16 v[100:103], v[190:193], v[160:163], v[100:103]
	v_mfma_f32_16x16x32_f16 v[96:99], v[198:201], v[160:163], v[96:99]
	v_mfma_f32_16x16x32_f16 v[68:71], v[190:193], v[168:171], v[68:71]
	v_mfma_f32_16x16x32_f16 v[64:67], v[198:201], v[168:171], v[64:67]
	v_mfma_f32_16x16x32_f16 v[132:135], v[194:197], v[148:151], v[132:135]
	v_mfma_f32_16x16x32_f16 v[128:131], v[202:205], v[148:151], v[128:131]
	v_mfma_f32_16x16x32_f16 v[116:119], v[194:197], v[156:159], v[116:119]
	v_mfma_f32_16x16x32_f16 v[112:115], v[202:205], v[156:159], v[112:115]
	v_mfma_f32_16x16x32_f16 v[100:103], v[194:197], v[164:167], v[100:103]
	v_mfma_f32_16x16x32_f16 v[96:99], v[202:205], v[164:167], v[96:99]
	v_mfma_f32_16x16x32_f16 v[68:71], v[194:197], v[172:175], v[68:71]
	v_mfma_f32_16x16x32_f16 v[64:67], v[202:205], v[172:175], v[64:67]
	s_setprio 0
	s_mov_b32 m0, s58
	v_lshl_add_u64 v[206:207], v[210:211], 0, s[36:37]
	s_barrier
	ds_read_b128 v[136:139], v232 offset:49152
	ds_read_b128 v[148:151], v232 offset:50176
	ds_read_b128 v[152:155], v232 offset:51200
	ds_read_b128 v[156:159], v232 offset:52224
	ds_read_b128 v[160:163], v232 offset:53248
	ds_read_b128 v[164:167], v232 offset:54272
	ds_read_b128 v[168:171], v232 offset:55296
	ds_read_b128 v[172:175], v232 offset:56320
	global_load_lds_dwordx4 v[206:207], off
	v_lshl_add_u64 v[206:207], v[212:213], 0, s[36:37]
	s_mov_b32 m0, s59
	s_nop 0
	global_load_lds_dwordx4 v[206:207], off
	s_barrier
	s_waitcnt lgkmcnt(0)
	s_setprio 1
	s_waitcnt lgkmcnt(0)
	v_mfma_f32_16x16x32_f16 v[60:63], v[72:75], v[136:139], v[60:63]
	v_mfma_f32_16x16x32_f16 v[56:59], v[88:91], v[136:139], v[56:59]
	v_mfma_f32_16x16x32_f16 v[44:47], v[72:75], v[152:155], v[44:47]
	v_mfma_f32_16x16x32_f16 v[40:43], v[88:91], v[152:155], v[40:43]
	v_mfma_f32_16x16x32_f16 v[28:31], v[72:75], v[160:163], v[28:31]
	v_mfma_f32_16x16x32_f16 v[24:27], v[88:91], v[160:163], v[24:27]
	v_mfma_f32_16x16x32_f16 v[12:15], v[72:75], v[168:171], v[12:15]
	v_mfma_f32_16x16x32_f16 v[8:11], v[88:91], v[168:171], v[8:11]
	v_mfma_f32_16x16x32_f16 v[60:63], v[80:83], v[148:151], v[60:63]
	v_mfma_f32_16x16x32_f16 v[56:59], v[92:95], v[148:151], v[56:59]
	v_mfma_f32_16x16x32_f16 v[44:47], v[80:83], v[156:159], v[44:47]
	v_mfma_f32_16x16x32_f16 v[40:43], v[92:95], v[156:159], v[40:43]
	v_mfma_f32_16x16x32_f16 v[28:31], v[80:83], v[164:167], v[28:31]
	v_mfma_f32_16x16x32_f16 v[24:27], v[92:95], v[164:167], v[24:27]
	v_mfma_f32_16x16x32_f16 v[12:15], v[80:83], v[172:175], v[12:15]
	v_mfma_f32_16x16x32_f16 v[8:11], v[92:95], v[172:175], v[8:11]
	s_setprio 0
	s_barrier
	s_add_u32 s40, s40, 0x30080
	s_addc_u32 s41, s41, 0
	s_add_i32 s42, s42, s50
	v_lshl_add_u64 v[72:73], s[40:41], 0, v[178:179]
	s_mov_b32 m0, s42
	s_nop 0
	global_load_lds_dwordx4 v[72:73], off
	v_lshl_add_u64 v[72:73], s[40:41], 0, v[182:183]
	s_add_i32 m0, s42, 0x2000
	s_nop 0
	global_load_lds_dwordx4 v[72:73], off
	s_waitcnt vmcnt(6)
	s_barrier
	s_setprio 1
	v_mfma_f32_16x16x32_f16 v[52:55], v[190:193], v[136:139], v[52:55]
	v_mfma_f32_16x16x32_f16 v[48:51], v[198:201], v[136:139], v[48:51]
	v_mfma_f32_16x16x32_f16 v[36:39], v[190:193], v[152:155], v[36:39]
	v_mfma_f32_16x16x32_f16 v[32:35], v[198:201], v[152:155], v[32:35]
	v_mfma_f32_16x16x32_f16 v[20:23], v[190:193], v[160:163], v[20:23]
	v_mfma_f32_16x16x32_f16 v[16:19], v[198:201], v[160:163], v[16:19]
	v_mfma_f32_16x16x32_f16 v[4:7], v[190:193], v[168:171], v[4:7]
	v_mfma_f32_16x16x32_f16 v[0:3], v[198:201], v[168:171], v[0:3]
	v_mfma_f32_16x16x32_f16 v[52:55], v[194:197], v[148:151], v[52:55]
	v_mfma_f32_16x16x32_f16 v[48:51], v[202:205], v[148:151], v[48:51]
	v_mfma_f32_16x16x32_f16 v[36:39], v[194:197], v[156:159], v[36:39]
	v_mfma_f32_16x16x32_f16 v[32:35], v[202:205], v[156:159], v[32:35]
	v_mfma_f32_16x16x32_f16 v[20:23], v[194:197], v[164:167], v[20:23]
	v_mfma_f32_16x16x32_f16 v[16:19], v[202:205], v[164:167], v[16:19]
	v_mfma_f32_16x16x32_f16 v[4:7], v[194:197], v[172:175], v[4:7]
	v_mfma_f32_16x16x32_f16 v[0:3], v[202:205], v[172:175], v[0:3]
	s_setprio 0
	s_add_i32 s87, s87, 2
	s_add_u32 s38, s38, 0x100
	s_addc_u32 s39, s39, 0
	s_add_u32 s85, s85, 0x100
	s_addc_u32 s86, s86, 0
	s_cmp_gt_u32 s87, 45
	s_barrier
	s_cbranch_scc0 .LBB10_27
	s_lshl_b32 s92, s84, 8
	s_add_i32 s92, s92, s57
	s_lshl_b32 s93, s83, 8
	s_or_b32 s93, s93, s60
	v_lshlrev_b32_e32 v237, 2, v226
	s_lshl_b32 s96, s93, 2
	s_add_u32 s94, s16, s96
	s_addc_u32 s95, s17, 0
	global_load_dwordx4 v[72:75], v237, s[94:95] offset:0
	global_load_dwordx4 v[80:83], v237, s[94:95] offset:16
	global_load_dwordx4 v[88:91], v237, s[94:95] offset:128
	global_load_dwordx4 v[92:95], v237, s[94:95] offset:144
	s_add_u32 s94, s18, s96
	s_addc_u32 s95, s19, 0
	global_load_dwordx4 v[136:139], v237, s[94:95] offset:0
	global_load_dwordx4 v[148:151], v237, s[94:95] offset:16
	global_load_dwordx4 v[152:155], v237, s[94:95] offset:128
	global_load_dwordx4 v[156:159], v237, s[94:95] offset:144
	s_add_u32 s94, s14, s96
	s_addc_u32 s95, s15, 0
	global_load_dwordx4 v[160:163], v237, s[94:95] offset:0
	global_load_dwordx4 v[164:167], v237, s[94:95] offset:16
	global_load_dwordx4 v[168:171], v237, s[94:95] offset:128
	global_load_dwordx4 v[172:175], v237, s[94:95] offset:144
	v_lshlrev_b32_e32 v190, 3, v227
	s_lshl_b32 s96, s92, 3
	s_add_u32 s94, s12, s96
	s_addc_u32 s95, s13, 0
	global_load_dwordx2 v[238:239], v190, s[94:95] offset:0
	global_load_dwordx2 v[192:193], v190, s[94:95] offset:128
	global_load_dwordx2 v[194:195], v190, s[94:95] offset:256
	global_load_dwordx2 v[196:197], v190, s[94:95] offset:384
	global_load_dwordx2 v[198:199], v190, s[94:95] offset:1024
	global_load_dwordx2 v[200:201], v190, s[94:95] offset:1152
	global_load_dwordx2 v[202:203], v190, s[94:95] offset:1280
	global_load_dwordx2 v[204:205], v190, s[94:95] offset:1408
	v_mul_u32_u24_e32 v191, 0x600, v227
	v_lshl_add_u32 v191, v226, 1, v191
	s_mul_i32 s96, s92, 0x600
	s_lshl_b32 s97, s93, 1
	s_add_u32 s96, s96, s97
	s_add_u32 s98, s10, s96
	s_addc_u32 s99, s11, 0
	s_add_u32 s94, s98, 0x0
	s_addc_u32 s95, s99, 0
	global_load_dwordx4 v[208:211], v191, s[94:95] offset:0 nt
	global_load_dwordx4 v[212:215], v191, s[94:95] offset:64 nt
	s_add_u32 s94, s98, 0x6000
	s_addc_u32 s95, s99, 0
	global_load_dwordx4 v[216:219], v191, s[94:95] offset:0 nt
	global_load_dwordx4 v[220:223], v191, s[94:95] offset:64 nt
	v_add_u32_e32 v224, s92, v229
	v_mul_u32_u24_e32 v224, 0x600, v224
	s_lshl_b32 s97, s93, 1
	v_add3_u32 v224, v224, v230, s97
	s_lshl_b32 s96, s83, 2
	s_lshr_b32 s97, s60, 6
	s_add_u32 s96, s96, s97
	s_lshl_b32 s96, s96, 19
	s_lshl_b32 s97, s92, 3
	s_add_u32 s96, s96, s97
	s_add_u32 s100, s28, s96
	s_addc_u32 s101, s29, 0
	s_waitcnt vmcnt(19)
	v_pk_add_f32 v[72:73], v[72:73], v[136:137]
	v_pk_add_f32 v[74:75], v[74:75], v[138:139]
	s_waitcnt vmcnt(18)
	v_pk_add_f32 v[80:81], v[80:81], v[148:149]
	v_pk_add_f32 v[82:83], v[82:83], v[150:151]
	s_waitcnt vmcnt(17)
	v_pk_add_f32 v[88:89], v[88:89], v[152:153]
	v_pk_add_f32 v[90:91], v[90:91], v[154:155]
	s_waitcnt vmcnt(16)
	v_pk_add_f32 v[92:93], v[92:93], v[156:157]
	v_pk_add_f32 v[94:95], v[94:95], v[158:159]
	v_pk_add_f32 v[144:145], v[144:145], v[72:73]
	v_pk_add_f32 v[146:147], v[146:147], v[74:75]
	v_pk_add_f32 v[124:125], v[124:125], v[72:73]
	v_pk_add_f32 v[126:127], v[126:127], v[74:75]
	v_pk_add_f32 v[108:109], v[108:109], v[72:73]
	v_pk_add_f32 v[110:111], v[110:111], v[74:75]
	v_pk_add_f32 v[84:85], v[84:85], v[72:73]
	v_pk_add_f32 v[86:87], v[86:87], v[74:75]
	v_pk_add_f32 v[60:61], v[60:61], v[72:73]
	v_pk_add_f32 v[62:63], v[62:63], v[74:75]
	v_pk_add_f32 v[44:45], v[44:45], v[72:73]
	v_pk_add_f32 v[46:47], v[46:47], v[74:75]
	v_pk_add_f32 v[28:29], v[28:29], v[72:73]
	v_pk_add_f32 v[30:31], v[30:31], v[74:75]
	v_pk_add_f32 v[12:13], v[12:13], v[72:73]
	v_pk_add_f32 v[14:15], v[14:15], v[74:75]
	v_pk_add_f32 v[140:141], v[140:141], v[80:81]
	v_pk_add_f32 v[142:143], v[142:143], v[82:83]
	v_pk_add_f32 v[120:121], v[120:121], v[80:81]
	v_pk_add_f32 v[122:123], v[122:123], v[82:83]
	v_pk_add_f32 v[104:105], v[104:105], v[80:81]
	v_pk_add_f32 v[106:107], v[106:107], v[82:83]
	v_pk_add_f32 v[76:77], v[76:77], v[80:81]
	v_pk_add_f32 v[78:79], v[78:79], v[82:83]
	v_pk_add_f32 v[56:57], v[56:57], v[80:81]
	v_pk_add_f32 v[58:59], v[58:59], v[82:83]
	v_pk_add_f32 v[40:41], v[40:41], v[80:81]
	v_pk_add_f32 v[42:43], v[42:43], v[82:83]
	v_pk_add_f32 v[24:25], v[24:25], v[80:81]
	v_pk_add_f32 v[26:27], v[26:27], v[82:83]
	v_pk_add_f32 v[8:9], v[8:9], v[80:81]
	v_pk_add_f32 v[10:11], v[10:11], v[82:83]
	v_pk_add_f32 v[132:133], v[132:133], v[88:89]
	v_pk_add_f32 v[134:135], v[134:135], v[90:91]
	v_pk_add_f32 v[116:117], v[116:117], v[88:89]
	v_pk_add_f32 v[118:119], v[118:119], v[90:91]
	v_pk_add_f32 v[100:101], v[100:101], v[88:89]
	v_pk_add_f32 v[102:103], v[102:103], v[90:91]
	v_pk_add_f32 v[68:69], v[68:69], v[88:89]
	v_pk_add_f32 v[70:71], v[70:71], v[90:91]
	v_pk_add_f32 v[52:53], v[52:53], v[88:89]
	v_pk_add_f32 v[54:55], v[54:55], v[90:91]
	v_pk_add_f32 v[36:37], v[36:37], v[88:89]
	v_pk_add_f32 v[38:39], v[38:39], v[90:91]
	v_pk_add_f32 v[20:21], v[20:21], v[88:89]
	v_pk_add_f32 v[22:23], v[22:23], v[90:91]
	v_pk_add_f32 v[4:5], v[4:5], v[88:89]
	v_pk_add_f32 v[6:7], v[6:7], v[90:91]
	v_pk_add_f32 v[128:129], v[128:129], v[92:93]
	v_pk_add_f32 v[130:131], v[130:131], v[94:95]
	v_pk_add_f32 v[112:113], v[112:113], v[92:93]
	v_pk_add_f32 v[114:115], v[114:115], v[94:95]
	v_pk_add_f32 v[96:97], v[96:97], v[92:93]
	v_pk_add_f32 v[98:99], v[98:99], v[94:95]
	v_pk_add_f32 v[64:65], v[64:65], v[92:93]
	v_pk_add_f32 v[66:67], v[66:67], v[94:95]
	v_pk_add_f32 v[48:49], v[48:49], v[92:93]
	v_pk_add_f32 v[50:51], v[50:51], v[94:95]
	v_pk_add_f32 v[32:33], v[32:33], v[92:93]
	v_pk_add_f32 v[34:35], v[34:35], v[94:95]
	v_pk_add_f32 v[16:17], v[16:17], v[92:93]
	v_pk_add_f32 v[18:19], v[18:19], v[94:95]
	v_pk_add_f32 v[0:1], v[0:1], v[92:93]
	v_pk_add_f32 v[2:3], v[2:3], v[94:95]
	s_add_u32 s94, s98, 0xc000
	s_addc_u32 s95, s99, 0
	global_load_dwordx4 v[240:243], v191, s[94:95] offset:0 nt
	global_load_dwordx4 v[244:247], v191, s[94:95] offset:64 nt
	s_add_u32 s94, s98, 0x12000
	s_addc_u32 s95, s99, 0
	global_load_dwordx4 v[248:251], v191, s[94:95] offset:0 nt
	global_load_dwordx4 v[252:255], v191, s[94:95] offset:64 nt
	s_add_u32 s94, s98, 0x30000
	s_addc_u32 s95, s99, 0
	global_load_dwordx4 v[136:139], v191, s[94:95] offset:0 nt
	global_load_dwordx4 v[148:151], v191, s[94:95] offset:64 nt
	s_add_u32 s94, s98, 0x36000
	s_addc_u32 s95, s99, 0
	global_load_dwordx4 v[152:155], v191, s[94:95] offset:0 nt
	global_load_dwordx4 v[156:159], v191, s[94:95] offset:64 nt
	s_waitcnt vmcnt(19)
	s_waitcnt vmcnt(11)
	v_cvt_f32_f16_e32 v72, v208
	v_cvt_f32_f16_sdwa v73, v208 dst_sel:DWORD dst_unused:UNUSED_PAD src0_sel:WORD_1
	v_cvt_f32_f16_e32 v74, v209
	v_cvt_f32_f16_sdwa v75, v209 dst_sel:DWORD dst_unused:UNUSED_PAD src0_sel:WORD_1
	v_cvt_f32_f16_e32 v80, v210
	v_cvt_f32_f16_sdwa v81, v210 dst_sel:DWORD dst_unused:UNUSED_PAD src0_sel:WORD_1
	v_cvt_f32_f16_e32 v82, v211
	v_cvt_f32_f16_sdwa v83, v211 dst_sel:DWORD dst_unused:UNUSED_PAD src0_sel:WORD_1
	v_sub_f32_e32 v72, v72, v238
	v_sub_f32_e32 v73, v73, v238
	v_sub_f32_e32 v74, v74, v238
	v_sub_f32_e32 v75, v75, v238
	v_sub_f32_e32 v80, v80, v238
	v_sub_f32_e32 v81, v81, v238
	v_sub_f32_e32 v82, v82, v238
	v_sub_f32_e32 v83, v83, v238
	v_pk_mul_f32 v[72:73], v[238:239], v[72:73] op_sel:[1,0]
	v_pk_mul_f32 v[74:75], v[238:239], v[74:75] op_sel:[1,0]
	v_pk_mul_f32 v[80:81], v[238:239], v[80:81] op_sel:[1,0]
	v_pk_mul_f32 v[82:83], v[238:239], v[82:83] op_sel:[1,0]
	v_pk_fma_f32 v[144:145], v[72:73], v[160:161], v[144:145]
	v_pk_fma_f32 v[146:147], v[74:75], v[162:163], v[146:147]
	v_pk_fma_f32 v[140:141], v[80:81], v[164:165], v[140:141]
	v_pk_fma_f32 v[142:143], v[82:83], v[166:167], v[142:143]
	v_cvt_pk_f16_f32 v144, v144, v145
	v_cvt_pk_f16_f32 v145, v146, v147
	v_cvt_pk_f16_f32 v146, v140, v141
	v_cvt_pk_f16_f32 v147, v142, v143
	ds_write_b128 v235, v[144:147]
	v_fma_mix_f32 v206, v144, 1.0, 0 op_sel_hi:[1,0,0]
	v_fma_mix_f32 v207, v144, v144, 0 op_sel_hi:[1,1,0]
	v_fma_mix_f32 v206, v144, 1.0, v206 op_sel:[1,0,0] op_sel_hi:[1,0,0]
	v_fma_mix_f32 v207, v144, v144, v207 op_sel:[1,1,0] op_sel_hi:[1,1,0]
	v_fma_mix_f32 v206, v145, 1.0, v206 op_sel_hi:[1,0,0]
	v_fma_mix_f32 v207, v145, v145, v207 op_sel_hi:[1,1,0]
	v_fma_mix_f32 v206, v145, 1.0, v206 op_sel:[1,0,0] op_sel_hi:[1,0,0]
	v_fma_mix_f32 v207, v145, v145, v207 op_sel:[1,1,0] op_sel_hi:[1,1,0]
	v_fma_mix_f32 v206, v146, 1.0, v206 op_sel_hi:[1,0,0]
	v_fma_mix_f32 v207, v146, v146, v207 op_sel_hi:[1,1,0]
	v_fma_mix_f32 v206, v146, 1.0, v206 op_sel:[1,0,0] op_sel_hi:[1,0,0]
	v_fma_mix_f32 v207, v146, v146, v207 op_sel:[1,1,0] op_sel_hi:[1,1,0]
	v_fma_mix_f32 v206, v147, 1.0, v206 op_sel_hi:[1,0,0]
	v_fma_mix_f32 v207, v147, v147, v207 op_sel_hi:[1,1,0]
	v_fma_mix_f32 v206, v147, 1.0, v206 op_sel:[1,0,0] op_sel_hi:[1,0,0]
	v_fma_mix_f32 v207, v147, v147, v207 op_sel:[1,1,0] op_sel_hi:[1,1,0]
	s_waitcnt vmcnt(10)
	v_cvt_f32_f16_e32 v72, v212
	v_cvt_f32_f16_sdwa v73, v212 dst_sel:DWORD dst_unused:UNUSED_PAD src0_sel:WORD_1
	v_cvt_f32_f16_e32 v74, v213
	v_cvt_f32_f16_sdwa v75, v213 dst_sel:DWORD dst_unused:UNUSED_PAD src0_sel:WORD_1
	v_cvt_f32_f16_e32 v80, v214
	v_cvt_f32_f16_sdwa v81, v214 dst_sel:DWORD dst_unused:UNUSED_PAD src0_sel:WORD_1
	v_cvt_f32_f16_e32 v82, v215
	v_cvt_f32_f16_sdwa v83, v215 dst_sel:DWORD dst_unused:UNUSED_PAD src0_sel:WORD_1
	v_sub_f32_e32 v72, v72, v238
	v_sub_f32_e32 v73, v73, v238
	v_sub_f32_e32 v74, v74, v238
	v_sub_f32_e32 v75, v75, v238
	v_sub_f32_e32 v80, v80, v238
	v_sub_f32_e32 v81, v81, v238
	v_sub_f32_e32 v82, v82, v238
	v_sub_f32_e32 v83, v83, v238
	v_pk_mul_f32 v[72:73], v[238:239], v[72:73] op_sel:[1,0]
	v_pk_mul_f32 v[74:75], v[238:239], v[74:75] op_sel:[1,0]
	v_pk_mul_f32 v[80:81], v[238:239], v[80:81] op_sel:[1,0]
	v_pk_mul_f32 v[82:83], v[238:239], v[82:83] op_sel:[1,0]
	v_pk_fma_f32 v[132:133], v[72:73], v[168:169], v[132:133]
	v_pk_fma_f32 v[134:135], v[74:75], v[170:171], v[134:135]
	v_pk_fma_f32 v[128:129], v[80:81], v[172:173], v[128:129]
	v_pk_fma_f32 v[130:131], v[82:83], v[174:175], v[130:131]
	v_cvt_pk_f16_f32 v132, v132, v133
	v_cvt_pk_f16_f32 v133, v134, v135
	v_cvt_pk_f16_f32 v134, v128, v129
	v_cvt_pk_f16_f32 v135, v130, v131
	ds_write_b128 v235, v[132:135] offset:64
	v_fma_mix_f32 v206, v132, 1.0, v206 op_sel_hi:[1,0,0]
	v_fma_mix_f32 v207, v132, v132, v207 op_sel_hi:[1,1,0]
	v_fma_mix_f32 v206, v132, 1.0, v206 op_sel:[1,0,0] op_sel_hi:[1,0,0]
	v_fma_mix_f32 v207, v132, v132, v207 op_sel:[1,1,0] op_sel_hi:[1,1,0]
	v_fma_mix_f32 v206, v133, 1.0, v206 op_sel_hi:[1,0,0]
	v_fma_mix_f32 v207, v133, v133, v207 op_sel_hi:[1,1,0]
	v_fma_mix_f32 v206, v133, 1.0, v206 op_sel:[1,0,0] op_sel_hi:[1,0,0]
	v_fma_mix_f32 v207, v133, v133, v207 op_sel:[1,1,0] op_sel_hi:[1,1,0]
	v_fma_mix_f32 v206, v134, 1.0, v206 op_sel_hi:[1,0,0]
	v_fma_mix_f32 v207, v134, v134, v207 op_sel_hi:[1,1,0]
	v_fma_mix_f32 v206, v134, 1.0, v206 op_sel:[1,0,0] op_sel_hi:[1,0,0]
	v_fma_mix_f32 v207, v134, v134, v207 op_sel:[1,1,0] op_sel_hi:[1,1,0]
	v_fma_mix_f32 v206, v135, 1.0, v206 op_sel_hi:[1,0,0]
	v_fma_mix_f32 v207, v135, v135, v207 op_sel_hi:[1,1,0]
	v_fma_mix_f32 v206, v135, 1.0, v206 op_sel:[1,0,0] op_sel_hi:[1,0,0]
	v_fma_mix_f32 v207, v135, v135, v207 op_sel:[1,1,0] op_sel_hi:[1,1,0]
	ds_read_b128 v[88:91], v236
	ds_read_b128 v[92:95], v236 offset:1152
	s_waitcnt vmcnt(9)
	v_cvt_f32_f16_e32 v72, v216
	v_cvt_f32_f16_sdwa v73, v216 dst_sel:DWORD dst_unused:UNUSED_PAD src0_sel:WORD_1
	v_cvt_f32_f16_e32 v74, v217
	v_cvt_f32_f16_sdwa v75, v217 dst_sel:DWORD dst_unused:UNUSED_PAD src0_sel:WORD_1
	v_cvt_f32_f16_e32 v80, v218
	v_cvt_f32_f16_sdwa v81, v218 dst_sel:DWORD dst_unused:UNUSED_PAD src0_sel:WORD_1
	v_cvt_f32_f16_e32 v82, v219
	v_cvt_f32_f16_sdwa v83, v219 dst_sel:DWORD dst_unused:UNUSED_PAD src0_sel:WORD_1
	v_sub_f32_e32 v72, v72, v192
	v_sub_f32_e32 v73, v73, v192
	v_sub_f32_e32 v74, v74, v192
	v_sub_f32_e32 v75, v75, v192
	v_sub_f32_e32 v80, v80, v192
	v_sub_f32_e32 v81, v81, v192
	v_sub_f32_e32 v82, v82, v192
	v_sub_f32_e32 v83, v83, v192
	v_pk_mul_f32 v[72:73], v[192:193], v[72:73] op_sel:[1,0]
	v_pk_mul_f32 v[74:75], v[192:193], v[74:75] op_sel:[1,0]
	v_pk_mul_f32 v[80:81], v[192:193], v[80:81] op_sel:[1,0]
	v_pk_mul_f32 v[82:83], v[192:193], v[82:83] op_sel:[1,0]
	v_pk_fma_f32 v[124:125], v[72:73], v[160:161], v[124:125]
	v_pk_fma_f32 v[126:127], v[74:75], v[162:163], v[126:127]
	v_pk_fma_f32 v[120:121], v[80:81], v[164:165], v[120:121]
	v_pk_fma_f32 v[122:123], v[82:83], v[166:167], v[122:123]
	v_cvt_pk_f16_f32 v124, v124, v125
	v_cvt_pk_f16_f32 v125, v126, v127
	v_cvt_pk_f16_f32 v126, v120, v121
	v_cvt_pk_f16_f32 v127, v122, v123
	s_waitcnt lgkmcnt(0)
	buffer_store_dwordx4 v[88:91], v224, s[24:27], 0 offen nt
	v_add_u32_e32 v82, 0x3000, v224
	buffer_store_dwordx4 v[92:95], v82, s[24:27], 0 offen nt
	ds_write_b128 v235, v[124:127]
	v_fma_mix_f32 v140, v124, 1.0, 0 op_sel_hi:[1,0,0]
	v_fma_mix_f32 v141, v124, v124, 0 op_sel_hi:[1,1,0]
	v_fma_mix_f32 v140, v124, 1.0, v140 op_sel:[1,0,0] op_sel_hi:[1,0,0]
	v_fma_mix_f32 v141, v124, v124, v141 op_sel:[1,1,0] op_sel_hi:[1,1,0]
	v_fma_mix_f32 v140, v125, 1.0, v140 op_sel_hi:[1,0,0]
	v_fma_mix_f32 v141, v125, v125, v141 op_sel_hi:[1,1,0]
	v_fma_mix_f32 v140, v125, 1.0, v140 op_sel:[1,0,0] op_sel_hi:[1,0,0]
	v_fma_mix_f32 v141, v125, v125, v141 op_sel:[1,1,0] op_sel_hi:[1,1,0]
	v_fma_mix_f32 v140, v126, 1.0, v140 op_sel_hi:[1,0,0]
	v_fma_mix_f32 v141, v126, v126, v141 op_sel_hi:[1,1,0]
	v_fma_mix_f32 v140, v126, 1.0, v140 op_sel:[1,0,0] op_sel_hi:[1,0,0]
	v_fma_mix_f32 v141, v126, v126, v141 op_sel:[1,1,0] op_sel_hi:[1,1,0]
	v_fma_mix_f32 v140, v127, 1.0, v140 op_sel_hi:[1,0,0]
	v_fma_mix_f32 v141, v127, v127, v141 op_sel_hi:[1,1,0]
	v_fma_mix_f32 v140, v127, 1.0, v140 op_sel:[1,0,0] op_sel_hi:[1,0,0]
	v_fma_mix_f32 v141, v127, v127, v141 op_sel:[1,1,0] op_sel_hi:[1,1,0]
	s_waitcnt vmcnt(10)
	v_cvt_f32_f16_e32 v72, v220
	v_cvt_f32_f16_sdwa v73, v220 dst_sel:DWORD dst_unused:UNUSED_PAD src0_sel:WORD_1
	v_cvt_f32_f16_e32 v74, v221
	v_cvt_f32_f16_sdwa v75, v221 dst_sel:DWORD dst_unused:UNUSED_PAD src0_sel:WORD_1
	v_cvt_f32_f16_e32 v80, v222
	v_cvt_f32_f16_sdwa v81, v222 dst_sel:DWORD dst_unused:UNUSED_PAD src0_sel:WORD_1
	v_cvt_f32_f16_e32 v82, v223
	v_cvt_f32_f16_sdwa v83, v223 dst_sel:DWORD dst_unused:UNUSED_PAD src0_sel:WORD_1
	v_sub_f32_e32 v72, v72, v192
	v_sub_f32_e32 v73, v73, v192
	v_sub_f32_e32 v74, v74, v192
	v_sub_f32_e32 v75, v75, v192
	v_sub_f32_e32 v80, v80, v192
	v_sub_f32_e32 v81, v81, v192
	v_sub_f32_e32 v82, v82, v192
	v_sub_f32_e32 v83, v83, v192
	v_pk_mul_f32 v[72:73], v[192:193], v[72:73] op_sel:[1,0]
	v_pk_mul_f32 v[74:75], v[192:193], v[74:75] op_sel:[1,0]
	v_pk_mul_f32 v[80:81], v[192:193], v[80:81] op_sel:[1,0]
	v_pk_mul_f32 v[82:83], v[192:193], v[82:83] op_sel:[1,0]
	v_pk_fma_f32 v[116:117], v[72:73], v[168:169], v[116:117]
	v_pk_fma_f32 v[118:119], v[74:75], v[170:171], v[118:119]
	v_pk_fma_f32 v[112:113], v[80:81], v[172:173], v[112:113]
	v_pk_fma_f32 v[114:115], v[82:83], v[174:175], v[114:115]
	v_cvt_pk_f16_f32 v116, v116, v117
	v_cvt_pk_f16_f32 v117, v118, v119
	v_cvt_pk_f16_f32 v118, v112, v113
	v_cvt_pk_f16_f32 v119, v114, v115
	ds_write_b128 v235, v[116:119] offset:64
	v_fma_mix_f32 v140, v116, 1.0, v140 op_sel_hi:[1,0,0]
	v_fma_mix_f32 v141, v116, v116, v141 op_sel_hi:[1,1,0]
	v_fma_mix_f32 v140, v116, 1.0, v140 op_sel:[1,0,0] op_sel_hi:[1,0,0]
	v_fma_mix_f32 v141, v116, v116, v141 op_sel:[1,1,0] op_sel_hi:[1,1,0]
	v_fma_mix_f32 v140, v117, 1.0, v140 op_sel_hi:[1,0,0]
	v_fma_mix_f32 v141, v117, v117, v141 op_sel_hi:[1,1,0]
	v_fma_mix_f32 v140, v117, 1.0, v140 op_sel:[1,0,0] op_sel_hi:[1,0,0]
	v_fma_mix_f32 v141, v117, v117, v141 op_sel:[1,1,0] op_sel_hi:[1,1,0]
	v_fma_mix_f32 v140, v118, 1.0, v140 op_sel_hi:[1,0,0]
	v_fma_mix_f32 v141, v118, v118, v141 op_sel_hi:[1,1,0]
	v_fma_mix_f32 v140, v118, 1.0, v140 op_sel:[1,0,0] op_sel_hi:[1,0,0]
	v_fma_mix_f32 v141, v118, v118, v141 op_sel:[1,1,0] op_sel_hi:[1,1,0]
	v_fma_mix_f32 v140, v119, 1.0, v140 op_sel_hi:[1,0,0]
	v_fma_mix_f32 v141, v119, v119, v141 op_sel_hi:[1,1,0]
	v_fma_mix_f32 v140, v119, 1.0, v140 op_sel:[1,0,0] op_sel_hi:[1,0,0]
	v_fma_mix_f32 v141, v119, v119, v141 op_sel:[1,1,0] op_sel_hi:[1,1,0]
	ds_read_b128 v[208:211], v236
	ds_read_b128 v[128:131], v236 offset:1152
	s_add_u32 s94, s98, 0x3c000
	s_addc_u32 s95, s99, 0
	global_load_dwordx4 v[212:215], v191, s[94:95] offset:0 nt
	global_load_dwordx4 v[144:147], v191, s[94:95] offset:64 nt
	s_add_u32 s94, s98, 0x42000
	s_addc_u32 s95, s99, 0
	global_load_dwordx4 v[132:135], v191, s[94:95] offset:0 nt
	global_load_dwordx4 v[88:91], v191, s[94:95] offset:64 nt
	s_waitcnt vmcnt(13)
	v_cvt_f32_f16_e32 v72, v240
	v_cvt_f32_f16_sdwa v73, v240 dst_sel:DWORD dst_unused:UNUSED_PAD src0_sel:WORD_1
	v_cvt_f32_f16_e32 v74, v241
	v_cvt_f32_f16_sdwa v75, v241 dst_sel:DWORD dst_unused:UNUSED_PAD src0_sel:WORD_1
	v_cvt_f32_f16_e32 v80, v242
	v_cvt_f32_f16_sdwa v81, v242 dst_sel:DWORD dst_unused:UNUSED_PAD src0_sel:WORD_1
	v_cvt_f32_f16_e32 v82, v243
	v_cvt_f32_f16_sdwa v83, v243 dst_sel:DWORD dst_unused:UNUSED_PAD src0_sel:WORD_1
	v_sub_f32_e32 v72, v72, v194
	v_sub_f32_e32 v73, v73, v194
	v_sub_f32_e32 v74, v74, v194
	v_sub_f32_e32 v75, v75, v194
	v_sub_f32_e32 v80, v80, v194
	v_sub_f32_e32 v81, v81, v194
	v_sub_f32_e32 v82, v82, v194
	v_sub_f32_e32 v83, v83, v194
	v_pk_mul_f32 v[72:73], v[194:195], v[72:73] op_sel:[1,0]
	v_pk_mul_f32 v[74:75], v[194:195], v[74:75] op_sel:[1,0]
	v_pk_mul_f32 v[80:81], v[194:195], v[80:81] op_sel:[1,0]
	v_pk_mul_f32 v[82:83], v[194:195], v[82:83] op_sel:[1,0]
	v_pk_fma_f32 v[108:109], v[72:73], v[160:161], v[108:109]
	v_pk_fma_f32 v[110:111], v[74:75], v[162:163], v[110:111]
	v_pk_fma_f32 v[104:105], v[80:81], v[164:165], v[104:105]
	v_pk_fma_f32 v[106:107], v[82:83], v[166:167], v[106:107]
	v_cvt_pk_f16_f32 v108, v108, v109
	v_cvt_pk_f16_f32 v109, v110, v111
	v_cvt_pk_f16_f32 v110, v104, v105
	v_cvt_pk_f16_f32 v111, v106, v107
	s_waitcnt lgkmcnt(0)
	v_add_u32_e32 v83, 0x6000, v224
	buffer_store_dwordx4 v[208:211], v83, s[24:27], 0 offen nt
	v_add_u32_e32 v82, 0x9000, v224
	buffer_store_dwordx4 v[128:131], v82, s[24:27], 0 offen nt
	ds_write_b128 v235, v[108:111]
	v_fma_mix_f32 v142, v108, 1.0, 0 op_sel_hi:[1,0,0]
	v_fma_mix_f32 v143, v108, v108, 0 op_sel_hi:[1,1,0]
	v_fma_mix_f32 v142, v108, 1.0, v142 op_sel:[1,0,0] op_sel_hi:[1,0,0]
	v_fma_mix_f32 v143, v108, v108, v143 op_sel:[1,1,0] op_sel_hi:[1,1,0]
	v_fma_mix_f32 v142, v109, 1.0, v142 op_sel_hi:[1,0,0]
	v_fma_mix_f32 v143, v109, v109, v143 op_sel_hi:[1,1,0]
	v_fma_mix_f32 v142, v109, 1.0, v142 op_sel:[1,0,0] op_sel_hi:[1,0,0]
	v_fma_mix_f32 v143, v109, v109, v143 op_sel:[1,1,0] op_sel_hi:[1,1,0]
	v_fma_mix_f32 v142, v110, 1.0, v142 op_sel_hi:[1,0,0]
	v_fma_mix_f32 v143, v110, v110, v143 op_sel_hi:[1,1,0]
	v_fma_mix_f32 v142, v110, 1.0, v142 op_sel:[1,0,0] op_sel_hi:[1,0,0]
	v_fma_mix_f32 v143, v110, v110, v143 op_sel:[1,1,0] op_sel_hi:[1,1,0]
	v_fma_mix_f32 v142, v111, 1.0, v142 op_sel_hi:[1,0,0]
	v_fma_mix_f32 v143, v111, v111, v143 op_sel_hi:[1,1,0]
	v_fma_mix_f32 v142, v111, 1.0, v142 op_sel:[1,0,0] op_sel_hi:[1,0,0]
	v_fma_mix_f32 v143, v111, v111, v143 op_sel:[1,1,0] op_sel_hi:[1,1,0]
	s_waitcnt vmcnt(14)
	v_cvt_f32_f16_e32 v72, v244
	v_cvt_f32_f16_sdwa v73, v244 dst_sel:DWORD dst_unused:UNUSED_PAD src0_sel:WORD_1
	v_cvt_f32_f16_e32 v74, v245
	v_cvt_f32_f16_sdwa v75, v245 dst_sel:DWORD dst_unused:UNUSED_PAD src0_sel:WORD_1
	v_cvt_f32_f16_e32 v80, v246
	v_cvt_f32_f16_sdwa v81, v246 dst_sel:DWORD dst_unused:UNUSED_PAD src0_sel:WORD_1
	v_cvt_f32_f16_e32 v82, v247
	v_cvt_f32_f16_sdwa v83, v247 dst_sel:DWORD dst_unused:UNUSED_PAD src0_sel:WORD_1
	v_sub_f32_e32 v72, v72, v194
	v_sub_f32_e32 v73, v73, v194
	v_sub_f32_e32 v74, v74, v194
	v_sub_f32_e32 v75, v75, v194
	v_sub_f32_e32 v80, v80, v194
	v_sub_f32_e32 v81, v81, v194
	v_sub_f32_e32 v82, v82, v194
	v_sub_f32_e32 v83, v83, v194
	v_pk_mul_f32 v[72:73], v[194:195], v[72:73] op_sel:[1,0]
	v_pk_mul_f32 v[74:75], v[194:195], v[74:75] op_sel:[1,0]
	v_pk_mul_f32 v[80:81], v[194:195], v[80:81] op_sel:[1,0]
	v_pk_mul_f32 v[82:83], v[194:195], v[82:83] op_sel:[1,0]
	v_pk_fma_f32 v[100:101], v[72:73], v[168:169], v[100:101]
	v_pk_fma_f32 v[102:103], v[74:75], v[170:171], v[102:103]
	v_pk_fma_f32 v[96:97], v[80:81], v[172:173], v[96:97]
	v_pk_fma_f32 v[98:99], v[82:83], v[174:175], v[98:99]
	v_cvt_pk_f16_f32 v100, v100, v101
	v_cvt_pk_f16_f32 v101, v102, v103
	v_cvt_pk_f16_f32 v102, v96, v97
	v_cvt_pk_f16_f32 v103, v98, v99
	ds_write_b128 v235, v[100:103] offset:64
	v_fma_mix_f32 v142, v100, 1.0, v142 op_sel_hi:[1,0,0]
	v_fma_mix_f32 v143, v100, v100, v143 op_sel_hi:[1,1,0]
	v_fma_mix_f32 v142, v100, 1.0, v142 op_sel:[1,0,0] op_sel_hi:[1,0,0]
	v_fma_mix_f32 v143, v100, v100, v143 op_sel:[1,1,0] op_sel_hi:[1,1,0]
	v_fma_mix_f32 v142, v101, 1.0, v142 op_sel_hi:[1,0,0]
	v_fma_mix_f32 v143, v101, v101, v143 op_sel_hi:[1,1,0]
	v_fma_mix_f32 v142, v101, 1.0, v142 op_sel:[1,0,0] op_sel_hi:[1,0,0]
	v_fma_mix_f32 v143, v101, v101, v143 op_sel:[1,1,0] op_sel_hi:[1,1,0]
	v_fma_mix_f32 v142, v102, 1.0, v142 op_sel_hi:[1,0,0]
	v_fma_mix_f32 v143, v102, v102, v143 op_sel_hi:[1,1,0]
	v_fma_mix_f32 v142, v102, 1.0, v142 op_sel:[1,0,0] op_sel_hi:[1,0,0]
	v_fma_mix_f32 v143, v102, v102, v143 op_sel:[1,1,0] op_sel_hi:[1,1,0]
	v_fma_mix_f32 v142, v103, 1.0, v142 op_sel_hi:[1,0,0]
	v_fma_mix_f32 v143, v103, v103, v143 op_sel_hi:[1,1,0]
	v_fma_mix_f32 v142, v103, 1.0, v142 op_sel:[1,0,0] op_sel_hi:[1,0,0]
	v_fma_mix_f32 v143, v103, v103, v143 op_sel:[1,1,0] op_sel_hi:[1,1,0]
	ds_read_b128 v[92:95], v236
	ds_read_b128 v[120:123], v236 offset:1152
	s_waitcnt vmcnt(13)
	v_cvt_f32_f16_e32 v72, v248
	v_cvt_f32_f16_sdwa v73, v248 dst_sel:DWORD dst_unused:UNUSED_PAD src0_sel:WORD_1
	v_cvt_f32_f16_e32 v74, v249
	v_cvt_f32_f16_sdwa v75, v249 dst_sel:DWORD dst_unused:UNUSED_PAD src0_sel:WORD_1
	v_cvt_f32_f16_e32 v80, v250
	v_cvt_f32_f16_sdwa v81, v250 dst_sel:DWORD dst_unused:UNUSED_PAD src0_sel:WORD_1
	v_cvt_f32_f16_e32 v82, v251
	v_cvt_f32_f16_sdwa v83, v251 dst_sel:DWORD dst_unused:UNUSED_PAD src0_sel:WORD_1
	v_sub_f32_e32 v72, v72, v196
	v_sub_f32_e32 v73, v73, v196
	v_sub_f32_e32 v74, v74, v196
	v_sub_f32_e32 v75, v75, v196
	v_sub_f32_e32 v80, v80, v196
	v_sub_f32_e32 v81, v81, v196
	v_sub_f32_e32 v82, v82, v196
	v_sub_f32_e32 v83, v83, v196
	v_pk_mul_f32 v[72:73], v[196:197], v[72:73] op_sel:[1,0]
	v_pk_mul_f32 v[74:75], v[196:197], v[74:75] op_sel:[1,0]
	v_pk_mul_f32 v[80:81], v[196:197], v[80:81] op_sel:[1,0]
	v_pk_mul_f32 v[82:83], v[196:197], v[82:83] op_sel:[1,0]
	v_pk_fma_f32 v[84:85], v[72:73], v[160:161], v[84:85]
	v_pk_fma_f32 v[86:87], v[74:75], v[162:163], v[86:87]
	v_pk_fma_f32 v[76:77], v[80:81], v[164:165], v[76:77]
	v_pk_fma_f32 v[78:79], v[82:83], v[166:167], v[78:79]
	v_cvt_pk_f16_f32 v84, v84, v85
	v_cvt_pk_f16_f32 v85, v86, v87
	v_cvt_pk_f16_f32 v86, v76, v77
	v_cvt_pk_f16_f32 v87, v78, v79
	s_waitcnt lgkmcnt(0)
	v_add_u32_e32 v83, 0xc000, v224
	buffer_store_dwordx4 v[92:95], v83, s[24:27], 0 offen nt
	v_add_u32_e32 v82, 0xf000, v224
	buffer_store_dwordx4 v[120:123], v82, s[24:27], 0 offen nt
	ds_write_b128 v235, v[84:87]
	v_fma_mix_f32 v216, v84, 1.0, 0 op_sel_hi:[1,0,0]
	v_fma_mix_f32 v217, v84, v84, 0 op_sel_hi:[1,1,0]
	v_fma_mix_f32 v216, v84, 1.0, v216 op_sel:[1,0,0] op_sel_hi:[1,0,0]
	v_fma_mix_f32 v217, v84, v84, v217 op_sel:[1,1,0] op_sel_hi:[1,1,0]
	v_fma_mix_f32 v216, v85, 1.0, v216 op_sel_hi:[1,0,0]
	v_fma_mix_f32 v217, v85, v85, v217 op_sel_hi:[1,1,0]
	v_fma_mix_f32 v216, v85, 1.0, v216 op_sel:[1,0,0] op_sel_hi:[1,0,0]
	v_fma_mix_f32 v217, v85, v85, v217 op_sel:[1,1,0] op_sel_hi:[1,1,0]
	v_fma_mix_f32 v216, v86, 1.0, v216 op_sel_hi:[1,0,0]
	v_fma_mix_f32 v217, v86, v86, v217 op_sel_hi:[1,1,0]
	v_fma_mix_f32 v216, v86, 1.0, v216 op_sel:[1,0,0] op_sel_hi:[1,0,0]
	v_fma_mix_f32 v217, v86, v86, v217 op_sel:[1,1,0] op_sel_hi:[1,1,0]
	v_fma_mix_f32 v216, v87, 1.0, v216 op_sel_hi:[1,0,0]
	v_fma_mix_f32 v217, v87, v87, v217 op_sel_hi:[1,1,0]
	v_fma_mix_f32 v216, v87, 1.0, v216 op_sel:[1,0,0] op_sel_hi:[1,0,0]
	v_fma_mix_f32 v217, v87, v87, v217 op_sel:[1,1,0] op_sel_hi:[1,1,0]
	s_waitcnt vmcnt(14)
	v_cvt_f32_f16_e32 v72, v252
	v_cvt_f32_f16_sdwa v73, v252 dst_sel:DWORD dst_unused:UNUSED_PAD src0_sel:WORD_1
	v_cvt_f32_f16_e32 v74, v253
	v_cvt_f32_f16_sdwa v75, v253 dst_sel:DWORD dst_unused:UNUSED_PAD src0_sel:WORD_1
	v_cvt_f32_f16_e32 v80, v254
	v_cvt_f32_f16_sdwa v81, v254 dst_sel:DWORD dst_unused:UNUSED_PAD src0_sel:WORD_1
	v_cvt_f32_f16_e32 v82, v255
	v_cvt_f32_f16_sdwa v83, v255 dst_sel:DWORD dst_unused:UNUSED_PAD src0_sel:WORD_1
	v_sub_f32_e32 v72, v72, v196
	v_sub_f32_e32 v73, v73, v196
	v_sub_f32_e32 v74, v74, v196
	v_sub_f32_e32 v75, v75, v196
	v_sub_f32_e32 v80, v80, v196
	v_sub_f32_e32 v81, v81, v196
	v_sub_f32_e32 v82, v82, v196
	v_sub_f32_e32 v83, v83, v196
	v_pk_mul_f32 v[72:73], v[196:197], v[72:73] op_sel:[1,0]
	v_pk_mul_f32 v[74:75], v[196:197], v[74:75] op_sel:[1,0]
	v_pk_mul_f32 v[80:81], v[196:197], v[80:81] op_sel:[1,0]
	v_pk_mul_f32 v[82:83], v[196:197], v[82:83] op_sel:[1,0]
	v_pk_fma_f32 v[68:69], v[72:73], v[168:169], v[68:69]
	v_pk_fma_f32 v[70:71], v[74:75], v[170:171], v[70:71]
	v_pk_fma_f32 v[64:65], v[80:81], v[172:173], v[64:65]
	v_pk_fma_f32 v[66:67], v[82:83], v[174:175], v[66:67]
	v_cvt_pk_f16_f32 v68, v68, v69
	v_cvt_pk_f16_f32 v69, v70, v71
	v_cvt_pk_f16_f32 v70, v64, v65
	v_cvt_pk_f16_f32 v71, v66, v67
	ds_write_b128 v235, v[68:71] offset:64
	v_fma_mix_f32 v216, v68, 1.0, v216 op_sel_hi:[1,0,0]
	v_fma_mix_f32 v217, v68, v68, v217 op_sel_hi:[1,1,0]
	v_fma_mix_f32 v216, v68, 1.0, v216 op_sel:[1,0,0] op_sel_hi:[1,0,0]
	v_fma_mix_f32 v217, v68, v68, v217 op_sel:[1,1,0] op_sel_hi:[1,1,0]
	v_fma_mix_f32 v216, v69, 1.0, v216 op_sel_hi:[1,0,0]
	v_fma_mix_f32 v217, v69, v69, v217 op_sel_hi:[1,1,0]
	v_fma_mix_f32 v216, v69, 1.0, v216 op_sel:[1,0,0] op_sel_hi:[1,0,0]
	v_fma_mix_f32 v217, v69, v69, v217 op_sel:[1,1,0] op_sel_hi:[1,1,0]
	v_fma_mix_f32 v216, v70, 1.0, v216 op_sel_hi:[1,0,0]
	v_fma_mix_f32 v217, v70, v70, v217 op_sel_hi:[1,1,0]
	v_fma_mix_f32 v216, v70, 1.0, v216 op_sel:[1,0,0] op_sel_hi:[1,0,0]
	v_fma_mix_f32 v217, v70, v70, v217 op_sel:[1,1,0] op_sel_hi:[1,1,0]
	v_fma_mix_f32 v216, v71, 1.0, v216 op_sel_hi:[1,0,0]
	v_fma_mix_f32 v217, v71, v71, v217 op_sel_hi:[1,1,0]
	v_fma_mix_f32 v216, v71, 1.0, v216 op_sel:[1,0,0] op_sel_hi:[1,0,0]
	v_fma_mix_f32 v217, v71, v71, v217 op_sel:[1,1,0] op_sel_hi:[1,1,0]
	ds_read_b128 v[112:115], v236
	ds_read_b128 v[220:223], v236 offset:1152
	s_waitcnt vmcnt(13)
	v_cvt_f32_f16_e32 v72, v136
	v_cvt_f32_f16_sdwa v73, v136 dst_sel:DWORD dst_unused:UNUSED_PAD src0_sel:WORD_1
	v_cvt_f32_f16_e32 v74, v137
	v_cvt_f32_f16_sdwa v75, v137 dst_sel:DWORD dst_unused:UNUSED_PAD src0_sel:WORD_1
	v_cvt_f32_f16_e32 v80, v138
	v_cvt_f32_f16_sdwa v81, v138 dst_sel:DWORD dst_unused:UNUSED_PAD src0_sel:WORD_1
	v_cvt_f32_f16_e32 v82, v139
	v_cvt_f32_f16_sdwa v83, v139 dst_sel:DWORD dst_unused:UNUSED_PAD src0_sel:WORD_1
	v_sub_f32_e32 v72, v72, v198
	v_sub_f32_e32 v73, v73, v198
	v_sub_f32_e32 v74, v74, v198
	v_sub_f32_e32 v75, v75, v198
	v_sub_f32_e32 v80, v80, v198
	v_sub_f32_e32 v81, v81, v198
	v_sub_f32_e32 v82, v82, v198
	v_sub_f32_e32 v83, v83, v198
	v_pk_mul_f32 v[72:73], v[198:199], v[72:73] op_sel:[1,0]
	v_pk_mul_f32 v[74:75], v[198:199], v[74:75] op_sel:[1,0]
	v_pk_mul_f32 v[80:81], v[198:199], v[80:81] op_sel:[1,0]
	v_pk_mul_f32 v[82:83], v[198:199], v[82:83] op_sel:[1,0]
	v_pk_fma_f32 v[60:61], v[72:73], v[160:161], v[60:61]
	v_pk_fma_f32 v[62:63], v[74:75], v[162:163], v[62:63]
	v_pk_fma_f32 v[56:57], v[80:81], v[164:165], v[56:57]
	v_pk_fma_f32 v[58:59], v[82:83], v[166:167], v[58:59]
	v_cvt_pk_f16_f32 v60, v60, v61
	v_cvt_pk_f16_f32 v61, v62, v63
	v_cvt_pk_f16_f32 v62, v56, v57
	v_cvt_pk_f16_f32 v63, v58, v59
	s_waitcnt lgkmcnt(0)
	v_add_u32_e32 v83, 0x12000, v224
	buffer_store_dwordx4 v[112:115], v83, s[24:27], 0 offen nt
	v_add_u32_e32 v82, 0x15000, v224
	buffer_store_dwordx4 v[220:223], v82, s[24:27], 0 offen nt
	ds_write_b128 v235, v[60:63]
	v_fma_mix_f32 v218, v60, 1.0, 0 op_sel_hi:[1,0,0]
	v_fma_mix_f32 v219, v60, v60, 0 op_sel_hi:[1,1,0]
	v_fma_mix_f32 v218, v60, 1.0, v218 op_sel:[1,0,0] op_sel_hi:[1,0,0]
	v_fma_mix_f32 v219, v60, v60, v219 op_sel:[1,1,0] op_sel_hi:[1,1,0]
	v_fma_mix_f32 v218, v61, 1.0, v218 op_sel_hi:[1,0,0]
	v_fma_mix_f32 v219, v61, v61, v219 op_sel_hi:[1,1,0]
	v_fma_mix_f32 v218, v61, 1.0, v218 op_sel:[1,0,0] op_sel_hi:[1,0,0]
	v_fma_mix_f32 v219, v61, v61, v219 op_sel:[1,1,0] op_sel_hi:[1,1,0]
	v_fma_mix_f32 v218, v62, 1.0, v218 op_sel_hi:[1,0,0]
	v_fma_mix_f32 v219, v62, v62, v219 op_sel_hi:[1,1,0]
	v_fma_mix_f32 v218, v62, 1.0, v218 op_sel:[1,0,0] op_sel_hi:[1,0,0]
	v_fma_mix_f32 v219, v62, v62, v219 op_sel:[1,1,0] op_sel_hi:[1,1,0]
	v_fma_mix_f32 v218, v63, 1.0, v218 op_sel_hi:[1,0,0]
	v_fma_mix_f32 v219, v63, v63, v219 op_sel_hi:[1,1,0]
	v_fma_mix_f32 v218, v63, 1.0, v218 op_sel:[1,0,0] op_sel_hi:[1,0,0]
	v_fma_mix_f32 v219, v63, v63, v219 op_sel:[1,1,0] op_sel_hi:[1,1,0]
	s_waitcnt vmcnt(14)
	v_cvt_f32_f16_e32 v72, v148
	v_cvt_f32_f16_sdwa v73, v148 dst_sel:DWORD dst_unused:UNUSED_PAD src0_sel:WORD_1
	v_cvt_f32_f16_e32 v74, v149
	v_cvt_f32_f16_sdwa v75, v149 dst_sel:DWORD dst_unused:UNUSED_PAD src0_sel:WORD_1
	v_cvt_f32_f16_e32 v80, v150
	v_cvt_f32_f16_sdwa v81, v150 dst_sel:DWORD dst_unused:UNUSED_PAD src0_sel:WORD_1
	v_cvt_f32_f16_e32 v82, v151
	v_cvt_f32_f16_sdwa v83, v151 dst_sel:DWORD dst_unused:UNUSED_PAD src0_sel:WORD_1
	v_sub_f32_e32 v72, v72, v198
	v_sub_f32_e32 v73, v73, v198
	v_sub_f32_e32 v74, v74, v198
	v_sub_f32_e32 v75, v75, v198
	v_sub_f32_e32 v80, v80, v198
	v_sub_f32_e32 v81, v81, v198
	v_sub_f32_e32 v82, v82, v198
	v_sub_f32_e32 v83, v83, v198
	v_pk_mul_f32 v[72:73], v[198:199], v[72:73] op_sel:[1,0]
	v_pk_mul_f32 v[74:75], v[198:199], v[74:75] op_sel:[1,0]
	v_pk_mul_f32 v[80:81], v[198:199], v[80:81] op_sel:[1,0]
	v_pk_mul_f32 v[82:83], v[198:199], v[82:83] op_sel:[1,0]
	v_pk_fma_f32 v[52:53], v[72:73], v[168:169], v[52:53]
	v_pk_fma_f32 v[54:55], v[74:75], v[170:171], v[54:55]
	v_pk_fma_f32 v[48:49], v[80:81], v[172:173], v[48:49]
	v_pk_fma_f32 v[50:51], v[82:83], v[174:175], v[50:51]
	v_cvt_pk_f16_f32 v52, v52, v53
	v_cvt_pk_f16_f32 v53, v54, v55
	v_cvt_pk_f16_f32 v54, v48, v49
	v_cvt_pk_f16_f32 v55, v50, v51
	ds_write_b128 v235, v[52:55] offset:64
	v_fma_mix_f32 v218, v52, 1.0, v218 op_sel_hi:[1,0,0]
	v_fma_mix_f32 v219, v52, v52, v219 op_sel_hi:[1,1,0]
	v_fma_mix_f32 v218, v52, 1.0, v218 op_sel:[1,0,0] op_sel_hi:[1,0,0]
	v_fma_mix_f32 v219, v52, v52, v219 op_sel:[1,1,0] op_sel_hi:[1,1,0]
	v_fma_mix_f32 v218, v53, 1.0, v218 op_sel_hi:[1,0,0]
	v_fma_mix_f32 v219, v53, v53, v219 op_sel_hi:[1,1,0]
	v_fma_mix_f32 v218, v53, 1.0, v218 op_sel:[1,0,0] op_sel_hi:[1,0,0]
	v_fma_mix_f32 v219, v53, v53, v219 op_sel:[1,1,0] op_sel_hi:[1,1,0]
	v_fma_mix_f32 v218, v54, 1.0, v218 op_sel_hi:[1,0,0]
	v_fma_mix_f32 v219, v54, v54, v219 op_sel_hi:[1,1,0]
	v_fma_mix_f32 v218, v54, 1.0, v218 op_sel:[1,0,0] op_sel_hi:[1,0,0]
	v_fma_mix_f32 v219, v54, v54, v219 op_sel:[1,1,0] op_sel_hi:[1,1,0]
	v_fma_mix_f32 v218, v55, 1.0, v218 op_sel_hi:[1,0,0]
	v_fma_mix_f32 v219, v55, v55, v219 op_sel_hi:[1,1,0]
	v_fma_mix_f32 v218, v55, 1.0, v218 op_sel:[1,0,0] op_sel_hi:[1,0,0]
	v_fma_mix_f32 v219, v55, v55, v219 op_sel:[1,1,0] op_sel_hi:[1,1,0]
	ds_read_b128 v[124:127], v236
	ds_read_b128 v[116:119], v236 offset:1152
	s_waitcnt vmcnt(13)
	v_cvt_f32_f16_e32 v72, v152
	v_cvt_f32_f16_sdwa v73, v152 dst_sel:DWORD dst_unused:UNUSED_PAD src0_sel:WORD_1
	v_cvt_f32_f16_e32 v74, v153
	v_cvt_f32_f16_sdwa v75, v153 dst_sel:DWORD dst_unused:UNUSED_PAD src0_sel:WORD_1
	v_cvt_f32_f16_e32 v80, v154
	v_cvt_f32_f16_sdwa v81, v154 dst_sel:DWORD dst_unused:UNUSED_PAD src0_sel:WORD_1
	v_cvt_f32_f16_e32 v82, v155
	v_cvt_f32_f16_sdwa v83, v155 dst_sel:DWORD dst_unused:UNUSED_PAD src0_sel:WORD_1
	v_sub_f32_e32 v72, v72, v200
	v_sub_f32_e32 v73, v73, v200
	v_sub_f32_e32 v74, v74, v200
	v_sub_f32_e32 v75, v75, v200
	v_sub_f32_e32 v80, v80, v200
	v_sub_f32_e32 v81, v81, v200
	v_sub_f32_e32 v82, v82, v200
	v_sub_f32_e32 v83, v83, v200
	v_pk_mul_f32 v[72:73], v[200:201], v[72:73] op_sel:[1,0]
	v_pk_mul_f32 v[74:75], v[200:201], v[74:75] op_sel:[1,0]
	v_pk_mul_f32 v[80:81], v[200:201], v[80:81] op_sel:[1,0]
	v_pk_mul_f32 v[82:83], v[200:201], v[82:83] op_sel:[1,0]
	v_pk_fma_f32 v[44:45], v[72:73], v[160:161], v[44:45]
	v_pk_fma_f32 v[46:47], v[74:75], v[162:163], v[46:47]
	v_pk_fma_f32 v[40:41], v[80:81], v[164:165], v[40:41]
	v_pk_fma_f32 v[42:43], v[82:83], v[166:167], v[42:43]
	v_cvt_pk_f16_f32 v44, v44, v45
	v_cvt_pk_f16_f32 v45, v46, v47
	v_cvt_pk_f16_f32 v46, v40, v41
	v_cvt_pk_f16_f32 v47, v42, v43
	s_waitcnt lgkmcnt(0)
	v_add_u32_e32 v83, 0x30000, v224
	buffer_store_dwordx4 v[124:127], v83, s[24:27], 0 offen nt
	v_add_u32_e32 v82, 0x33000, v224
	buffer_store_dwordx4 v[116:119], v82, s[24:27], 0 offen nt
	ds_write_b128 v235, v[44:47]
	v_fma_mix_f32 v208, v44, 1.0, 0 op_sel_hi:[1,0,0]
	v_fma_mix_f32 v209, v44, v44, 0 op_sel_hi:[1,1,0]
	v_fma_mix_f32 v208, v44, 1.0, v208 op_sel:[1,0,0] op_sel_hi:[1,0,0]
	v_fma_mix_f32 v209, v44, v44, v209 op_sel:[1,1,0] op_sel_hi:[1,1,0]
	v_fma_mix_f32 v208, v45, 1.0, v208 op_sel_hi:[1,0,0]
	v_fma_mix_f32 v209, v45, v45, v209 op_sel_hi:[1,1,0]
	v_fma_mix_f32 v208, v45, 1.0, v208 op_sel:[1,0,0] op_sel_hi:[1,0,0]
	v_fma_mix_f32 v209, v45, v45, v209 op_sel:[1,1,0] op_sel_hi:[1,1,0]
	v_fma_mix_f32 v208, v46, 1.0, v208 op_sel_hi:[1,0,0]
	v_fma_mix_f32 v209, v46, v46, v209 op_sel_hi:[1,1,0]
	v_fma_mix_f32 v208, v46, 1.0, v208 op_sel:[1,0,0] op_sel_hi:[1,0,0]
	v_fma_mix_f32 v209, v46, v46, v209 op_sel:[1,1,0] op_sel_hi:[1,1,0]
	v_fma_mix_f32 v208, v47, 1.0, v208 op_sel_hi:[1,0,0]
	v_fma_mix_f32 v209, v47, v47, v209 op_sel_hi:[1,1,0]
	v_fma_mix_f32 v208, v47, 1.0, v208 op_sel:[1,0,0] op_sel_hi:[1,0,0]
	v_fma_mix_f32 v209, v47, v47, v209 op_sel:[1,1,0] op_sel_hi:[1,1,0]
	s_waitcnt vmcnt(14)
	v_cvt_f32_f16_e32 v72, v156
	v_cvt_f32_f16_sdwa v73, v156 dst_sel:DWORD dst_unused:UNUSED_PAD src0_sel:WORD_1
	v_cvt_f32_f16_e32 v74, v157
	v_cvt_f32_f16_sdwa v75, v157 dst_sel:DWORD dst_unused:UNUSED_PAD src0_sel:WORD_1
	v_cvt_f32_f16_e32 v80, v158
	v_cvt_f32_f16_sdwa v81, v158 dst_sel:DWORD dst_unused:UNUSED_PAD src0_sel:WORD_1
	v_cvt_f32_f16_e32 v82, v159
	v_cvt_f32_f16_sdwa v83, v159 dst_sel:DWORD dst_unused:UNUSED_PAD src0_sel:WORD_1
	v_sub_f32_e32 v72, v72, v200
	v_sub_f32_e32 v73, v73, v200
	v_sub_f32_e32 v74, v74, v200
	v_sub_f32_e32 v75, v75, v200
	v_sub_f32_e32 v80, v80, v200
	v_sub_f32_e32 v81, v81, v200
	v_sub_f32_e32 v82, v82, v200
	v_sub_f32_e32 v83, v83, v200
	v_pk_mul_f32 v[72:73], v[200:201], v[72:73] op_sel:[1,0]
	v_pk_mul_f32 v[74:75], v[200:201], v[74:75] op_sel:[1,0]
	v_pk_mul_f32 v[80:81], v[200:201], v[80:81] op_sel:[1,0]
	v_pk_mul_f32 v[82:83], v[200:201], v[82:83] op_sel:[1,0]
	v_pk_fma_f32 v[36:37], v[72:73], v[168:169], v[36:37]
	v_pk_fma_f32 v[38:39], v[74:75], v[170:171], v[38:39]
	v_pk_fma_f32 v[32:33], v[80:81], v[172:173], v[32:33]
	v_pk_fma_f32 v[34:35], v[82:83], v[174:175], v[34:35]
	v_cvt_pk_f16_f32 v36, v36, v37
	v_cvt_pk_f16_f32 v37, v38, v39
	v_cvt_pk_f16_f32 v38, v32, v33
	v_cvt_pk_f16_f32 v39, v34, v35
	ds_write_b128 v235, v[36:39] offset:64
	v_fma_mix_f32 v208, v36, 1.0, v208 op_sel_hi:[1,0,0]
	v_fma_mix_f32 v209, v36, v36, v209 op_sel_hi:[1,1,0]
	v_fma_mix_f32 v208, v36, 1.0, v208 op_sel:[1,0,0] op_sel_hi:[1,0,0]
	v_fma_mix_f32 v209, v36, v36, v209 op_sel:[1,1,0] op_sel_hi:[1,1,0]
	v_fma_mix_f32 v208, v37, 1.0, v208 op_sel_hi:[1,0,0]
	v_fma_mix_f32 v209, v37, v37, v209 op_sel_hi:[1,1,0]
	v_fma_mix_f32 v208, v37, 1.0, v208 op_sel:[1,0,0] op_sel_hi:[1,0,0]
	v_fma_mix_f32 v209, v37, v37, v209 op_sel:[1,1,0] op_sel_hi:[1,1,0]
	v_fma_mix_f32 v208, v38, 1.0, v208 op_sel_hi:[1,0,0]
	v_fma_mix_f32 v209, v38, v38, v209 op_sel_hi:[1,1,0]
	v_fma_mix_f32 v208, v38, 1.0, v208 op_sel:[1,0,0] op_sel_hi:[1,0,0]
	v_fma_mix_f32 v209, v38, v38, v209 op_sel:[1,1,0] op_sel_hi:[1,1,0]
	v_fma_mix_f32 v208, v39, 1.0, v208 op_sel_hi:[1,0,0]
	v_fma_mix_f32 v209, v39, v39, v209 op_sel_hi:[1,1,0]
	v_fma_mix_f32 v208, v39, 1.0, v208 op_sel:[1,0,0] op_sel_hi:[1,0,0]
	v_fma_mix_f32 v209, v39, v39, v209 op_sel:[1,1,0] op_sel_hi:[1,1,0]
	ds_read_b128 v[128:131], v236
	ds_read_b128 v[104:107], v236 offset:1152
	s_waitcnt vmcnt(11)
	v_cvt_f32_f16_e32 v72, v212
	v_cvt_f32_f16_sdwa v73, v212 dst_sel:DWORD dst_unused:UNUSED_PAD src0_sel:WORD_1
	v_cvt_f32_f16_e32 v74, v213
	v_cvt_f32_f16_sdwa v75, v213 dst_sel:DWORD dst_unused:UNUSED_PAD src0_sel:WORD_1
	v_cvt_f32_f16_e32 v80, v214
	v_cvt_f32_f16_sdwa v81, v214 dst_sel:DWORD dst_unused:UNUSED_PAD src0_sel:WORD_1
	v_cvt_f32_f16_e32 v82, v215
	v_cvt_f32_f16_sdwa v83, v215 dst_sel:DWORD dst_unused:UNUSED_PAD src0_sel:WORD_1
	v_sub_f32_e32 v72, v72, v202
	v_sub_f32_e32 v73, v73, v202
	v_sub_f32_e32 v74, v74, v202
	v_sub_f32_e32 v75, v75, v202
	v_sub_f32_e32 v80, v80, v202
	v_sub_f32_e32 v81, v81, v202
	v_sub_f32_e32 v82, v82, v202
	v_sub_f32_e32 v83, v83, v202
	v_pk_mul_f32 v[72:73], v[202:203], v[72:73] op_sel:[1,0]
	v_pk_mul_f32 v[74:75], v[202:203], v[74:75] op_sel:[1,0]
	v_pk_mul_f32 v[80:81], v[202:203], v[80:81] op_sel:[1,0]
	v_pk_mul_f32 v[82:83], v[202:203], v[82:83] op_sel:[1,0]
	v_pk_fma_f32 v[28:29], v[72:73], v[160:161], v[28:29]
	v_pk_fma_f32 v[30:31], v[74:75], v[162:163], v[30:31]
	v_pk_fma_f32 v[24:25], v[80:81], v[164:165], v[24:25]
	v_pk_fma_f32 v[26:27], v[82:83], v[166:167], v[26:27]
	v_cvt_pk_f16_f32 v28, v28, v29
	v_cvt_pk_f16_f32 v29, v30, v31
	v_cvt_pk_f16_f32 v30, v24, v25
	v_cvt_pk_f16_f32 v31, v26, v27
	s_waitcnt lgkmcnt(0)
	v_add_u32_e32 v83, 0x36000, v224
	buffer_store_dwordx4 v[128:131], v83, s[24:27], 0 offen nt
	v_add_u32_e32 v82, 0x39000, v224
	buffer_store_dwordx4 v[104:107], v82, s[24:27], 0 offen nt
	ds_write_b128 v235, v[28:31]
	v_fma_mix_f32 v210, v28, 1.0, 0 op_sel_hi:[1,0,0]
	v_fma_mix_f32 v211, v28, v28, 0 op_sel_hi:[1,1,0]
	v_fma_mix_f32 v210, v28, 1.0, v210 op_sel:[1,0,0] op_sel_hi:[1,0,0]
	v_fma_mix_f32 v211, v28, v28, v211 op_sel:[1,1,0] op_sel_hi:[1,1,0]
	v_fma_mix_f32 v210, v29, 1.0, v210 op_sel_hi:[1,0,0]
	v_fma_mix_f32 v211, v29, v29, v211 op_sel_hi:[1,1,0]
	v_fma_mix_f32 v210, v29, 1.0, v210 op_sel:[1,0,0] op_sel_hi:[1,0,0]
	v_fma_mix_f32 v211, v29, v29, v211 op_sel:[1,1,0] op_sel_hi:[1,1,0]
	v_fma_mix_f32 v210, v30, 1.0, v210 op_sel_hi:[1,0,0]
	v_fma_mix_f32 v211, v30, v30, v211 op_sel_hi:[1,1,0]
	v_fma_mix_f32 v210, v30, 1.0, v210 op_sel:[1,0,0] op_sel_hi:[1,0,0]
	v_fma_mix_f32 v211, v30, v30, v211 op_sel:[1,1,0] op_sel_hi:[1,1,0]
	v_fma_mix_f32 v210, v31, 1.0, v210 op_sel_hi:[1,0,0]
	v_fma_mix_f32 v211, v31, v31, v211 op_sel_hi:[1,1,0]
	v_fma_mix_f32 v210, v31, 1.0, v210 op_sel:[1,0,0] op_sel_hi:[1,0,0]
	v_fma_mix_f32 v211, v31, v31, v211 op_sel:[1,1,0] op_sel_hi:[1,1,0]
	s_waitcnt vmcnt(12)
	v_cvt_f32_f16_e32 v72, v144
	v_cvt_f32_f16_sdwa v73, v144 dst_sel:DWORD dst_unused:UNUSED_PAD src0_sel:WORD_1
	v_cvt_f32_f16_e32 v74, v145
	v_cvt_f32_f16_sdwa v75, v145 dst_sel:DWORD dst_unused:UNUSED_PAD src0_sel:WORD_1
	v_cvt_f32_f16_e32 v80, v146
	v_cvt_f32_f16_sdwa v81, v146 dst_sel:DWORD dst_unused:UNUSED_PAD src0_sel:WORD_1
	v_cvt_f32_f16_e32 v82, v147
	v_cvt_f32_f16_sdwa v83, v147 dst_sel:DWORD dst_unused:UNUSED_PAD src0_sel:WORD_1
	v_sub_f32_e32 v72, v72, v202
	v_sub_f32_e32 v73, v73, v202
	v_sub_f32_e32 v74, v74, v202
	v_sub_f32_e32 v75, v75, v202
	v_sub_f32_e32 v80, v80, v202
	v_sub_f32_e32 v81, v81, v202
	v_sub_f32_e32 v82, v82, v202
	v_sub_f32_e32 v83, v83, v202
	v_pk_mul_f32 v[72:73], v[202:203], v[72:73] op_sel:[1,0]
	v_pk_mul_f32 v[74:75], v[202:203], v[74:75] op_sel:[1,0]
	v_pk_mul_f32 v[80:81], v[202:203], v[80:81] op_sel:[1,0]
	v_pk_mul_f32 v[82:83], v[202:203], v[82:83] op_sel:[1,0]
	v_pk_fma_f32 v[20:21], v[72:73], v[168:169], v[20:21]
	v_pk_fma_f32 v[22:23], v[74:75], v[170:171], v[22:23]
	v_pk_fma_f32 v[16:17], v[80:81], v[172:173], v[16:17]
	v_pk_fma_f32 v[18:19], v[82:83], v[174:175], v[18:19]
	v_cvt_pk_f16_f32 v20, v20, v21
	v_cvt_pk_f16_f32 v21, v22, v23
	v_cvt_pk_f16_f32 v22, v16, v17
	v_cvt_pk_f16_f32 v23, v18, v19
	ds_write_b128 v235, v[20:23] offset:64
	v_fma_mix_f32 v210, v20, 1.0, v210 op_sel_hi:[1,0,0]
	v_fma_mix_f32 v211, v20, v20, v211 op_sel_hi:[1,1,0]
	v_fma_mix_f32 v210, v20, 1.0, v210 op_sel:[1,0,0] op_sel_hi:[1,0,0]
	v_fma_mix_f32 v211, v20, v20, v211 op_sel:[1,1,0] op_sel_hi:[1,1,0]
	v_fma_mix_f32 v210, v21, 1.0, v210 op_sel_hi:[1,0,0]
	v_fma_mix_f32 v211, v21, v21, v211 op_sel_hi:[1,1,0]
	v_fma_mix_f32 v210, v21, 1.0, v210 op_sel:[1,0,0] op_sel_hi:[1,0,0]
	v_fma_mix_f32 v211, v21, v21, v211 op_sel:[1,1,0] op_sel_hi:[1,1,0]
	v_fma_mix_f32 v210, v22, 1.0, v210 op_sel_hi:[1,0,0]
	v_fma_mix_f32 v211, v22, v22, v211 op_sel_hi:[1,1,0]
	v_fma_mix_f32 v210, v22, 1.0, v210 op_sel:[1,0,0] op_sel_hi:[1,0,0]
	v_fma_mix_f32 v211, v22, v22, v211 op_sel:[1,1,0] op_sel_hi:[1,1,0]
	v_fma_mix_f32 v210, v23, 1.0, v210 op_sel_hi:[1,0,0]
	v_fma_mix_f32 v211, v23, v23, v211 op_sel_hi:[1,1,0]
	v_fma_mix_f32 v210, v23, 1.0, v210 op_sel:[1,0,0] op_sel_hi:[1,0,0]
	v_fma_mix_f32 v211, v23, v23, v211 op_sel:[1,1,0] op_sel_hi:[1,1,0]
	ds_read_b128 v[240:243], v236
	ds_read_b128 v[96:99], v236 offset:1152
	s_waitcnt vmcnt(11)
	v_cvt_f32_f16_e32 v72, v132
	v_cvt_f32_f16_sdwa v73, v132 dst_sel:DWORD dst_unused:UNUSED_PAD src0_sel:WORD_1
	v_cvt_f32_f16_e32 v74, v133
	v_cvt_f32_f16_sdwa v75, v133 dst_sel:DWORD dst_unused:UNUSED_PAD src0_sel:WORD_1
	v_cvt_f32_f16_e32 v80, v134
	v_cvt_f32_f16_sdwa v81, v134 dst_sel:DWORD dst_unused:UNUSED_PAD src0_sel:WORD_1
	v_cvt_f32_f16_e32 v82, v135
	v_cvt_f32_f16_sdwa v83, v135 dst_sel:DWORD dst_unused:UNUSED_PAD src0_sel:WORD_1
	v_sub_f32_e32 v72, v72, v204
	v_sub_f32_e32 v73, v73, v204
	v_sub_f32_e32 v74, v74, v204
	v_sub_f32_e32 v75, v75, v204
	v_sub_f32_e32 v80, v80, v204
	v_sub_f32_e32 v81, v81, v204
	v_sub_f32_e32 v82, v82, v204
	v_sub_f32_e32 v83, v83, v204
	v_pk_mul_f32 v[72:73], v[204:205], v[72:73] op_sel:[1,0]
	v_pk_mul_f32 v[74:75], v[204:205], v[74:75] op_sel:[1,0]
	v_pk_mul_f32 v[80:81], v[204:205], v[80:81] op_sel:[1,0]
	v_pk_mul_f32 v[82:83], v[204:205], v[82:83] op_sel:[1,0]
	v_pk_fma_f32 v[12:13], v[72:73], v[160:161], v[12:13]
	v_pk_fma_f32 v[14:15], v[74:75], v[162:163], v[14:15]
	v_pk_fma_f32 v[8:9], v[80:81], v[164:165], v[8:9]
	v_pk_fma_f32 v[10:11], v[82:83], v[166:167], v[10:11]
	v_cvt_pk_f16_f32 v12, v12, v13
	v_cvt_pk_f16_f32 v13, v14, v15
	v_cvt_pk_f16_f32 v14, v8, v9
	v_cvt_pk_f16_f32 v15, v10, v11
	s_waitcnt lgkmcnt(0)
	v_add_u32_e32 v83, 0x3c000, v224
	buffer_store_dwordx4 v[240:243], v83, s[24:27], 0 offen nt
	v_add_u32_e32 v82, 0x3f000, v224
	buffer_store_dwordx4 v[96:99], v82, s[24:27], 0 offen nt
	ds_write_b128 v235, v[12:15]
	v_fma_mix_f32 v244, v12, 1.0, 0 op_sel_hi:[1,0,0]
	v_fma_mix_f32 v245, v12, v12, 0 op_sel_hi:[1,1,0]
	v_fma_mix_f32 v244, v12, 1.0, v244 op_sel:[1,0,0] op_sel_hi:[1,0,0]
	v_fma_mix_f32 v245, v12, v12, v245 op_sel:[1,1,0] op_sel_hi:[1,1,0]
	v_fma_mix_f32 v244, v13, 1.0, v244 op_sel_hi:[1,0,0]
	v_fma_mix_f32 v245, v13, v13, v245 op_sel_hi:[1,1,0]
	v_fma_mix_f32 v244, v13, 1.0, v244 op_sel:[1,0,0] op_sel_hi:[1,0,0]
	v_fma_mix_f32 v245, v13, v13, v245 op_sel:[1,1,0] op_sel_hi:[1,1,0]
	v_fma_mix_f32 v244, v14, 1.0, v244 op_sel_hi:[1,0,0]
	v_fma_mix_f32 v245, v14, v14, v245 op_sel_hi:[1,1,0]
	v_fma_mix_f32 v244, v14, 1.0, v244 op_sel:[1,0,0] op_sel_hi:[1,0,0]
	v_fma_mix_f32 v245, v14, v14, v245 op_sel:[1,1,0] op_sel_hi:[1,1,0]
	v_fma_mix_f32 v244, v15, 1.0, v244 op_sel_hi:[1,0,0]
	v_fma_mix_f32 v245, v15, v15, v245 op_sel_hi:[1,1,0]
	v_fma_mix_f32 v244, v15, 1.0, v244 op_sel:[1,0,0] op_sel_hi:[1,0,0]
	v_fma_mix_f32 v245, v15, v15, v245 op_sel:[1,1,0] op_sel_hi:[1,1,0]
	s_waitcnt vmcnt(12)
	v_cvt_f32_f16_e32 v72, v88
	v_cvt_f32_f16_sdwa v73, v88 dst_sel:DWORD dst_unused:UNUSED_PAD src0_sel:WORD_1
	v_cvt_f32_f16_e32 v74, v89
	v_cvt_f32_f16_sdwa v75, v89 dst_sel:DWORD dst_unused:UNUSED_PAD src0_sel:WORD_1
	v_cvt_f32_f16_e32 v80, v90
	v_cvt_f32_f16_sdwa v81, v90 dst_sel:DWORD dst_unused:UNUSED_PAD src0_sel:WORD_1
	v_cvt_f32_f16_e32 v82, v91
	v_cvt_f32_f16_sdwa v83, v91 dst_sel:DWORD dst_unused:UNUSED_PAD src0_sel:WORD_1
	v_sub_f32_e32 v72, v72, v204
	v_sub_f32_e32 v73, v73, v204
	v_sub_f32_e32 v74, v74, v204
	v_sub_f32_e32 v75, v75, v204
	v_sub_f32_e32 v80, v80, v204
	v_sub_f32_e32 v81, v81, v204
	v_sub_f32_e32 v82, v82, v204
	v_sub_f32_e32 v83, v83, v204
	v_pk_mul_f32 v[72:73], v[204:205], v[72:73] op_sel:[1,0]
	v_pk_mul_f32 v[74:75], v[204:205], v[74:75] op_sel:[1,0]
	v_pk_mul_f32 v[80:81], v[204:205], v[80:81] op_sel:[1,0]
	v_pk_mul_f32 v[82:83], v[204:205], v[82:83] op_sel:[1,0]
	v_pk_fma_f32 v[4:5], v[72:73], v[168:169], v[4:5]
	v_pk_fma_f32 v[6:7], v[74:75], v[170:171], v[6:7]
	v_pk_fma_f32 v[0:1], v[80:81], v[172:173], v[0:1]
	v_pk_fma_f32 v[2:3], v[82:83], v[174:175], v[2:3]
	v_cvt_pk_f16_f32 v4, v4, v5
	v_cvt_pk_f16_f32 v5, v6, v7
	v_cvt_pk_f16_f32 v6, v0, v1
	v_cvt_pk_f16_f32 v7, v2, v3
	ds_write_b128 v235, v[4:7] offset:64
	v_fma_mix_f32 v244, v4, 1.0, v244 op_sel_hi:[1,0,0]
	v_fma_mix_f32 v245, v4, v4, v245 op_sel_hi:[1,1,0]
	v_fma_mix_f32 v244, v4, 1.0, v244 op_sel:[1,0,0] op_sel_hi:[1,0,0]
	v_fma_mix_f32 v245, v4, v4, v245 op_sel:[1,1,0] op_sel_hi:[1,1,0]
	v_fma_mix_f32 v244, v5, 1.0, v244 op_sel_hi:[1,0,0]
	v_fma_mix_f32 v245, v5, v5, v245 op_sel_hi:[1,1,0]
	v_fma_mix_f32 v244, v5, 1.0, v244 op_sel:[1,0,0] op_sel_hi:[1,0,0]
	v_fma_mix_f32 v245, v5, v5, v245 op_sel:[1,1,0] op_sel_hi:[1,1,0]
	v_fma_mix_f32 v244, v6, 1.0, v244 op_sel_hi:[1,0,0]
	v_fma_mix_f32 v245, v6, v6, v245 op_sel_hi:[1,1,0]
	v_fma_mix_f32 v244, v6, 1.0, v244 op_sel:[1,0,0] op_sel_hi:[1,0,0]
	v_fma_mix_f32 v245, v6, v6, v245 op_sel:[1,1,0] op_sel_hi:[1,1,0]
	v_fma_mix_f32 v244, v7, 1.0, v244 op_sel_hi:[1,0,0]
	v_fma_mix_f32 v245, v7, v7, v245 op_sel_hi:[1,1,0]
	v_fma_mix_f32 v244, v7, 1.0, v244 op_sel:[1,0,0] op_sel_hi:[1,0,0]
	v_fma_mix_f32 v245, v7, v7, v245 op_sel:[1,1,0] op_sel_hi:[1,1,0]
	ds_read_b128 v[108:111], v236
	ds_read_b128 v[100:103], v236 offset:1152
	s_waitcnt lgkmcnt(0)
	v_add_u32_e32 v83, 0x42000, v224
	buffer_store_dwordx4 v[108:111], v83, s[24:27], 0 offen nt
	v_add_u32_e32 v82, 0x45000, v224
	buffer_store_dwordx4 v[100:103], v82, s[24:27], 0 offen nt
	v_xor_b32_e32 v225, 16, v234
	v_lshlrev_b32_e32 v225, 2, v225
	v_xor_b32_e32 v246, 32, v234
	v_lshlrev_b32_e32 v246, 2, v246
	ds_bpermute_b32 v92, v225, v206
	ds_bpermute_b32 v93, v225, v207
	ds_bpermute_b32 v94, v225, v140
	ds_bpermute_b32 v95, v225, v141
	ds_bpermute_b32 v120, v225, v142
	ds_bpermute_b32 v121, v225, v143
	ds_bpermute_b32 v122, v225, v216
	ds_bpermute_b32 v123, v225, v217
	s_waitcnt lgkmcnt(0)
	v_pk_add_f32 v[206:207], v[206:207], v[92:93]
	v_pk_add_f32 v[140:141], v[140:141], v[94:95]
	v_pk_add_f32 v[142:143], v[142:143], v[120:121]
	v_pk_add_f32 v[216:217], v[216:217], v[122:123]
	ds_bpermute_b32 v92, v225, v218
	ds_bpermute_b32 v93, v225, v219
	ds_bpermute_b32 v94, v225, v208
	ds_bpermute_b32 v95, v225, v209
	ds_bpermute_b32 v120, v225, v210
	ds_bpermute_b32 v121, v225, v211
	ds_bpermute_b32 v122, v225, v244
	ds_bpermute_b32 v123, v225, v245
	s_waitcnt lgkmcnt(0)
	v_pk_add_f32 v[218:219], v[218:219], v[92:93]
	v_pk_add_f32 v[208:209], v[208:209], v[94:95]
	v_pk_add_f32 v[210:211], v[210:211], v[120:121]
	v_pk_add_f32 v[244:245], v[244:245], v[122:123]
	ds_bpermute_b32 v92, v246, v206
	ds_bpermute_b32 v93, v246, v207
	ds_bpermute_b32 v94, v246, v140
	ds_bpermute_b32 v95, v246, v141
	ds_bpermute_b32 v120, v246, v142
	ds_bpermute_b32 v121, v246, v143
	ds_bpermute_b32 v122, v246, v216
	ds_bpermute_b32 v123, v246, v217
	s_waitcnt lgkmcnt(0)
	v_pk_add_f32 v[206:207], v[206:207], v[92:93]
	v_pk_add_f32 v[140:141], v[140:141], v[94:95]
	v_pk_add_f32 v[142:143], v[142:143], v[120:121]
	v_pk_add_f32 v[216:217], v[216:217], v[122:123]
	ds_bpermute_b32 v92, v246, v218
	ds_bpermute_b32 v93, v246, v219
	ds_bpermute_b32 v94, v246, v208
	ds_bpermute_b32 v95, v246, v209
	ds_bpermute_b32 v120, v246, v210
	ds_bpermute_b32 v121, v246, v211
	ds_bpermute_b32 v122, v246, v244
	ds_bpermute_b32 v123, v246, v245
	s_waitcnt lgkmcnt(0)
	v_pk_add_f32 v[218:219], v[218:219], v[92:93]
	v_pk_add_f32 v[208:209], v[208:209], v[94:95]
	v_pk_add_f32 v[210:211], v[210:211], v[120:121]
	v_pk_add_f32 v[244:245], v[244:245], v[122:123]
	s_mov_b64 exec, 0xffff
	global_store_dwordx2 v190, v[206:207], s[100:101] offset:0
	global_store_dwordx2 v190, v[140:141], s[100:101] offset:128
	global_store_dwordx2 v190, v[142:143], s[100:101] offset:256
	global_store_dwordx2 v190, v[216:217], s[100:101] offset:384
	global_store_dwordx2 v190, v[218:219], s[100:101] offset:1024
	global_store_dwordx2 v190, v[208:209], s[100:101] offset:1152
	global_store_dwordx2 v190, v[210:211], s[100:101] offset:1280
	global_store_dwordx2 v190, v[244:245], s[100:101] offset:1408
	s_mov_b64 exec, -1
	s_mov_b32 s83, s81
	s_mov_b32 s84, s82
	s_mov_b64 s[40:41], s[0:1]
	s_mov_b64 s[38:39], s[8:9]
	s_mov_b64 vcc, s[6:7]
	s_cbranch_vccz .LBB10_12
	s_waitcnt vmcnt(0)
	s_cmpk_gt_u32 s44, 0xff
	s_cbranch_scc1 .LBB10_31
	s_barrier

amdhsa.kernels:
  - .agpr_count:     16
    .args:
      - .actual_access:  read_only
        .address_space:  global
        .offset:         0
        .size:           8
        .value_kind:     global_buffer
      - .actual_access:  read_only
        .address_space:  global
        .offset:         8
        .size:           8
        .value_kind:     global_buffer
      - .actual_access:  write_only
        .address_space:  global
        .offset:         16
        .size:           8
        .value_kind:     global_buffer
    .group_segment_fixed_size: 45056
    .kernarg_segment_align: 8
    .kernarg_segment_size: 24
    .language:       OpenCL C
    .language_version:
      - 2
      - 0
    .max_flat_workgroup_size: 256
    .name:           _Z6k_attnPKDF16_PKfPDF16_
    .private_segment_fixed_size: 0
    .sgpr_count:     16
    .sgpr_spill_count: 0
    .symbol:         _Z6k_attnPKDF16_PKfPDF16_.kd
    .uniform_work_group_size: 1
    .uses_dynamic_stack: false
    .vgpr_count:     84
    .vgpr_spill_count: 0
    .wavefront_size: 64
  - .agpr_count:     0
    .args:
      - .actual_access:  read_only
        .address_space:  global
        .offset:         0
        .size:           8
        .value_kind:     global_buffer
      - .actual_access:  read_only
        .address_space:  global
        .offset:         8
        .size:           8
        .value_kind:     global_buffer
      - .actual_access:  write_only
        .address_space:  global
        .offset:         16
        .size:           8
        .value_kind:     global_buffer
      - .actual_access:  write_only
        .address_space:  global
        .offset:         24
        .size:           8
        .value_kind:     global_buffer
      - .actual_access:  write_only
        .address_space:  global
        .offset:         32
        .size:           8
        .value_kind:     global_buffer
      - .actual_access:  write_only
        .address_space:  global
        .offset:         40
        .size:           8
        .value_kind:     global_buffer
    .group_segment_fixed_size: 0
    .kernarg_segment_align: 8
    .kernarg_segment_size: 48
    .language:       OpenCL C
    .language_version:
      - 2
      - 0
    .max_flat_workgroup_size: 256
    .name:           _Z11k_prep_miscPKiPKfPfPDv2_fS3_S3_
    .private_segment_fixed_size: 0
    .sgpr_count:     16
    .sgpr_spill_count: 0
    .symbol:         _Z11k_prep_miscPKiPKfPfPDv2_fS3_S3_.kd
    .uniform_work_group_size: 1
    .uses_dynamic_stack: false
    .vgpr_count:     6
    .vgpr_spill_count: 0
    .wavefront_size: 64
  - .agpr_count:     0
    .args:
      - .actual_access:  read_only
        .address_space:  global
        .offset:         0
        .size:           8
        .value_kind:     global_buffer
      - .actual_access:  write_only
        .address_space:  global
        .offset:         8
        .size:           8
        .value_kind:     global_buffer
    .group_segment_fixed_size: 0
    .kernarg_segment_align: 8
    .kernarg_segment_size: 16
    .language:       OpenCL C
    .language_version:
      - 2
      - 0
    .max_flat_workgroup_size: 256
    .name:           _Z7k_cvt_xPKfPDF16_
    .private_segment_fixed_size: 0
    .sgpr_count:     14
    .sgpr_spill_count: 0
    .symbol:         _Z7k_cvt_xPKfPDF16_.kd
    .uniform_work_group_size: 1
    .uses_dynamic_stack: false
    .vgpr_count:     12
    .vgpr_spill_count: 0
    .wavefront_size: 64
  - .agpr_count:     0
    .args:
      - .offset:         0
        .size:           176
        .value_kind:     by_value
    .group_segment_fixed_size: 9216
    .kernarg_segment_align: 8
    .kernarg_segment_size: 176
    .language:       OpenCL C
    .language_version:
      - 2
      - 0
    .max_flat_workgroup_size: 256
    .name:           _Z8k_wtrans8PrepArgs
    .private_segment_fixed_size: 0
    .sgpr_count:     44
    .sgpr_spill_count: 0
    .symbol:         _Z8k_wtrans8PrepArgs.kd
    .uniform_work_group_size: 1
    .uses_dynamic_stack: false
    .vgpr_count:     18
    .vgpr_spill_count: 0
    .wavefront_size: 64
  - .agpr_count:     0
    .args:
      - .offset:         0
        .size:           176
        .value_kind:     by_value
      - .actual_access:  read_only
        .address_space:  global
        .offset:         176
        .size:           8
        .value_kind:     global_buffer
      - .actual_access:  read_only
        .address_space:  global
        .offset:         184
        .size:           8
        .value_kind:     global_buffer
    .group_segment_fixed_size: 2048
    .kernarg_segment_align: 8
    .kernarg_segment_size: 192
    .language:       OpenCL C
    .language_version:
      - 2
      - 0
    .max_flat_workgroup_size: 256
    .name:           _Z8k_colvec8PrepArgsPKfS1_
    .private_segment_fixed_size: 0
    .sgpr_count:     38
    .sgpr_spill_count: 0
    .symbol:         _Z8k_colvec8PrepArgsPKfS1_.kd
    .uniform_work_group_size: 1
    .uses_dynamic_stack: false
    .vgpr_count:     114
    .vgpr_spill_count: 0
    .wavefront_size: 64
  - .agpr_count:     0
    .args:
      - .actual_access:  read_only
        .address_space:  global
        .offset:         0
        .size:           8
        .value_kind:     global_buffer
      - .actual_access:  write_only
        .address_space:  global
        .offset:         8
        .size:           8
        .value_kind:     global_buffer
    .group_segment_fixed_size: 0
    .kernarg_segment_align: 8
    .kernarg_segment_size: 16
    .language:       OpenCL C
    .language_version:
      - 2
      - 0
    .max_flat_workgroup_size: 256
    .name:           _Z9k_rowstatPKDv2_fPS_
    .private_segment_fixed_size: 0
    .sgpr_count:     16
    .sgpr_spill_count: 0
    .symbol:         _Z9k_rowstatPKDv2_fPS_.kd
    .uniform_work_group_size: 1
    .uses_dynamic_stack: false
    .vgpr_count:     28
    .vgpr_spill_count: 0
    .wavefront_size: 64
  - .agpr_count:     0
    .args:
      - .actual_access:  read_only
        .address_space:  global
        .offset:         0
        .size:           8
        .value_kind:     global_buffer
      - .actual_access:  read_only
        .address_space:  global
        .offset:         8
        .size:           8
        .value_kind:     global_buffer
      - .actual_access:  read_only
        .address_space:  global
        .offset:         16
        .size:           8
        .value_kind:     global_buffer
      - .actual_access:  read_only
        .address_space:  global
        .offset:         24
        .size:           8
        .value_kind:     global_buffer
      - .actual_access:  write_only
        .address_space:  global
        .offset:         32
        .size:           8
        .value_kind:     global_buffer
    .group_segment_fixed_size: 0
    .kernarg_segment_align: 8
    .kernarg_segment_size: 40
    .language:       OpenCL C
    .language_version:
      - 2
      - 0
    .max_flat_workgroup_size: 256
    .name:           _Z10k_final_lnPKDF16_PKDv2_fPKfS5_Pf
    .private_segment_fixed_size: 0
    .sgpr_count:     19
    .sgpr_spill_count: 0
    .symbol:         _Z10k_final_lnPKDF16_PKDv2_fPKfS5_Pf.kd
    .uniform_work_group_size: 1
    .uses_dynamic_stack: false
    .vgpr_count:     19
    .vgpr_spill_count: 0
    .wavefront_size: 64
  - .agpr_count:     0
    .args:
      - .offset:         0
        .size:           32
        .value_kind:     by_value
      - .offset:         32
        .size:           32
        .value_kind:     by_value
      - .offset:         64
        .size:           4
        .value_kind:     hidden_block_count_x
      - .offset:         68
        .size:           4
        .value_kind:     hidden_block_count_y
      - .offset:         72
        .size:           4
        .value_kind:     hidden_block_count_z
      - .offset:         76
        .size:           2
        .value_kind:     hidden_group_size_x
      - .offset:         78
        .size:           2
        .value_kind:     hidden_group_size_y
      - .offset:         80
        .size:           2
        .value_kind:     hidden_group_size_z
      - .offset:         82
        .size:           2
        .value_kind:     hidden_remainder_x
      - .offset:         84
        .size:           2
        .value_kind:     hidden_remainder_y
      - .offset:         86
        .size:           2
        .value_kind:     hidden_remainder_z
      - .offset:         104
        .size:           8
        .value_kind:     hidden_global_offset_x
      - .offset:         112
        .size:           8
        .value_kind:     hidden_global_offset_y
      - .offset:         120
        .size:           8
        .value_kind:     hidden_global_offset_z
      - .offset:         128
        .size:           2
        .value_kind:     hidden_grid_dims
      - .offset:         184
        .size:           4
        .value_kind:     hidden_dynamic_lds_size
    .group_segment_fixed_size: 0
    .kernarg_segment_align: 8
    .kernarg_segment_size: 320
    .language:       OpenCL C
    .language_version:
      - 2
      - 0
    .max_flat_workgroup_size: 512
    .name:           _Z6k_gemmIN2pg6EpiLinILi0EEELi768EEvNS0_4GemmET_
    .private_segment_fixed_size: 0
    .sgpr_count:     83
    .sgpr_spill_count: 0
    .symbol:         _Z6k_gemmIN2pg6EpiLinILi0EEELi768EEvNS0_4GemmET_.kd
    .uniform_work_group_size: 1
    .uses_dynamic_stack: false
    .vgpr_count:     254
    .vgpr_spill_count: 0
    .wavefront_size: 64
  - .agpr_count:     0
    .args:
      - .offset:         0
        .size:           32
        .value_kind:     by_value
      - .offset:         32
        .size:           56
        .value_kind:     by_value
      - .offset:         88
        .size:           4
        .value_kind:     hidden_block_count_x
      - .offset:         92
        .size:           4
        .value_kind:     hidden_block_count_y
      - .offset:         96
        .size:           4
        .value_kind:     hidden_block_count_z
      - .offset:         100
        .size:           2
        .value_kind:     hidden_group_size_x
      - .offset:         102
        .size:           2
        .value_kind:     hidden_group_size_y
      - .offset:         104
        .size:           2
        .value_kind:     hidden_group_size_z
      - .offset:         106
        .size:           2
        .value_kind:     hidden_remainder_x
      - .offset:         108
        .size:           2
        .value_kind:     hidden_remainder_y
      - .offset:         110
        .size:           2
        .value_kind:     hidden_remainder_z
      - .offset:         128
        .size:           8
        .value_kind:     hidden_global_offset_x
      - .offset:         136
        .size:           8
        .value_kind:     hidden_global_offset_y
      - .offset:         144
        .size:           8
        .value_kind:     hidden_global_offset_z
      - .offset:         152
        .size:           2
        .value_kind:     hidden_grid_dims
      - .offset:         208
        .size:           4
        .value_kind:     hidden_dynamic_lds_size
    .group_segment_fixed_size: 0
    .kernarg_segment_align: 8
    .kernarg_segment_size: 344
    .language:       OpenCL C
    .language_version:
      - 2
      - 0
    .max_flat_workgroup_size: 512
    .name:           _Z6k_gemmIN2pg6EpiResELi768EEvNS0_4GemmET_
    .private_segment_fixed_size: 0
    .sgpr_count:     108
    .sgpr_spill_count: 0
    .symbol:         _Z6k_gemmIN2pg6EpiResELi768EEvNS0_4GemmET_.kd
    .uniform_work_group_size: 1
    .uses_dynamic_stack: false
    .vgpr_count:     256
    .vgpr_spill_count: 0
    .wavefront_size: 64
  - .agpr_count:     0
    .args:
      - .offset:         0
        .size:           32
        .value_kind:     by_value
      - .offset:         32
        .size:           32
        .value_kind:     by_value
      - .offset:         64
        .size:           4
        .value_kind:     hidden_block_count_x
      - .offset:         68
        .size:           4
        .value_kind:     hidden_block_count_y
      - .offset:         72
        .size:           4
        .value_kind:     hidden_block_count_z
      - .offset:         76
        .size:           2
        .value_kind:     hidden_group_size_x
      - .offset:         78
        .size:           2
        .value_kind:     hidden_group_size_y
      - .offset:         80
        .size:           2
        .value_kind:     hidden_group_size_z
      - .offset:         82
        .size:           2
        .value_kind:     hidden_remainder_x
      - .offset:         84
        .size:           2
        .value_kind:     hidden_remainder_y
      - .offset:         86
        .size:           2
        .value_kind:     hidden_remainder_z
      - .offset:         104
        .size:           8
        .value_kind:     hidden_global_offset_x
      - .offset:         112
        .size:           8
        .value_kind:     hidden_global_offset_y
      - .offset:         120
        .size:           8
        .value_kind:     hidden_global_offset_z
      - .offset:         128
        .size:           2
        .value_kind:     hidden_grid_dims
      - .offset:         184
        .size:           4
        .value_kind:     hidden_dynamic_lds_size
    .group_segment_fixed_size: 0
    .kernarg_segment_align: 8
    .kernarg_segment_size: 320
    .language:       OpenCL C
    .language_version:
      - 2
      - 0
    .max_flat_workgroup_size: 512
    .name:           _Z6k_gemmIN2pg6EpiLinILi1EEELi768EEvNS0_4GemmET_
    .private_segment_fixed_size: 0
    .sgpr_count:     83
    .sgpr_spill_count: 0
    .symbol:         _Z6k_gemmIN2pg6EpiLinILi1EEELi768EEvNS0_4GemmET_.kd
    .uniform_work_group_size: 1
    .uses_dynamic_stack: false
    .vgpr_count:     254
    .vgpr_spill_count: 0
    .wavefront_size: 64
  - .agpr_count:     0
    .args:
      - .offset:         0
        .size:           32
        .value_kind:     by_value
      - .offset:         32
        .size:           56
        .value_kind:     by_value
      - .offset:         88
        .size:           4
        .value_kind:     hidden_block_count_x
      - .offset:         92
        .size:           4
        .value_kind:     hidden_block_count_y
      - .offset:         96
        .size:           4
        .value_kind:     hidden_block_count_z
      - .offset:         100
        .size:           2
        .value_kind:     hidden_group_size_x
      - .offset:         102
        .size:           2
        .value_kind:     hidden_group_size_y
      - .offset:         104
        .size:           2
        .value_kind:     hidden_group_size_z
      - .offset:         106
        .size:           2
        .value_kind:     hidden_remainder_x
      - .offset:         108
        .size:           2
        .value_kind:     hidden_remainder_y
      - .offset:         110
        .size:           2
        .value_kind:     hidden_remainder_z
      - .offset:         128
        .size:           8
        .value_kind:     hidden_global_offset_x
      - .offset:         136
        .size:           8
        .value_kind:     hidden_global_offset_y
      - .offset:         144
        .size:           8
        .value_kind:     hidden_global_offset_z
      - .offset:         152
        .size:           2
        .value_kind:     hidden_grid_dims
      - .offset:         208
        .size:           4
        .value_kind:     hidden_dynamic_lds_size
    .group_segment_fixed_size: 0
    .kernarg_segment_align: 8
    .kernarg_segment_size: 344
    .language:       OpenCL C
    .language_version:
      - 2
      - 0
    .max_flat_workgroup_size: 512
    .name:           _Z6k_gemmIN2pg6EpiResELi3072EEvNS0_4GemmET_
    .private_segment_fixed_size: 0
    .sgpr_count:     108
    .sgpr_spill_count: 0
    .symbol:         _Z6k_gemmIN2pg6EpiResELi3072EEvNS0_4GemmET_.kd
    .uniform_work_group_size: 1
    .uses_dynamic_stack: false
    .vgpr_count:     256
    .vgpr_spill_count: 0
    .wavefront_size: 64
